# diff-attn: row-max test skipped (fixed reference from tile 0, fp8 overflow shows as NaN row sum -> unit redone with the tested path); 16x16x128 row-sum MFMA
# speedup vs baseline: 1.1070x; 1.0612x over previous
.LBB0_1195:
	s_cmp_lt_i32 s30, 12
	s_cselect_b64 s[20:21], -1, 0
	s_and_b64 s[4:5], s[20:21], s[4:5]
	s_andn2_b64 vcc, exec, s[4:5]
	s_cbranch_vccnz .LBB0_1428
	s_mov_b64 s[10:11], s[0:1]
	s_mov_b32 s98, 0
	s_mov_b32 s99, 0
	v_mbcnt_hi_u32_b32 v178, -1, v208
	s_waitcnt lgkmcnt(0)
	s_load_dwordx8 s[12:19], s[10:11], 0x78
	v_ashrrev_i32_e32 v179, 31, v178
	s_waitcnt vmcnt(2)
	v_lshlrev_b64 v[2:3], 2, v[178:179]
	s_waitcnt vmcnt(1)
	v_mov_b32_e32 v7, 0
	v_mov_b32_e32 v10, 0
	s_waitcnt lgkmcnt(0)
	v_lshl_add_u64 v[4:5], s[12:13], 0, v[2:3]
	global_load_dword v1, v[4:5], off
	v_lshl_add_u64 v[4:5], s[14:15], 0, v[2:3]
	global_load_dword v6, v[4:5], off
	v_lshl_add_u64 v[4:5], s[16:17], 0, v[2:3]
	v_lshl_add_u64 v[2:3], s[18:19], 0, v[2:3]
	global_load_dword v4, v[4:5], off
	s_cmp_gt_i32 s22, 7
	global_load_dword v3, v[2:3], off
	s_cselect_b64 s[4:5], -1, 0
	s_lshr_b32 s6, s22, 3
	v_cvt_f32_u32_e32 v2, s6
	v_mov_b32_e32 v8, 0
	v_mov_b32_e32 v11, 0
	v_mov_b32_e32 v5, 0
	v_mov_b32_e32 v9, 0
	v_rcp_iflag_f32_e32 v2, v2
	s_and_b64 s[12:13], s[4:5], s[36:37]
	s_xor_b64 s[4:5], s[12:13], -1
	s_movk_i32 s35, 0x400
	s_mov_b32 s53, s88
	s_and_b64 vcc, exec, s[4:5]
	s_waitcnt vmcnt(2)
	v_mul_f32_e32 v12, v1, v6
	s_nop 1
	v_mov_b32_dpp v7, v12 quad_perm:[1,0,3,2] row_mask:0xf bank_mask:0xf
	v_fmac_f32_e32 v7, v1, v6
	s_waitcnt vmcnt(0)
	v_mul_f32_e32 v13, v4, v3
	s_nop 1
	v_mov_b32_dpp v10, v13 quad_perm:[1,0,3,2] row_mask:0xf bank_mask:0xf
	v_fmac_f32_e32 v10, v4, v3
	v_add_f32_dpp v1, v7, v7 quad_perm:[2,3,0,1] row_mask:0xf bank_mask:0xf bound_ctrl:1
	s_nop 0
	v_add_f32_dpp v3, v10, v10 quad_perm:[2,3,0,1] row_mask:0xf bank_mask:0xf bound_ctrl:1
	v_add_f32_dpp v1, v1, v1 row_half_mirror row_mask:0xf bank_mask:0xf bound_ctrl:1
	s_nop 0
	v_add_f32_dpp v3, v3, v3 row_half_mirror row_mask:0xf bank_mask:0xf bound_ctrl:1
	v_add_f32_dpp v1, v1, v1 row_mirror row_mask:0xf bank_mask:0xf bound_ctrl:1
	s_nop 0
	v_add_f32_dpp v3, v3, v3 row_mirror row_mask:0xf bank_mask:0xf bound_ctrl:1
	v_mov_b32_dpp v8, v1 row_bcast:15 row_mask:0xa bank_mask:0xf
	v_add_f32_e32 v1, v1, v8
	v_mov_b32_dpp v11, v3 row_bcast:15 row_mask:0xa bank_mask:0xf
	v_add_f32_e32 v3, v3, v11
	v_mov_b32_dpp v9, v1 row_bcast:31 row_mask:0xc bank_mask:0xf
	v_add_f32_e32 v1, v1, v9
	v_mov_b32_dpp v5, v3 row_bcast:31 row_mask:0xc bank_mask:0xf
	v_add_f32_e32 v3, v3, v5
	v_readlane_b32 s7, v1, 63
	v_readlane_b32 s3, v3, 63
	s_cbranch_vccnz .LBB0_1198
	v_mul_f32_e32 v1, 0x4f7ffffe, v2
	v_cvt_u32_f32_e32 v1, v1
	s_sub_i32 s14, 0, s6
	s_abs_i32 s9, s88
	s_ashr_i32 s8, s88, 31
	v_readfirstlane_b32 s15, v1
	s_mul_i32 s14, s14, s15
	s_mul_hi_u32 s14, s15, s14
	s_add_i32 s15, s15, s14
	s_mul_hi_u32 s14, s9, s15
	s_mul_i32 s14, s14, s6
	s_sub_i32 s9, s9, s14
	s_sub_i32 s14, s9, s6
	s_cmp_ge_u32 s9, s6
	s_cselect_b32 s9, s14, s9
	s_sub_i32 s14, s9, s6
	s_cmp_ge_u32 s9, s6
	s_cselect_b32 s9, s14, s9
	s_xor_b32 s9, s9, s8
	s_sub_i32 s53, s9, s8
	s_movk_i32 s35, 0x80

.LBB0_1202:
	s_nop 15
	v_add_f32_e32 v248, v18, v19
	v_add_f32_e32 v249, v20, v21
	v_add_f32_e32 v248, v248, v249
	v_cmp_u_f32_e64 s[100:101], v248, v248
	s_nop 1
	s_cmp_lg_u64 s[100:101], 0
	s_cselect_b32 s100, 1, 0
	s_or_b32 s99, s99, s100
	s_mov_b64 s[100:101], exec
	s_mov_b32 exec_lo, 0x30003
	s_mov_b32 exec_hi, 0x30003
	ds_write_b128 v250, v[18:21] offset:49152
	s_mov_b64 exec, s[100:101]
	v_add_u32_e32 v249, s78, v186
	v_mov_b32_e32 v248, s78
	v_mov_b32_e32 v251, s99
	ds_write_b32 v248, v251 offset:49404
	s_waitcnt lgkmcnt(0)
	ds_read_b128 v[30:33], v249 offset:49248
	ds_read_b128 v[26:29], v249 offset:49216
	ds_read_b128 v[22:25], v249 offset:49184
	ds_read_b128 v[18:21], v249 offset:49152
	s_waitcnt lgkmcnt(0)
	v_rcp_f32_e32 v18, v18
	v_rcp_f32_e32 v19, v19
	v_mov_b32_e32 v92, v179
	s_waitcnt vmcnt(0) lgkmcnt(0)
	s_barrier
	v_and_b32_e32 v248, 7, v193
	v_lshlrev_b32_e32 v248, 8, v248
	ds_read_b32 v251, v248 offset:49404
	s_waitcnt lgkmcnt(0)
	v_cmp_ne_u32_e64 s[100:101], 0, v251
	s_nop 1
	s_cmp_lg_u64 s[100:101], 0
	s_cselect_b32 s99, 1, 0
	v_mul_f32_e32 v2, v2, v18
	v_mul_f32_e32 v34, v34, v18
	v_mul_f32_e32 v50, v50, v18
	v_mul_f32_e32 v82, v66, v18
	v_mul_f32_e32 v18, v3, v19
	v_rcp_f32_e32 v3, v20
	v_mul_f32_e32 v35, v35, v19
	v_mul_f32_e32 v83, v51, v19
	v_mul_f32_e32 v19, v67, v19
	v_mul_f32_e32 v20, v4, v3
	v_rcp_f32_e32 v4, v21
	v_mul_f32_e32 v21, v36, v3
	v_mul_f32_e32 v52, v52, v3
	v_mul_f32_e32 v67, v68, v3
	v_rcp_f32_e32 v3, v22
	v_mul_f32_e32 v36, v5, v4
	v_mul_f32_e32 v22, v37, v4
	v_mul_f32_e32 v84, v53, v4
	v_mul_f32_e32 v85, v69, v4
	v_rcp_f32_e32 v4, v23
	v_mul_f32_e32 v37, v6, v3
	v_mul_f32_e32 v23, v38, v3
	v_mul_f32_e32 v38, v54, v3
	v_mul_f32_e32 v70, v70, v3
	v_rcp_f32_e32 v3, v24
	v_mul_f32_e32 v51, v7, v4
	v_mul_f32_e32 v39, v39, v4
	v_mul_f32_e32 v54, v55, v4
	v_mul_f32_e32 v55, v71, v4
	v_rcp_f32_e32 v4, v25
	v_mul_f32_e32 v8, v8, v3
	v_mul_f32_e32 v25, v40, v3
	v_mul_f32_e32 v40, v56, v3
	v_mul_f32_e32 v72, v72, v3
	v_rcp_f32_e32 v3, v26
	v_mul_f32_e32 v9, v9, v4
	v_mul_f32_e32 v26, v41, v4
	v_mul_f32_e32 v57, v57, v4
	v_mul_f32_e32 v86, v73, v4
	v_rcp_f32_e32 v4, v27
	v_mul_f32_e32 v10, v10, v3
	v_mul_f32_e32 v27, v42, v3
	v_mul_f32_e32 v87, v58, v3
	v_mul_f32_e32 v88, v74, v3
	v_rcp_f32_e32 v3, v28
	v_mul_f32_e32 v11, v11, v4
	v_mul_f32_e32 v43, v43, v4
	v_mul_f32_e32 v74, v59, v4
	v_mul_f32_e32 v75, v75, v4
	v_rcp_f32_e32 v4, v29
	v_mul_f32_e32 v12, v12, v3
	v_mul_f32_e32 v44, v44, v3
	v_mul_f32_e32 v60, v60, v3
	v_mul_f32_e32 v89, v76, v3
	v_rcp_f32_e32 v3, v30
	v_mul_f32_e32 v13, v13, v4
	v_mul_f32_e32 v30, v45, v4
	v_mul_f32_e32 v45, v61, v4
	v_mul_f32_e32 v77, v77, v4
	v_rcp_f32_e32 v4, v31
	v_mul_f32_e32 v14, v14, v3
	v_mul_f32_e32 v31, v46, v3
	v_mul_f32_e32 v62, v62, v3
	v_mul_f32_e32 v78, v78, v3
	v_rcp_f32_e32 v3, v32
	v_mul_f32_e32 v15, v15, v4
	v_mul_f32_e32 v32, v47, v4
	v_mul_f32_e32 v90, v63, v4
	v_mul_f32_e32 v79, v79, v4
	ds_read2st64_b32 v[4:5], v92 offset1:8
	v_mul_f32_e32 v29, v16, v3
	v_mul_f32_e32 v48, v48, v3
	v_mul_f32_e32 v91, v64, v3
	v_mul_f32_e32 v80, v80, v3
	v_rcp_f32_e32 v3, v33
	ds_read2st64_b32 v[6:7], v92 offset0:16 offset1:24
	v_mul_f32_e32 v17, v17, v3
	v_mul_f32_e32 v33, v49, v3
	v_mul_f32_e32 v65, v65, v3
	v_mul_f32_e32 v81, v81, v3
	s_waitcnt lgkmcnt(0)
	v_lshlrev_b32_e32 v3, 16, v4
	v_fma_f32 v3, -v1, v2, v3
	v_and_b32_e32 v2, 0xffff0000, v4
	v_fma_f32 v68, -v1, v18, v2
	v_lshlrev_b32_e32 v2, 16, v5
	v_fma_f32 v63, -v1, v20, v2
	v_and_b32_e32 v2, 0xffff0000, v5
	ds_read2st64_b32 v[4:5], v92 offset0:32 offset1:40
	v_fma_f32 v58, -v1, v36, v2
	v_lshlrev_b32_e32 v2, 16, v6
	v_fma_f32 v53, -v1, v37, v2
	v_and_b32_e32 v2, 0xffff0000, v6
	v_fma_f32 v47, -v1, v51, v2
	v_lshlrev_b32_e32 v2, 16, v7
	v_fma_f32 v42, -v1, v8, v2
	v_and_b32_e32 v2, 0xffff0000, v7
	v_fma_f32 v36, -v1, v9, v2
	s_waitcnt lgkmcnt(0)
	v_lshlrev_b32_e32 v2, 16, v4
	v_fma_f32 v28, -v1, v10, v2
	v_and_b32_e32 v2, 0xffff0000, v4
	v_fma_f32 v24, -v1, v11, v2
	ds_read2st64_b32 v[10:11], v92 offset0:48 offset1:56
	v_lshlrev_b32_e32 v2, 16, v5
	v_fma_f32 v20, -v1, v12, v2
	v_and_b32_e32 v2, 0xffff0000, v5
	ds_read2st64_b32 v[4:5], v92 offset0:64 offset1:72
	v_fma_f32 v16, -v1, v13, v2
	s_waitcnt lgkmcnt(0)
	v_lshlrev_b32_e32 v2, 16, v10
	v_fma_f32 v12, -v1, v14, v2
	v_and_b32_e32 v2, 0xffff0000, v10
	v_fma_f32 v9, -v1, v15, v2
	v_lshlrev_b32_e32 v2, 16, v11
	v_fma_f32 v7, -v1, v29, v2
	v_and_b32_e32 v2, 0xffff0000, v11
	v_fma_f32 v6, -v1, v17, v2
	v_lshlrev_b32_e32 v2, 16, v4
	v_fma_f32 v76, -v1, v34, v2
	v_and_b32_e32 v2, 0xffff0000, v4
	v_lshlrev_b32_e32 v4, 16, v5
	v_fma_f32 v66, -v1, v21, v4
	v_and_b32_e32 v4, 0xffff0000, v5
	v_fma_f32 v61, -v1, v22, v4
	ds_read2st64_b32 v[4:5], v92 offset0:80 offset1:88
	ds_read2st64_b32 v[14:15], v92 offset0:144 offset1:152
	v_fma_f32 v71, -v1, v35, v2
	v_mul_f32_e32 v2, v76, v76
	v_fmac_f32_e32 v2, v3, v3
	s_waitcnt lgkmcnt(0)
	v_lshlrev_b32_e32 v8, 16, v4
	v_and_b32_e32 v4, 0xffff0000, v4
	v_fma_f32 v51, -v1, v39, v4
	v_lshlrev_b32_e32 v4, 16, v5
	v_fma_f32 v46, -v1, v25, v4
	v_and_b32_e32 v4, 0xffff0000, v5
	v_fma_f32 v41, -v1, v26, v4
	ds_read2st64_b32 v[4:5], v92 offset0:96 offset1:104
	v_fma_f32 v56, -v1, v23, v8
	v_mul_f32_e32 v34, v71, v71
	v_fmac_f32_e32 v34, v68, v68
	v_mul_f32_e32 v93, v66, v66
	s_waitcnt lgkmcnt(0)
	v_lshlrev_b32_e32 v8, 16, v4
	v_and_b32_e32 v4, 0xffff0000, v4
	v_fma_f32 v29, -v1, v43, v4
	v_lshlrev_b32_e32 v4, 16, v5
	v_fma_f32 v25, -v1, v44, v4
	v_and_b32_e32 v4, 0xffff0000, v5
	v_fma_f32 v21, -v1, v30, v4
	ds_read2st64_b32 v[4:5], v92 offset0:112 offset1:120
	v_fma_f32 v37, -v1, v27, v8
	v_fmac_f32_e32 v93, v63, v63
	v_mul_f32_e32 v94, v61, v61
	v_fmac_f32_e32 v94, v58, v58
	s_waitcnt lgkmcnt(0)
	v_lshlrev_b32_e32 v8, 16, v4
	v_and_b32_e32 v4, 0xffff0000, v4
	v_fma_f32 v13, -v1, v32, v4
	v_lshlrev_b32_e32 v4, 16, v5
	v_fma_f32 v10, -v1, v48, v4
	v_and_b32_e32 v4, 0xffff0000, v5
	v_fma_f32 v17, -v1, v31, v8
	v_fma_f32 v8, -v1, v33, v4
	ds_read2st64_b32 v[4:5], v92 offset0:128 offset1:136
	ds_read2st64_b32 v[30:31], v92 offset0:208 offset1:216
	v_mul_f32_e32 v95, v56, v56
	v_fmac_f32_e32 v95, v53, v53
	v_mul_f32_e32 v96, v51, v51
	s_waitcnt lgkmcnt(0)
	v_lshlrev_b32_e32 v11, 16, v4
	v_and_b32_e32 v4, 0xffff0000, v4
	v_fma_f32 v83, -v1, v83, v4
	v_lshlrev_b32_e32 v4, 16, v5
	v_fma_f32 v73, -v1, v52, v4
	v_and_b32_e32 v4, 0xffff0000, v5
	v_fma_f32 v69, -v1, v84, v4
	v_lshlrev_b32_e32 v4, 16, v14
	v_fma_f32 v64, -v1, v38, v4
	v_and_b32_e32 v4, 0xffff0000, v14
	v_fma_f32 v59, -v1, v54, v4
	v_lshlrev_b32_e32 v4, 16, v15
	v_fma_f32 v54, -v1, v40, v4
	ds_read2st64_b32 v[4:5], v92 offset0:160 offset1:168
	v_fma_f32 v105, -v1, v50, v11
	v_and_b32_e32 v11, 0xffff0000, v15
	ds_read2st64_b32 v[14:15], v92 offset0:176 offset1:184
	v_fma_f32 v49, -v1, v57, v11
	s_waitcnt lgkmcnt(0)
	v_lshlrev_b32_e32 v11, 16, v4
	v_and_b32_e32 v4, 0xffff0000, v4
	v_fma_f32 v39, -v1, v74, v4
	v_lshlrev_b32_e32 v4, 16, v5
	v_fma_f32 v33, -v1, v60, v4
	v_and_b32_e32 v4, 0xffff0000, v5
	v_fma_f32 v26, -v1, v45, v4
	v_lshlrev_b32_e32 v4, 16, v14
	v_fma_f32 v22, -v1, v62, v4
	v_and_b32_e32 v4, 0xffff0000, v14
	v_fma_f32 v18, -v1, v90, v4
	v_lshlrev_b32_e32 v4, 16, v15
	v_fma_f32 v14, -v1, v91, v4
	ds_read2st64_b32 v[4:5], v92 offset0:192 offset1:200
	v_fma_f32 v44, -v1, v87, v11
	v_and_b32_e32 v11, 0xffff0000, v15
	v_fma_f32 v11, -v1, v65, v11
	v_fmac_f32_e32 v2, v105, v105
	s_waitcnt lgkmcnt(0)
	v_lshlrev_b32_e32 v15, 16, v4
	v_and_b32_e32 v4, 0xffff0000, v4
	v_fma_f32 v84, -v1, v19, v4
	v_lshlrev_b32_e32 v4, 16, v5
	v_fma_f32 v87, -v1, v67, v4
	v_and_b32_e32 v4, 0xffff0000, v5
	v_fma_f32 v74, -v1, v85, v4
	v_lshlrev_b32_e32 v4, 16, v30
	v_fma_f32 v70, -v1, v70, v4
	v_and_b32_e32 v4, 0xffff0000, v30
	v_fma_f32 v65, -v1, v55, v4
	v_lshlrev_b32_e32 v4, 16, v31
	v_fma_f32 v60, -v1, v72, v4
	ds_read2st64_b32 v[4:5], v92 offset0:224 offset1:232
	v_fma_f32 v82, -v1, v82, v15
	v_and_b32_e32 v15, 0xffff0000, v31
	ds_read2st64_b32 v[30:31], v92 offset0:240 offset1:248
	v_fma_f32 v55, -v1, v86, v15
	s_waitcnt lgkmcnt(0)
	v_lshlrev_b32_e32 v15, 16, v4
	v_and_b32_e32 v4, 0xffff0000, v4
	v_fma_f32 v45, -v1, v75, v4
	v_lshlrev_b32_e32 v4, 16, v5
	v_fmac_f32_e32 v2, v82, v82
	v_fma_f32 v40, -v1, v89, v4
	v_and_b32_e32 v4, 0xffff0000, v5
	v_fma_f32 v35, -v1, v77, v4
	v_lshlrev_b32_e32 v4, 16, v30
	v_add_f32_dpp v2, v2, v2 quad_perm:[1,0,3,2] row_mask:0xf bank_mask:0xf bound_ctrl:1
	v_fma_f32 v27, -v1, v78, v4
	v_and_b32_e32 v4, 0xffff0000, v30
	v_add_f32_dpp v2, v2, v2 quad_perm:[2,3,0,1] row_mask:0xf bank_mask:0xf bound_ctrl:1
	v_fma_f32 v23, -v1, v79, v4
	v_lshlrev_b32_e32 v4, 16, v31
	v_add_f32_dpp v2, v2, v2 row_half_mirror row_mask:0xf bank_mask:0xf bound_ctrl:1
	v_fma_f32 v19, -v1, v80, v4
	v_and_b32_e32 v4, 0xffff0000, v31
	v_add_f32_dpp v2, v2, v2 row_mirror row_mask:0xf bank_mask:0xf bound_ctrl:1
	v_fmac_f32_e32 v34, v83, v83
	v_fma_f32 v50, -v1, v88, v15
	v_fma_f32 v15, -v1, v81, v4
	v_mov_b32_e32 v4, v2
	v_fmac_f32_e32 v34, v84, v84
	s_nop 0
	v_permlane16_swap_b32_e32 v2, v4
	v_add_f32_e32 v2, v2, v4
	s_nop 0
	v_add_f32_dpp v4, v34, v34 quad_perm:[1,0,3,2] row_mask:0xf bank_mask:0xf bound_ctrl:1
	v_fmac_f32_e32 v93, v73, v73
	v_fmac_f32_e32 v93, v87, v87
	v_add_f32_dpp v4, v4, v4 quad_perm:[2,3,0,1] row_mask:0xf bank_mask:0xf bound_ctrl:1
	v_fmac_f32_e32 v94, v69, v69
	v_fmac_f32_e32 v94, v74, v74
	v_add_f32_dpp v4, v4, v4 row_half_mirror row_mask:0xf bank_mask:0xf bound_ctrl:1
	v_fmac_f32_e32 v95, v64, v64
	v_fmac_f32_e32 v95, v70, v70
	v_add_f32_dpp v4, v4, v4 row_mirror row_mask:0xf bank_mask:0xf bound_ctrl:1
	v_mov_b32_e32 v5, v4
	s_nop 1
	v_permlane16_swap_b32_e32 v4, v5
	v_add_f32_e32 v77, v4, v5
	s_nop 0
	v_add_f32_dpp v4, v93, v93 quad_perm:[1,0,3,2] row_mask:0xf bank_mask:0xf bound_ctrl:1
	v_fmac_f32_e32 v96, v47, v47
	v_fmac_f32_e32 v96, v59, v59
	v_add_f32_dpp v4, v4, v4 quad_perm:[2,3,0,1] row_mask:0xf bank_mask:0xf bound_ctrl:1
	v_fmac_f32_e32 v96, v65, v65
	v_mul_f32_e32 v97, v46, v46
	v_add_f32_dpp v4, v4, v4 row_half_mirror row_mask:0xf bank_mask:0xf bound_ctrl:1
	v_fmac_f32_e32 v97, v42, v42
	v_fmac_f32_e32 v97, v54, v54
	v_add_f32_dpp v4, v4, v4 row_mirror row_mask:0xf bank_mask:0xf bound_ctrl:1
	v_mov_b32_e32 v5, v4
	s_nop 1
	v_permlane16_swap_b32_e32 v4, v5
	v_add_f32_e32 v80, v4, v5
	s_nop 0
	v_add_f32_dpp v4, v94, v94 quad_perm:[1,0,3,2] row_mask:0xf bank_mask:0xf bound_ctrl:1
	v_fmac_f32_e32 v97, v60, v60
	v_mul_f32_e32 v98, v41, v41
	v_add_f32_dpp v4, v4, v4 quad_perm:[2,3,0,1] row_mask:0xf bank_mask:0xf bound_ctrl:1
	v_fmac_f32_e32 v98, v36, v36
	v_fmac_f32_e32 v98, v49, v49
	v_add_f32_dpp v4, v4, v4 row_half_mirror row_mask:0xf bank_mask:0xf bound_ctrl:1
	v_fmac_f32_e32 v98, v55, v55
	v_mul_f32_e32 v43, v37, v37
	v_add_f32_dpp v4, v4, v4 row_mirror row_mask:0xf bank_mask:0xf bound_ctrl:1
	v_mov_b32_e32 v5, v4
	s_nop 1
	v_permlane16_swap_b32_e32 v4, v5
	v_add_f32_e32 v81, v4, v5
	s_nop 0
	v_add_f32_dpp v4, v95, v95 quad_perm:[1,0,3,2] row_mask:0xf bank_mask:0xf bound_ctrl:1
	v_fmac_f32_e32 v43, v28, v28
	v_fmac_f32_e32 v43, v44, v44
	v_add_f32_dpp v4, v4, v4 quad_perm:[2,3,0,1] row_mask:0xf bank_mask:0xf bound_ctrl:1
	v_fmac_f32_e32 v43, v50, v50
	v_mul_f32_e32 v99, v29, v29
	v_add_f32_dpp v4, v4, v4 row_half_mirror row_mask:0xf bank_mask:0xf bound_ctrl:1
	v_fmac_f32_e32 v99, v24, v24
	v_fmac_f32_e32 v99, v39, v39
	v_add_f32_dpp v4, v4, v4 row_mirror row_mask:0xf bank_mask:0xf bound_ctrl:1
	v_mov_b32_e32 v5, v4
	s_nop 1
	v_permlane16_swap_b32_e32 v4, v5
	v_add_f32_e32 v85, v4, v5
	s_nop 0
	v_add_f32_dpp v4, v96, v96 quad_perm:[1,0,3,2] row_mask:0xf bank_mask:0xf bound_ctrl:1
	v_fmac_f32_e32 v99, v45, v45
	v_mul_f32_e32 v100, v25, v25
	v_add_f32_dpp v4, v4, v4 quad_perm:[2,3,0,1] row_mask:0xf bank_mask:0xf bound_ctrl:1
	v_fmac_f32_e32 v100, v20, v20
	v_fmac_f32_e32 v100, v33, v33
	v_add_f32_dpp v4, v4, v4 row_half_mirror row_mask:0xf bank_mask:0xf bound_ctrl:1
	v_fmac_f32_e32 v100, v40, v40
	v_mul_f32_e32 v101, v21, v21
	v_add_f32_dpp v4, v4, v4 row_mirror row_mask:0xf bank_mask:0xf bound_ctrl:1
	v_mov_b32_e32 v5, v4
	s_nop 1
	v_permlane16_swap_b32_e32 v4, v5
	v_add_f32_e32 v86, v4, v5
	v_mov_b32_e32 v5, v178
	s_load_dwordx2 s[6:7], s[10:11], 0x98
	v_and_b32_e32 v180, 31, v5
	v_lshlrev_b32_e32 v30, 2, v180
	s_waitcnt lgkmcnt(0)
	global_load_dword v31, v30, s[6:7]
	global_load_dword v78, v30, s[6:7] offset:128
	global_load_dword v79, v30, s[6:7] offset:256
	s_nop 0
	global_load_dword v30, v30, s[6:7] offset:384
	v_add_f32_dpp v4, v97, v97 quad_perm:[1,0,3,2] row_mask:0xf bank_mask:0xf bound_ctrl:1
	v_fmac_f32_e32 v101, v16, v16
	v_fmac_f32_e32 v101, v26, v26
	v_add_f32_dpp v4, v4, v4 quad_perm:[2,3,0,1] row_mask:0xf bank_mask:0xf bound_ctrl:1
	v_fmac_f32_e32 v101, v35, v35
	v_mul_f32_e32 v32, v17, v17
	v_add_f32_dpp v4, v4, v4 row_half_mirror row_mask:0xf bank_mask:0xf bound_ctrl:1
	v_fmac_f32_e32 v32, v12, v12
	v_fmac_f32_e32 v32, v22, v22
	v_add_f32_dpp v4, v4, v4 row_mirror row_mask:0xf bank_mask:0xf bound_ctrl:1
	v_mov_b32_e32 v34, v4
	s_nop 1
	v_permlane16_swap_b32_e32 v4, v34
	v_add_f32_e32 v88, v4, v34
	s_nop 0
	v_add_f32_dpp v4, v98, v98 quad_perm:[1,0,3,2] row_mask:0xf bank_mask:0xf bound_ctrl:1
	v_fmac_f32_e32 v32, v27, v27
	v_mul_f32_e32 v102, v13, v13
	v_add_f32_dpp v4, v4, v4 quad_perm:[2,3,0,1] row_mask:0xf bank_mask:0xf bound_ctrl:1
	v_fmac_f32_e32 v102, v9, v9
	v_fmac_f32_e32 v102, v18, v18
	v_add_f32_dpp v4, v4, v4 row_half_mirror row_mask:0xf bank_mask:0xf bound_ctrl:1
	v_fmac_f32_e32 v102, v23, v23
	v_mul_f32_e32 v103, v10, v10
	v_add_f32_dpp v4, v4, v4 row_mirror row_mask:0xf bank_mask:0xf bound_ctrl:1
	v_mov_b32_e32 v34, v4
	s_nop 1
	v_permlane16_swap_b32_e32 v4, v34
	v_add_f32_e32 v75, v4, v34
	s_nop 0
	v_add_f32_dpp v4, v43, v43 quad_perm:[1,0,3,2] row_mask:0xf bank_mask:0xf bound_ctrl:1
	v_fmac_f32_e32 v103, v7, v7
	v_fmac_f32_e32 v103, v14, v14
	v_add_f32_dpp v4, v4, v4 quad_perm:[2,3,0,1] row_mask:0xf bank_mask:0xf bound_ctrl:1
	v_fmac_f32_e32 v103, v19, v19
	v_mul_f32_e32 v104, v8, v8
	v_add_f32_dpp v4, v4, v4 row_half_mirror row_mask:0xf bank_mask:0xf bound_ctrl:1
	v_fmac_f32_e32 v104, v6, v6
	v_fmac_f32_e32 v104, v11, v11
	v_add_f32_dpp v4, v4, v4 row_mirror row_mask:0xf bank_mask:0xf bound_ctrl:1
	v_mov_b32_e32 v34, v4
	s_nop 1
	v_permlane16_swap_b32_e32 v4, v34
	v_add_f32_e32 v72, v4, v34
	s_nop 0
	v_add_f32_dpp v4, v99, v99 quad_perm:[1,0,3,2] row_mask:0xf bank_mask:0xf bound_ctrl:1
	v_fmac_f32_e32 v104, v15, v15
	v_fmamk_f32 v2, v2, 0x3c000000, v184
	v_add_f32_dpp v4, v4, v4 quad_perm:[2,3,0,1] row_mask:0xf bank_mask:0xf bound_ctrl:1
	v_cmp_gt_f32_e32 vcc, s55, v2
	v_fmamk_f32 v77, v77, 0x3c000000, v184
	v_add_f32_dpp v4, v4, v4 row_half_mirror row_mask:0xf bank_mask:0xf bound_ctrl:1
	s_waitcnt vmcnt(0)
	v_mul_f32_e32 v30, 0x3f24fd5c, v30
	v_add_f32_dpp v4, v4, v4 row_mirror row_mask:0xf bank_mask:0xf bound_ctrl:1
	v_mov_b32_e32 v34, v4
	s_nop 1
	v_permlane16_swap_b32_e32 v4, v34
	v_add_f32_e32 v67, v4, v34
	s_nop 0
	v_add_f32_dpp v4, v100, v100 quad_perm:[1,0,3,2] row_mask:0xf bank_mask:0xf bound_ctrl:1
	s_nop 1
	v_add_f32_dpp v4, v4, v4 quad_perm:[2,3,0,1] row_mask:0xf bank_mask:0xf bound_ctrl:1
	s_nop 1
	v_add_f32_dpp v4, v4, v4 row_half_mirror row_mask:0xf bank_mask:0xf bound_ctrl:1
	s_nop 1
	v_add_f32_dpp v4, v4, v4 row_mirror row_mask:0xf bank_mask:0xf bound_ctrl:1
	v_mov_b32_e32 v34, v4
	s_nop 1
	v_permlane16_swap_b32_e32 v4, v34
	v_add_f32_e32 v62, v4, v34
	s_nop 0
	v_add_f32_dpp v4, v101, v101 quad_perm:[1,0,3,2] row_mask:0xf bank_mask:0xf bound_ctrl:1
	s_nop 1
	v_add_f32_dpp v4, v4, v4 quad_perm:[2,3,0,1] row_mask:0xf bank_mask:0xf bound_ctrl:1
	s_nop 1
	v_add_f32_dpp v4, v4, v4 row_half_mirror row_mask:0xf bank_mask:0xf bound_ctrl:1
	s_nop 1
	v_add_f32_dpp v4, v4, v4 row_mirror row_mask:0xf bank_mask:0xf bound_ctrl:1
	v_mov_b32_e32 v34, v4
	s_nop 1
	v_permlane16_swap_b32_e32 v4, v34
	v_add_f32_e32 v57, v4, v34
	s_nop 0
	v_add_f32_dpp v4, v32, v32 quad_perm:[1,0,3,2] row_mask:0xf bank_mask:0xf bound_ctrl:1
	v_mul_f32_e32 v34, 0x3f24fd5c, v31
	v_mul_f32_e32 v31, 0x3f24fd5c, v79
	v_add_f32_dpp v4, v4, v4 quad_perm:[2,3,0,1] row_mask:0xf bank_mask:0xf bound_ctrl:1
	s_nop 1
	v_add_f32_dpp v4, v4, v4 row_half_mirror row_mask:0xf bank_mask:0xf bound_ctrl:1
	s_nop 1
	v_add_f32_dpp v4, v4, v4 row_mirror row_mask:0xf bank_mask:0xf bound_ctrl:1
	v_mov_b32_e32 v32, v4
	s_nop 1
	v_permlane16_swap_b32_e32 v4, v32
	v_add_f32_e32 v52, v4, v32
	s_nop 0
	v_add_f32_dpp v4, v102, v102 quad_perm:[1,0,3,2] row_mask:0xf bank_mask:0xf bound_ctrl:1
	s_nop 1
	v_add_f32_dpp v4, v4, v4 quad_perm:[2,3,0,1] row_mask:0xf bank_mask:0xf bound_ctrl:1
	s_nop 1
	v_add_f32_dpp v4, v4, v4 row_half_mirror row_mask:0xf bank_mask:0xf bound_ctrl:1
	s_nop 1
	v_add_f32_dpp v4, v4, v4 row_mirror row_mask:0xf bank_mask:0xf bound_ctrl:1
	v_mov_b32_e32 v32, v4
	s_nop 1
	v_permlane16_swap_b32_e32 v4, v32
	v_add_f32_e32 v48, v4, v32
	s_nop 0
	v_add_f32_dpp v4, v103, v103 quad_perm:[1,0,3,2] row_mask:0xf bank_mask:0xf bound_ctrl:1
	s_nop 1
	v_add_f32_dpp v4, v4, v4 quad_perm:[2,3,0,1] row_mask:0xf bank_mask:0xf bound_ctrl:1
	s_nop 1
	v_add_f32_dpp v4, v4, v4 row_half_mirror row_mask:0xf bank_mask:0xf bound_ctrl:1
	s_nop 1
	v_add_f32_dpp v4, v4, v4 row_mirror row_mask:0xf bank_mask:0xf bound_ctrl:1
	v_mov_b32_e32 v32, v4
	s_nop 1
	v_permlane16_swap_b32_e32 v4, v32
	v_add_f32_e32 v43, v4, v32
	s_nop 0
	v_add_f32_dpp v4, v104, v104 quad_perm:[1,0,3,2] row_mask:0xf bank_mask:0xf bound_ctrl:1
	s_nop 1
	v_add_f32_dpp v4, v4, v4 quad_perm:[2,3,0,1] row_mask:0xf bank_mask:0xf bound_ctrl:1
	s_nop 1
	v_add_f32_dpp v4, v4, v4 row_half_mirror row_mask:0xf bank_mask:0xf bound_ctrl:1
	s_nop 1
	v_add_f32_dpp v4, v4, v4 row_mirror row_mask:0xf bank_mask:0xf bound_ctrl:1
	v_mov_b32_e32 v32, v4
	s_nop 1
	v_permlane16_swap_b32_e32 v4, v32
	v_add_f32_e32 v38, v4, v32
	v_mul_f32_e32 v4, 0x4f800000, v2
	v_cndmask_b32_e32 v4, v2, v4, vcc
	v_mul_f32_e32 v32, 0x3f24fd5c, v78
	v_sqrt_f32_e32 v78, v4
	v_ashrrev_i32_e32 v2, 3, v5
	v_and_b32_e32 v2, -4, v2
	v_add_u32_e32 v2, s86, v2
	v_add_u32_e32 v5, -1, v78
	v_fma_f32 v79, -v5, v78, v4
	v_cmp_ge_f32_e64 s[6:7], 0, v79
	v_add_u32_e32 v79, 1, v78
	s_nop 0
	v_cndmask_b32_e64 v5, v78, v5, s[6:7]
	v_fma_f32 v78, -v79, v78, v4
	v_cmp_lt_f32_e64 s[6:7], 0, v78
	s_nop 1
	v_cndmask_b32_e64 v5, v5, v79, s[6:7]
	v_mul_f32_e32 v78, 0x37800000, v5
	v_cndmask_b32_e32 v5, v5, v78, vcc
	v_cmp_class_f32_e32 vcc, v4, v185
	s_nop 1
	v_cndmask_b32_e32 v78, v5, v4, vcc
	v_div_scale_f32 v79, s[6:7], v78, v78, 1.0
	v_rcp_f32_e32 v89, v79
	s_add_u32 s6, s27, s87
	s_addc_u32 s7, s23, s76
	v_lshl_add_u64 v[4:5], s[6:7], 0, v[180:181]
	v_fma_f32 v90, -v79, v89, 1.0
	v_fmac_f32_e32 v89, v90, v89
	v_div_scale_f32 v90, vcc, 1.0, v78, 1.0
	v_mul_f32_e32 v91, v90, v89
	v_fma_f32 v92, -v79, v91, v90
	v_fmac_f32_e32 v91, v92, v89
	v_fma_f32 v79, -v79, v91, v90
	v_div_fmas_f32 v79, v79, v89, v91
	v_div_fixup_f32 v89, v79, v78, 1.0
	v_mul_f32_e32 v3, v3, v89
	v_mul_f32_e32 v3, v3, v34
	v_mov_b32_e32 v90, v181
	v_cvt_pk_fp8_f32 v90, v3, 0
	v_ashrrev_i32_e32 v3, 31, v2
	v_lshlrev_b64 v[78:79], 10, v[2:3]
	v_mul_f32_e32 v3, v76, v89
	v_mul_f32_e32 v3, v3, v32
	v_mov_b32_e32 v76, v181
	v_lshl_add_u64 v[78:79], v[4:5], 0, v[78:79]
	v_cvt_pk_fp8_f32 v76, v3, 0
	v_mul_f32_e32 v3, v105, v89
	global_store_byte v[78:79], v90, off
	v_mul_f32_e32 v3, v3, v31
	v_mov_b32_e32 v90, v181
	v_cvt_pk_fp8_f32 v90, v3, 0
	v_mul_f32_e32 v3, v82, v89
	v_mul_f32_e32 v82, 0x4f800000, v77
	v_cmp_gt_f32_e32 vcc, s55, v77
	v_mul_f32_e32 v3, v3, v30
	v_mov_b32_e32 v89, v181
	v_cndmask_b32_e32 v77, v77, v82, vcc
	v_sqrt_f32_e32 v82, v77
	v_cvt_pk_fp8_f32 v89, v3, 0
	global_store_byte v[78:79], v76, off offset:32
	global_store_byte v[78:79], v90, off offset:64
	global_store_byte v[78:79], v89, off offset:96
	v_add_u32_e32 v3, -1, v82
	v_fma_f32 v91, -v3, v82, v77
	v_cmp_ge_f32_e64 s[6:7], 0, v91
	v_add_u32_e32 v91, 1, v82
	s_xor_b32 s100, s98, 1
	s_and_b32 s100, s100, s99
	s_cselect_b32 s101, 0, s18
	s_mov_b32 s98, s100
	s_mov_b32 s99, 0
	s_add_i32 s53, s53, s101
	v_cndmask_b32_e64 v3, v82, v3, s[6:7]
	v_fma_f32 v82, -v91, v82, v77
	v_cmp_lt_f32_e64 s[6:7], 0, v82
	s_cmp_lt_i32 s53, s35
	s_nop 0
	v_cndmask_b32_e64 v3, v3, v91, s[6:7]
	v_mul_f32_e32 v82, 0x37800000, v3
	v_cndmask_b32_e32 v3, v3, v82, vcc
	v_cmp_class_f32_e32 vcc, v77, v185
	s_nop 1
	v_cndmask_b32_e32 v3, v3, v77, vcc
	v_div_scale_f32 v77, s[6:7], v3, v3, 1.0
	v_rcp_f32_e32 v82, v77
	s_nop 0
	v_fma_f32 v76, -v77, v82, 1.0
	v_fmac_f32_e32 v82, v76, v82
	v_div_scale_f32 v76, vcc, 1.0, v3, 1.0
	v_mul_f32_e32 v78, v76, v82
	v_fma_f32 v79, -v77, v78, v76
	v_fmac_f32_e32 v78, v79, v82
	v_fma_f32 v76, -v77, v78, v76
	v_div_fmas_f32 v76, v76, v82, v78
	v_div_fixup_f32 v3, v76, v3, 1.0
	v_mul_f32_e32 v68, v68, v3
	v_mul_f32_e32 v68, v68, v34
	v_mov_b32_e32 v78, v181
	v_or_b32_e32 v76, 1, v2
	v_cvt_pk_fp8_f32 v78, v68, 0
	v_ashrrev_i32_e32 v77, 31, v76
	v_mul_f32_e32 v68, v71, v3
	v_lshlrev_b64 v[76:77], 10, v[76:77]
	v_mul_f32_e32 v68, v68, v32
	v_mov_b32_e32 v71, v181
	v_lshl_add_u64 v[76:77], v[4:5], 0, v[76:77]
	v_cvt_pk_fp8_f32 v71, v68, 0
	v_mul_f32_e32 v68, v83, v3
	global_store_byte v[76:77], v78, off
	v_mul_f32_e32 v68, v68, v31
	v_mov_b32_e32 v78, v181
	v_cvt_pk_fp8_f32 v78, v68, 0
	v_fmamk_f32 v68, v80, 0x3c000000, v184
	v_mul_f32_e32 v79, 0x4f800000, v68
	v_cmp_gt_f32_e32 vcc, s55, v68
	v_mul_f32_e32 v3, v84, v3
	v_mul_f32_e32 v3, v3, v30
	v_cndmask_b32_e32 v68, v68, v79, vcc
	v_sqrt_f32_e32 v79, v68
	v_mov_b32_e32 v80, v181
	v_cvt_pk_fp8_f32 v80, v3, 0
	global_store_byte v[76:77], v71, off offset:32
	global_store_byte v[76:77], v78, off offset:64
	global_store_byte v[76:77], v80, off offset:96
	v_add_u32_e32 v3, -1, v79
	v_fma_f32 v82, -v3, v79, v68
	v_cmp_ge_f32_e64 s[6:7], 0, v82
	v_add_u32_e32 v82, 1, v79
	s_nop 0
	v_cndmask_b32_e64 v3, v79, v3, s[6:7]
	v_fma_f32 v79, -v82, v79, v68
	v_cmp_lt_f32_e64 s[6:7], 0, v79
	s_nop 1
	v_cndmask_b32_e64 v3, v3, v82, s[6:7]
	v_mul_f32_e32 v79, 0x37800000, v3
	v_cndmask_b32_e32 v3, v3, v79, vcc
	v_cmp_class_f32_e32 vcc, v68, v185
	s_nop 1
	v_cndmask_b32_e32 v3, v3, v68, vcc
	v_div_scale_f32 v68, s[6:7], v3, v3, 1.0
	v_rcp_f32_e32 v79, v68
	s_nop 0
	v_fma_f32 v71, -v68, v79, 1.0
	v_fmac_f32_e32 v79, v71, v79
	v_div_scale_f32 v71, vcc, 1.0, v3, 1.0
	v_mul_f32_e32 v76, v71, v79
	v_fma_f32 v77, -v68, v76, v71
	v_fmac_f32_e32 v76, v77, v79
	v_fma_f32 v68, -v68, v76, v71
	v_div_fmas_f32 v68, v68, v79, v76
	v_div_fixup_f32 v3, v68, v3, 1.0
	v_mul_f32_e32 v63, v63, v3
	v_mul_f32_e32 v63, v63, v34
	v_mov_b32_e32 v68, v181
	v_or_b32_e32 v76, 2, v2
	v_cvt_pk_fp8_f32 v68, v63, 0
	v_ashrrev_i32_e32 v77, 31, v76
	v_mul_f32_e32 v63, v66, v3
	v_lshlrev_b64 v[76:77], 10, v[76:77]
	v_mul_f32_e32 v63, v63, v32
	v_mov_b32_e32 v66, v181
	v_lshl_add_u64 v[76:77], v[4:5], 0, v[76:77]
	v_cvt_pk_fp8_f32 v66, v63, 0
	v_mul_f32_e32 v63, v73, v3
	global_store_byte v[76:77], v68, off
	v_mul_f32_e32 v63, v63, v31
	v_mov_b32_e32 v68, v181
	v_cvt_pk_fp8_f32 v68, v63, 0
	v_fmamk_f32 v63, v81, 0x3c000000, v184
	v_mul_f32_e32 v71, 0x4f800000, v63
	v_cmp_gt_f32_e32 vcc, s55, v63
	v_mul_f32_e32 v3, v87, v3
	v_mul_f32_e32 v3, v3, v30
	v_cndmask_b32_e32 v63, v63, v71, vcc
	v_sqrt_f32_e32 v71, v63
	v_mov_b32_e32 v73, v181
	v_cvt_pk_fp8_f32 v73, v3, 0
	global_store_byte v[76:77], v66, off offset:32
	global_store_byte v[76:77], v68, off offset:64
	global_store_byte v[76:77], v73, off offset:96
	v_add_u32_e32 v3, -1, v71
	v_fma_f32 v78, -v3, v71, v63
	v_cmp_ge_f32_e64 s[6:7], 0, v78
	v_add_u32_e32 v78, 1, v71
	v_or_b32_e32 v76, 3, v2
	v_cndmask_b32_e64 v3, v71, v3, s[6:7]
	v_fma_f32 v71, -v78, v71, v63
	v_cmp_lt_f32_e64 s[6:7], 0, v71
	v_ashrrev_i32_e32 v77, 31, v76
	v_lshlrev_b64 v[76:77], 10, v[76:77]
	v_cndmask_b32_e64 v3, v3, v78, s[6:7]
	v_mul_f32_e32 v71, 0x37800000, v3
	v_cndmask_b32_e32 v3, v3, v71, vcc
	v_cmp_class_f32_e32 vcc, v63, v185
	v_lshl_add_u64 v[76:77], v[4:5], 0, v[76:77]
	s_nop 0
	v_cndmask_b32_e32 v3, v3, v63, vcc
	v_div_scale_f32 v63, s[6:7], v3, v3, 1.0
	v_rcp_f32_e32 v71, v63
	s_nop 0
	v_fma_f32 v66, -v63, v71, 1.0
	v_fmac_f32_e32 v71, v66, v71
	v_div_scale_f32 v66, vcc, 1.0, v3, 1.0
	v_mul_f32_e32 v68, v66, v71
	v_fma_f32 v73, -v63, v68, v66
	v_fmac_f32_e32 v68, v73, v71
	v_fma_f32 v63, -v63, v68, v66
	v_div_fmas_f32 v63, v63, v71, v68
	v_div_fixup_f32 v3, v63, v3, 1.0
	v_mul_f32_e32 v58, v58, v3
	v_mul_f32_e32 v58, v58, v34
	v_mov_b32_e32 v63, v181
	v_cvt_pk_fp8_f32 v63, v58, 0
	v_mul_f32_e32 v58, v61, v3
	v_mul_f32_e32 v58, v58, v32
	v_mov_b32_e32 v61, v181
	v_cvt_pk_fp8_f32 v61, v58, 0
	v_mul_f32_e32 v58, v69, v3
	global_store_byte v[76:77], v63, off
	v_mul_f32_e32 v58, v58, v31
	v_mov_b32_e32 v63, v181
	v_cvt_pk_fp8_f32 v63, v58, 0
	v_fmamk_f32 v58, v85, 0x3c000000, v184
	v_mul_f32_e32 v66, 0x4f800000, v58
	v_cmp_gt_f32_e32 vcc, s55, v58
	v_mul_f32_e32 v3, v74, v3
	v_mul_f32_e32 v3, v3, v30
	v_cndmask_b32_e32 v58, v58, v66, vcc
	v_sqrt_f32_e32 v66, v58
	v_mov_b32_e32 v68, v181
	v_cvt_pk_fp8_f32 v68, v3, 0
	global_store_byte v[76:77], v61, off offset:32
	global_store_byte v[76:77], v63, off offset:64
	global_store_byte v[76:77], v68, off offset:96
	v_add_u32_e32 v3, -1, v66
	v_fma_f32 v69, -v3, v66, v58
	v_cmp_ge_f32_e64 s[6:7], 0, v69
	v_add_u32_e32 v69, 1, v66
	s_nop 0
	v_cndmask_b32_e64 v3, v66, v3, s[6:7]
	v_fma_f32 v66, -v69, v66, v58
	v_cmp_lt_f32_e64 s[6:7], 0, v66
	s_nop 1
	v_cndmask_b32_e64 v3, v3, v69, s[6:7]
	v_mul_f32_e32 v66, 0x37800000, v3
	v_cndmask_b32_e32 v3, v3, v66, vcc
	v_cmp_class_f32_e32 vcc, v58, v185
	s_nop 1
	v_cndmask_b32_e32 v3, v3, v58, vcc
	v_div_scale_f32 v58, s[6:7], v3, v3, 1.0
	v_rcp_f32_e32 v66, v58
	s_nop 0
	v_fma_f32 v61, -v58, v66, 1.0
	v_fmac_f32_e32 v66, v61, v66
	v_div_scale_f32 v61, vcc, 1.0, v3, 1.0
	v_mul_f32_e32 v63, v61, v66
	v_fma_f32 v68, -v58, v63, v61
	v_fmac_f32_e32 v63, v68, v66
	v_fma_f32 v58, -v58, v63, v61
	v_div_fmas_f32 v58, v58, v66, v63
	v_div_fixup_f32 v3, v58, v3, 1.0
	v_mul_f32_e32 v53, v53, v3
	v_mul_f32_e32 v53, v53, v34
	v_mov_b32_e32 v58, v181
	v_add_u32_e32 v68, 8, v2
	v_cvt_pk_fp8_f32 v58, v53, 0
	v_ashrrev_i32_e32 v69, 31, v68
	v_mul_f32_e32 v53, v56, v3
	v_lshlrev_b64 v[68:69], 10, v[68:69]
	v_mul_f32_e32 v53, v53, v32
	v_mov_b32_e32 v56, v181
	v_lshl_add_u64 v[68:69], v[4:5], 0, v[68:69]
	v_cvt_pk_fp8_f32 v56, v53, 0
	v_mul_f32_e32 v53, v64, v3
	global_store_byte v[68:69], v58, off
	v_mul_f32_e32 v53, v53, v31
	v_mov_b32_e32 v58, v181
	v_cvt_pk_fp8_f32 v58, v53, 0
	v_fmamk_f32 v53, v86, 0x3c000000, v184
	v_mul_f32_e32 v61, 0x4f800000, v53
	v_cmp_gt_f32_e32 vcc, s55, v53
	v_mul_f32_e32 v3, v70, v3
	v_mul_f32_e32 v3, v3, v30
	v_cndmask_b32_e32 v53, v53, v61, vcc
	v_sqrt_f32_e32 v61, v53
	v_mov_b32_e32 v63, v181
	v_cvt_pk_fp8_f32 v63, v3, 0
	global_store_byte v[68:69], v56, off offset:32
	global_store_byte v[68:69], v58, off offset:64
	global_store_byte v[68:69], v63, off offset:96
	v_add_u32_e32 v3, -1, v61
	v_fma_f32 v64, -v3, v61, v53
	v_cmp_ge_f32_e64 s[6:7], 0, v64
	v_add_u32_e32 v64, 1, v61
	v_add_u32_e32 v68, 9, v2
	v_cndmask_b32_e64 v3, v61, v3, s[6:7]
	v_fma_f32 v61, -v64, v61, v53
	v_cmp_lt_f32_e64 s[6:7], 0, v61
	v_ashrrev_i32_e32 v69, 31, v68
	v_lshlrev_b64 v[68:69], 10, v[68:69]
	v_cndmask_b32_e64 v3, v3, v64, s[6:7]
	v_mul_f32_e32 v61, 0x37800000, v3
	v_cndmask_b32_e32 v3, v3, v61, vcc
	v_cmp_class_f32_e32 vcc, v53, v185
	v_lshl_add_u64 v[68:69], v[4:5], 0, v[68:69]
	s_nop 0
	v_cndmask_b32_e32 v3, v3, v53, vcc
	v_div_scale_f32 v53, s[6:7], v3, v3, 1.0
	v_rcp_f32_e32 v61, v53
	s_nop 0
	v_fma_f32 v56, -v53, v61, 1.0
	v_fmac_f32_e32 v61, v56, v61
	v_div_scale_f32 v56, vcc, 1.0, v3, 1.0
	v_mul_f32_e32 v58, v56, v61
	v_fma_f32 v63, -v53, v58, v56
	v_fmac_f32_e32 v58, v63, v61
	v_fma_f32 v53, -v53, v58, v56
	v_div_fmas_f32 v53, v53, v61, v58
	v_div_fixup_f32 v3, v53, v3, 1.0
	v_mul_f32_e32 v47, v47, v3
	v_mul_f32_e32 v47, v47, v34
	v_mov_b32_e32 v53, v181
	v_cvt_pk_fp8_f32 v53, v47, 0
	v_mul_f32_e32 v47, v51, v3
	v_mul_f32_e32 v47, v47, v32
	v_mov_b32_e32 v51, v181
	v_cvt_pk_fp8_f32 v51, v47, 0
	v_mul_f32_e32 v47, v59, v3
	global_store_byte v[68:69], v53, off
	v_mul_f32_e32 v47, v47, v31
	v_mov_b32_e32 v53, v181
	v_cvt_pk_fp8_f32 v53, v47, 0
	v_fmamk_f32 v47, v88, 0x3c000000, v184
	v_mul_f32_e32 v56, 0x4f800000, v47
	v_cmp_gt_f32_e32 vcc, s55, v47
	v_mul_f32_e32 v3, v65, v3
	v_mul_f32_e32 v3, v3, v30
	v_cndmask_b32_e32 v47, v47, v56, vcc
	v_sqrt_f32_e32 v56, v47
	v_mov_b32_e32 v58, v181
	v_cvt_pk_fp8_f32 v58, v3, 0
	global_store_byte v[68:69], v51, off offset:32
	global_store_byte v[68:69], v53, off offset:64
	global_store_byte v[68:69], v58, off offset:96
	v_add_u32_e32 v3, -1, v56
	v_fma_f32 v59, -v3, v56, v47
	v_cmp_ge_f32_e64 s[6:7], 0, v59
	v_add_u32_e32 v59, 1, v56
	s_nop 0
	v_cndmask_b32_e64 v3, v56, v3, s[6:7]
	v_fma_f32 v56, -v59, v56, v47
	v_cmp_lt_f32_e64 s[6:7], 0, v56
	s_nop 1
	v_cndmask_b32_e64 v3, v3, v59, s[6:7]
	v_mul_f32_e32 v56, 0x37800000, v3
	v_cndmask_b32_e32 v3, v3, v56, vcc
	v_cmp_class_f32_e32 vcc, v47, v185
	s_nop 1
	v_cndmask_b32_e32 v3, v3, v47, vcc
	v_div_scale_f32 v47, s[6:7], v3, v3, 1.0
	v_rcp_f32_e32 v56, v47
	s_nop 0
	v_fma_f32 v51, -v47, v56, 1.0
	v_fmac_f32_e32 v56, v51, v56
	v_div_scale_f32 v51, vcc, 1.0, v3, 1.0
	v_mul_f32_e32 v53, v51, v56
	v_fma_f32 v58, -v47, v53, v51
	v_fmac_f32_e32 v53, v58, v56
	v_fma_f32 v47, -v47, v53, v51
	v_div_fmas_f32 v47, v47, v56, v53
	v_div_fixup_f32 v3, v47, v3, 1.0
	v_mul_f32_e32 v42, v42, v3
	v_mul_f32_e32 v42, v42, v34
	v_mov_b32_e32 v47, v181
	v_add_u32_e32 v58, 10, v2
	v_cvt_pk_fp8_f32 v47, v42, 0
	v_ashrrev_i32_e32 v59, 31, v58
	v_mul_f32_e32 v42, v46, v3
	v_lshlrev_b64 v[58:59], 10, v[58:59]
	v_mul_f32_e32 v42, v42, v32
	v_mov_b32_e32 v46, v181
	v_lshl_add_u64 v[58:59], v[4:5], 0, v[58:59]
	v_cvt_pk_fp8_f32 v46, v42, 0
	v_mul_f32_e32 v42, v54, v3
	global_store_byte v[58:59], v47, off
	v_mul_f32_e32 v42, v42, v31
	v_mov_b32_e32 v47, v181
	v_cvt_pk_fp8_f32 v47, v42, 0
	v_fmamk_f32 v42, v75, 0x3c000000, v184
	v_mul_f32_e32 v51, 0x4f800000, v42
	v_cmp_gt_f32_e32 vcc, s55, v42
	v_mul_f32_e32 v3, v60, v3
	v_mul_f32_e32 v3, v3, v30
	v_cndmask_b32_e32 v42, v42, v51, vcc
	v_sqrt_f32_e32 v51, v42
	v_mov_b32_e32 v53, v181
	v_cvt_pk_fp8_f32 v53, v3, 0
	global_store_byte v[58:59], v46, off offset:32
	global_store_byte v[58:59], v47, off offset:64
	global_store_byte v[58:59], v53, off offset:96
	v_add_u32_e32 v3, -1, v51
	v_fma_f32 v54, -v3, v51, v42
	v_cmp_ge_f32_e64 s[6:7], 0, v54
	v_add_u32_e32 v54, 1, v51
	s_nop 0
	v_cndmask_b32_e64 v3, v51, v3, s[6:7]
	v_fma_f32 v51, -v54, v51, v42
	v_cmp_lt_f32_e64 s[6:7], 0, v51
	s_nop 1
	v_cndmask_b32_e64 v3, v3, v54, s[6:7]
	v_mul_f32_e32 v51, 0x37800000, v3
	v_cndmask_b32_e32 v3, v3, v51, vcc
	v_cmp_class_f32_e32 vcc, v42, v185
	s_nop 1
	v_cndmask_b32_e32 v3, v3, v42, vcc
	v_div_scale_f32 v42, s[6:7], v3, v3, 1.0
	v_rcp_f32_e32 v51, v42
	s_nop 0
	v_fma_f32 v46, -v42, v51, 1.0
	v_fmac_f32_e32 v51, v46, v51
	v_div_scale_f32 v46, vcc, 1.0, v3, 1.0
	v_mul_f32_e32 v47, v46, v51
	v_fma_f32 v53, -v42, v47, v46
	v_fmac_f32_e32 v47, v53, v51
	v_fma_f32 v42, -v42, v47, v46
	v_div_fmas_f32 v42, v42, v51, v47
	v_div_fixup_f32 v3, v42, v3, 1.0
	v_mul_f32_e32 v36, v36, v3
	v_mul_f32_e32 v36, v36, v34
	v_mov_b32_e32 v42, v181
	v_add_u32_e32 v46, 11, v2
	v_cvt_pk_fp8_f32 v42, v36, 0
	v_ashrrev_i32_e32 v47, 31, v46
	v_mul_f32_e32 v36, v41, v3
	v_lshlrev_b64 v[46:47], 10, v[46:47]
	v_mul_f32_e32 v36, v36, v32
	v_mov_b32_e32 v41, v181
	v_lshl_add_u64 v[46:47], v[4:5], 0, v[46:47]
	v_cvt_pk_fp8_f32 v41, v36, 0
	v_mul_f32_e32 v36, v49, v3
	global_store_byte v[46:47], v42, off
	v_mul_f32_e32 v36, v36, v31
	v_mov_b32_e32 v42, v181
	v_cvt_pk_fp8_f32 v42, v36, 0
	v_fmamk_f32 v36, v72, 0x3c000000, v184
	v_mul_f32_e32 v49, 0x4f800000, v36
	v_cmp_gt_f32_e32 vcc, s55, v36
	v_mul_f32_e32 v3, v55, v3
	v_mul_f32_e32 v3, v3, v30
	v_cndmask_b32_e32 v36, v36, v49, vcc
	v_sqrt_f32_e32 v49, v36
	v_mov_b32_e32 v51, v181
	v_cvt_pk_fp8_f32 v51, v3, 0
	global_store_byte v[46:47], v41, off offset:32
	global_store_byte v[46:47], v42, off offset:64
	global_store_byte v[46:47], v51, off offset:96
	v_add_u32_e32 v3, -1, v49
	v_fma_f32 v53, -v3, v49, v36
	v_cmp_ge_f32_e64 s[6:7], 0, v53
	v_add_u32_e32 v53, 1, v49
	s_nop 0
	v_cndmask_b32_e64 v3, v49, v3, s[6:7]
	v_fma_f32 v49, -v53, v49, v36
	v_cmp_lt_f32_e64 s[6:7], 0, v49
	s_nop 1
	v_cndmask_b32_e64 v3, v3, v53, s[6:7]
	v_mul_f32_e32 v49, 0x37800000, v3
	v_cndmask_b32_e32 v3, v3, v49, vcc
	v_cmp_class_f32_e32 vcc, v36, v185
	s_nop 1
	v_cndmask_b32_e32 v3, v3, v36, vcc
	v_div_scale_f32 v36, s[6:7], v3, v3, 1.0
	v_rcp_f32_e32 v49, v36
	s_nop 0
	v_fma_f32 v41, -v36, v49, 1.0
	v_fmac_f32_e32 v49, v41, v49
	v_div_scale_f32 v41, vcc, 1.0, v3, 1.0
	v_mul_f32_e32 v42, v41, v49
	v_fma_f32 v46, -v36, v42, v41
	v_fmac_f32_e32 v42, v46, v49
	v_fma_f32 v36, -v36, v42, v41
	v_div_fmas_f32 v36, v36, v49, v42
	v_div_fixup_f32 v3, v36, v3, 1.0
	v_mul_f32_e32 v28, v28, v3
	v_mul_f32_e32 v28, v28, v34
	v_mov_b32_e32 v36, v181
	v_add_u32_e32 v46, 16, v2
	v_cvt_pk_fp8_f32 v36, v28, 0
	v_ashrrev_i32_e32 v47, 31, v46
	v_lshlrev_b64 v[46:47], 10, v[46:47]
	v_lshl_add_u64 v[46:47], v[4:5], 0, v[46:47]
	v_mul_f32_e32 v28, v37, v3
	global_store_byte v[46:47], v36, off
	v_mul_f32_e32 v28, v28, v32
	v_mov_b32_e32 v36, v181
	v_cvt_pk_fp8_f32 v36, v28, 0
	v_mul_f32_e32 v28, v44, v3
	v_mul_f32_e32 v28, v28, v31
	v_mov_b32_e32 v37, v181
	v_cvt_pk_fp8_f32 v37, v28, 0
	v_fmamk_f32 v28, v67, 0x3c000000, v184
	v_mul_f32_e32 v41, 0x4f800000, v28
	v_cmp_gt_f32_e32 vcc, s55, v28
	v_mul_f32_e32 v3, v50, v3
	v_mul_f32_e32 v3, v3, v30
	v_cndmask_b32_e32 v28, v28, v41, vcc
	v_sqrt_f32_e32 v41, v28
	v_mov_b32_e32 v42, v181
	v_cvt_pk_fp8_f32 v42, v3, 0
	global_store_byte v[46:47], v36, off offset:32
	global_store_byte v[46:47], v37, off offset:64
	global_store_byte v[46:47], v42, off offset:96
	v_add_u32_e32 v3, -1, v41
	v_fma_f32 v44, -v3, v41, v28
	v_cmp_ge_f32_e64 s[6:7], 0, v44
	v_add_u32_e32 v44, 1, v41
	s_nop 0
	v_cndmask_b32_e64 v3, v41, v3, s[6:7]
	v_fma_f32 v41, -v44, v41, v28
	v_cmp_lt_f32_e64 s[6:7], 0, v41
	s_nop 1
	v_cndmask_b32_e64 v3, v3, v44, s[6:7]
	v_mul_f32_e32 v41, 0x37800000, v3
	v_cndmask_b32_e32 v3, v3, v41, vcc
	v_cmp_class_f32_e32 vcc, v28, v185
	s_nop 1
	v_cndmask_b32_e32 v3, v3, v28, vcc
	v_div_scale_f32 v28, s[6:7], v3, v3, 1.0
	v_rcp_f32_e32 v41, v28
	s_nop 0
	v_fma_f32 v36, -v28, v41, 1.0
	v_fmac_f32_e32 v41, v36, v41
	v_div_scale_f32 v36, vcc, 1.0, v3, 1.0
	v_mul_f32_e32 v37, v36, v41
	v_fma_f32 v42, -v28, v37, v36
	v_fmac_f32_e32 v37, v42, v41
	v_fma_f32 v28, -v28, v37, v36
	v_div_fmas_f32 v28, v28, v41, v37
	v_div_fixup_f32 v3, v28, v3, 1.0
	v_mul_f32_e32 v24, v24, v3
	v_mul_f32_e32 v24, v24, v34
	v_mov_b32_e32 v28, v181
	v_add_u32_e32 v36, 17, v2
	v_cvt_pk_fp8_f32 v28, v24, 0
	v_ashrrev_i32_e32 v37, 31, v36
	v_lshlrev_b64 v[36:37], 10, v[36:37]
	v_lshl_add_u64 v[36:37], v[4:5], 0, v[36:37]
	v_mul_f32_e32 v24, v29, v3
	global_store_byte v[36:37], v28, off
	v_mul_f32_e32 v24, v24, v32
	v_mov_b32_e32 v28, v181
	v_cvt_pk_fp8_f32 v28, v24, 0
	v_mul_f32_e32 v24, v39, v3
	v_mul_f32_e32 v24, v24, v31
	v_mov_b32_e32 v29, v181
	v_cvt_pk_fp8_f32 v29, v24, 0
	v_fmamk_f32 v24, v62, 0x3c000000, v184
	v_mul_f32_e32 v39, 0x4f800000, v24
	v_cmp_gt_f32_e32 vcc, s55, v24
	v_mul_f32_e32 v3, v45, v3
	v_mul_f32_e32 v3, v3, v30
	v_cndmask_b32_e32 v24, v24, v39, vcc
	v_sqrt_f32_e32 v39, v24
	v_mov_b32_e32 v41, v181
	v_cvt_pk_fp8_f32 v41, v3, 0
	global_store_byte v[36:37], v28, off offset:32
	global_store_byte v[36:37], v29, off offset:64
	global_store_byte v[36:37], v41, off offset:96
	v_add_u32_e32 v3, -1, v39
	v_fma_f32 v42, -v3, v39, v24
	v_cmp_ge_f32_e64 s[6:7], 0, v42
	v_add_u32_e32 v42, 1, v39
	s_nop 0
	v_cndmask_b32_e64 v3, v39, v3, s[6:7]
	v_fma_f32 v39, -v42, v39, v24
	v_cmp_lt_f32_e64 s[6:7], 0, v39
	s_nop 1
	v_cndmask_b32_e64 v3, v3, v42, s[6:7]
	v_mul_f32_e32 v39, 0x37800000, v3
	v_cndmask_b32_e32 v3, v3, v39, vcc
	v_cmp_class_f32_e32 vcc, v24, v185
	s_nop 1
	v_cndmask_b32_e32 v3, v3, v24, vcc
	v_div_scale_f32 v24, s[6:7], v3, v3, 1.0
	v_rcp_f32_e32 v39, v24
	s_nop 0
	v_fma_f32 v28, -v24, v39, 1.0
	v_fmac_f32_e32 v39, v28, v39
	v_div_scale_f32 v28, vcc, 1.0, v3, 1.0
	v_mul_f32_e32 v29, v28, v39
	v_fma_f32 v36, -v24, v29, v28
	v_fmac_f32_e32 v29, v36, v39
	v_fma_f32 v24, -v24, v29, v28
	v_div_fmas_f32 v24, v24, v39, v29
	v_div_fixup_f32 v3, v24, v3, 1.0
	v_mul_f32_e32 v20, v20, v3
	v_mul_f32_e32 v20, v20, v34
	v_mov_b32_e32 v24, v181
	v_add_u32_e32 v28, 18, v2
	v_cvt_pk_fp8_f32 v24, v20, 0
	v_ashrrev_i32_e32 v29, 31, v28
	v_lshlrev_b64 v[28:29], 10, v[28:29]
	v_lshl_add_u64 v[28:29], v[4:5], 0, v[28:29]
	v_mul_f32_e32 v20, v25, v3
	global_store_byte v[28:29], v24, off
	v_mul_f32_e32 v20, v20, v32
	v_mov_b32_e32 v24, v181
	v_cvt_pk_fp8_f32 v24, v20, 0
	v_mul_f32_e32 v20, v33, v3
	v_mul_f32_e32 v20, v20, v31
	v_mov_b32_e32 v25, v181
	v_cvt_pk_fp8_f32 v25, v20, 0
	v_fmamk_f32 v20, v57, 0x3c000000, v184
	v_mul_f32_e32 v33, 0x4f800000, v20
	v_cmp_gt_f32_e32 vcc, s55, v20
	v_mul_f32_e32 v3, v40, v3
	v_mul_f32_e32 v3, v3, v30
	v_cndmask_b32_e32 v20, v20, v33, vcc
	v_sqrt_f32_e32 v33, v20
	v_mov_b32_e32 v36, v181
	v_cvt_pk_fp8_f32 v36, v3, 0
	global_store_byte v[28:29], v24, off offset:32
	global_store_byte v[28:29], v25, off offset:64
	global_store_byte v[28:29], v36, off offset:96
	v_add_u32_e32 v3, -1, v33
	v_fma_f32 v37, -v3, v33, v20
	v_cmp_ge_f32_e64 s[6:7], 0, v37
	v_add_u32_e32 v37, 1, v33
	s_nop 0
	v_cndmask_b32_e64 v3, v33, v3, s[6:7]
	v_fma_f32 v33, -v37, v33, v20
	v_cmp_lt_f32_e64 s[6:7], 0, v33
	s_nop 1
	v_cndmask_b32_e64 v3, v3, v37, s[6:7]
	v_mul_f32_e32 v33, 0x37800000, v3
	v_cndmask_b32_e32 v3, v3, v33, vcc
	v_cmp_class_f32_e32 vcc, v20, v185
	s_nop 1
	v_cndmask_b32_e32 v3, v3, v20, vcc
	v_div_scale_f32 v20, s[6:7], v3, v3, 1.0
	v_rcp_f32_e32 v33, v20
	s_nop 0
	v_fma_f32 v24, -v20, v33, 1.0
	v_fmac_f32_e32 v33, v24, v33
	v_div_scale_f32 v24, vcc, 1.0, v3, 1.0
	v_mul_f32_e32 v25, v24, v33
	v_fma_f32 v28, -v20, v25, v24
	v_fmac_f32_e32 v25, v28, v33
	v_fma_f32 v20, -v20, v25, v24
	v_div_fmas_f32 v20, v20, v33, v25
	v_div_fixup_f32 v3, v20, v3, 1.0
	v_mul_f32_e32 v16, v16, v3
	v_mul_f32_e32 v16, v16, v34
	v_mov_b32_e32 v20, v181
	v_add_u32_e32 v24, 19, v2
	v_cvt_pk_fp8_f32 v20, v16, 0
	v_ashrrev_i32_e32 v25, 31, v24
	v_lshlrev_b64 v[24:25], 10, v[24:25]
	v_lshl_add_u64 v[24:25], v[4:5], 0, v[24:25]
	v_mul_f32_e32 v16, v21, v3
	global_store_byte v[24:25], v20, off
	v_mul_f32_e32 v16, v16, v32
	v_mov_b32_e32 v20, v181
	v_cvt_pk_fp8_f32 v20, v16, 0
	v_mul_f32_e32 v16, v26, v3
	v_mul_f32_e32 v16, v16, v31
	v_mov_b32_e32 v21, v181
	v_cvt_pk_fp8_f32 v21, v16, 0
	v_fmamk_f32 v16, v52, 0x3c000000, v184
	v_mul_f32_e32 v26, 0x4f800000, v16
	v_cmp_gt_f32_e32 vcc, s55, v16
	v_mul_f32_e32 v3, v35, v3
	v_mul_f32_e32 v3, v3, v30
	v_cndmask_b32_e32 v16, v16, v26, vcc
	v_sqrt_f32_e32 v26, v16
	v_mov_b32_e32 v28, v181
	v_cvt_pk_fp8_f32 v28, v3, 0
	global_store_byte v[24:25], v20, off offset:32
	global_store_byte v[24:25], v21, off offset:64
	global_store_byte v[24:25], v28, off offset:96
	v_add_u32_e32 v3, -1, v26
	v_fma_f32 v29, -v3, v26, v16
	v_cmp_ge_f32_e64 s[6:7], 0, v29
	v_add_u32_e32 v29, 1, v26
	s_nop 0
	v_cndmask_b32_e64 v3, v26, v3, s[6:7]
	v_fma_f32 v26, -v29, v26, v16
	v_cmp_lt_f32_e64 s[6:7], 0, v26
	s_nop 1
	v_cndmask_b32_e64 v3, v3, v29, s[6:7]
	v_mul_f32_e32 v26, 0x37800000, v3
	v_cndmask_b32_e32 v3, v3, v26, vcc
	v_cmp_class_f32_e32 vcc, v16, v185
	s_nop 1
	v_cndmask_b32_e32 v3, v3, v16, vcc
	v_div_scale_f32 v16, s[6:7], v3, v3, 1.0
	v_rcp_f32_e32 v26, v16
	s_nop 0
	v_fma_f32 v20, -v16, v26, 1.0
	v_fmac_f32_e32 v26, v20, v26
	v_div_scale_f32 v20, vcc, 1.0, v3, 1.0
	v_mul_f32_e32 v21, v20, v26
	v_fma_f32 v24, -v16, v21, v20
	v_fmac_f32_e32 v21, v24, v26
	v_fma_f32 v16, -v16, v21, v20
	v_div_fmas_f32 v16, v16, v26, v21
	v_div_fixup_f32 v3, v16, v3, 1.0
	v_mul_f32_e32 v12, v12, v3
	v_mul_f32_e32 v12, v12, v34
	v_mov_b32_e32 v16, v181
	v_add_u32_e32 v20, 24, v2
	v_cvt_pk_fp8_f32 v16, v12, 0
	v_ashrrev_i32_e32 v21, 31, v20
	v_lshlrev_b64 v[20:21], 10, v[20:21]
	v_lshl_add_u64 v[20:21], v[4:5], 0, v[20:21]
	v_mul_f32_e32 v12, v17, v3
	global_store_byte v[20:21], v16, off
	v_mul_f32_e32 v12, v12, v32
	v_mov_b32_e32 v16, v181
	v_cvt_pk_fp8_f32 v16, v12, 0
	v_mul_f32_e32 v12, v22, v3
	v_mul_f32_e32 v12, v12, v31
	v_mov_b32_e32 v17, v181
	v_cvt_pk_fp8_f32 v17, v12, 0
	v_fmamk_f32 v12, v48, 0x3c000000, v184
	v_mul_f32_e32 v22, 0x4f800000, v12
	v_cmp_gt_f32_e32 vcc, s55, v12
	v_mul_f32_e32 v3, v27, v3
	v_mul_f32_e32 v3, v3, v30
	v_cndmask_b32_e32 v12, v12, v22, vcc
	v_sqrt_f32_e32 v22, v12
	v_mov_b32_e32 v24, v181
	v_cvt_pk_fp8_f32 v24, v3, 0
	global_store_byte v[20:21], v16, off offset:32
	global_store_byte v[20:21], v17, off offset:64
	global_store_byte v[20:21], v24, off offset:96
	v_add_u32_e32 v3, -1, v22
	v_fma_f32 v25, -v3, v22, v12
	v_cmp_ge_f32_e64 s[6:7], 0, v25
	v_add_u32_e32 v25, 1, v22
	s_nop 0
	v_cndmask_b32_e64 v3, v22, v3, s[6:7]
	v_fma_f32 v22, -v25, v22, v12
	v_cmp_lt_f32_e64 s[6:7], 0, v22
	s_nop 1
	v_cndmask_b32_e64 v3, v3, v25, s[6:7]
	v_mul_f32_e32 v22, 0x37800000, v3
	v_cndmask_b32_e32 v3, v3, v22, vcc
	v_cmp_class_f32_e32 vcc, v12, v185
	s_nop 1
	v_cndmask_b32_e32 v3, v3, v12, vcc
	v_div_scale_f32 v12, s[6:7], v3, v3, 1.0
	v_rcp_f32_e32 v22, v12
	s_nop 0
	v_fma_f32 v16, -v12, v22, 1.0
	v_fmac_f32_e32 v22, v16, v22
	v_div_scale_f32 v16, vcc, 1.0, v3, 1.0
	v_mul_f32_e32 v17, v16, v22
	v_fma_f32 v20, -v12, v17, v16
	v_fmac_f32_e32 v17, v20, v22
	v_fma_f32 v12, -v12, v17, v16
	v_div_fmas_f32 v12, v12, v22, v17
	v_div_fixup_f32 v3, v12, v3, 1.0
	v_mul_f32_e32 v9, v9, v3
	v_mul_f32_e32 v9, v9, v34
	v_mov_b32_e32 v12, v181
	v_add_u32_e32 v16, 25, v2
	v_cvt_pk_fp8_f32 v12, v9, 0
	v_ashrrev_i32_e32 v17, 31, v16
	v_lshlrev_b64 v[16:17], 10, v[16:17]
	v_lshl_add_u64 v[16:17], v[4:5], 0, v[16:17]
	v_mul_f32_e32 v9, v13, v3
	global_store_byte v[16:17], v12, off
	v_mul_f32_e32 v9, v9, v32
	v_mov_b32_e32 v12, v181
	v_cvt_pk_fp8_f32 v12, v9, 0
	v_mul_f32_e32 v9, v18, v3
	v_mul_f32_e32 v9, v9, v31
	v_mov_b32_e32 v13, v181
	v_cvt_pk_fp8_f32 v13, v9, 0
	v_fmamk_f32 v9, v43, 0x3c000000, v184
	v_mul_f32_e32 v18, 0x4f800000, v9
	v_cmp_gt_f32_e32 vcc, s55, v9
	v_mul_f32_e32 v3, v23, v3
	v_mul_f32_e32 v3, v3, v30
	v_cndmask_b32_e32 v9, v9, v18, vcc
	v_sqrt_f32_e32 v18, v9
	v_mov_b32_e32 v20, v181
	v_cvt_pk_fp8_f32 v20, v3, 0
	global_store_byte v[16:17], v12, off offset:32
	global_store_byte v[16:17], v13, off offset:64
	global_store_byte v[16:17], v20, off offset:96
	v_add_u32_e32 v3, -1, v18
	v_fma_f32 v21, -v3, v18, v9
	v_cmp_ge_f32_e64 s[6:7], 0, v21
	v_add_u32_e32 v21, 1, v18
	s_nop 0
	v_cndmask_b32_e64 v3, v18, v3, s[6:7]
	v_fma_f32 v18, -v21, v18, v9
	v_cmp_lt_f32_e64 s[6:7], 0, v18
	s_nop 1
	v_cndmask_b32_e64 v3, v3, v21, s[6:7]
	v_mul_f32_e32 v18, 0x37800000, v3
	v_cndmask_b32_e32 v3, v3, v18, vcc
	v_cmp_class_f32_e32 vcc, v9, v185
	s_nop 1
	v_cndmask_b32_e32 v3, v3, v9, vcc
	v_div_scale_f32 v9, s[6:7], v3, v3, 1.0
	v_rcp_f32_e32 v18, v9
	s_nop 0
	v_fma_f32 v12, -v9, v18, 1.0
	v_fmac_f32_e32 v18, v12, v18
	v_div_scale_f32 v12, vcc, 1.0, v3, 1.0
	v_mul_f32_e32 v13, v12, v18
	v_fma_f32 v16, -v9, v13, v12
	v_fmac_f32_e32 v13, v16, v18
	v_fma_f32 v9, -v9, v13, v12
	v_div_fmas_f32 v9, v9, v18, v13
	v_div_fixup_f32 v3, v9, v3, 1.0
	v_mul_f32_e32 v7, v7, v3
	v_mul_f32_e32 v7, v7, v34
	v_mov_b32_e32 v9, v181
	v_add_u32_e32 v12, 26, v2
	v_cvt_pk_fp8_f32 v9, v7, 0
	v_ashrrev_i32_e32 v13, 31, v12
	v_lshlrev_b64 v[12:13], 10, v[12:13]
	v_lshl_add_u64 v[12:13], v[4:5], 0, v[12:13]
	v_mul_f32_e32 v7, v10, v3
	global_store_byte v[12:13], v9, off
	v_mul_f32_e32 v7, v7, v32
	v_mov_b32_e32 v9, v181
	v_cvt_pk_fp8_f32 v9, v7, 0
	v_mul_f32_e32 v7, v14, v3
	v_mul_f32_e32 v7, v7, v31
	v_mov_b32_e32 v10, v181
	v_cvt_pk_fp8_f32 v10, v7, 0
	v_fmamk_f32 v7, v38, 0x3c000000, v184
	v_mul_f32_e32 v14, 0x4f800000, v7
	v_cmp_gt_f32_e32 vcc, s55, v7
	v_mul_f32_e32 v3, v19, v3
	v_mul_f32_e32 v3, v3, v30
	v_cndmask_b32_e32 v7, v7, v14, vcc
	v_sqrt_f32_e32 v14, v7
	v_mov_b32_e32 v16, v181
	v_cvt_pk_fp8_f32 v16, v3, 0
	global_store_byte v[12:13], v9, off offset:32
	global_store_byte v[12:13], v10, off offset:64
	global_store_byte v[12:13], v16, off offset:96
	v_add_u32_e32 v3, -1, v14
	v_fma_f32 v17, -v3, v14, v7
	v_cmp_ge_f32_e64 s[6:7], 0, v17
	v_add_u32_e32 v17, 1, v14
	v_add_u32_e32 v2, 27, v2
	v_cndmask_b32_e64 v3, v14, v3, s[6:7]
	v_fma_f32 v14, -v17, v14, v7
	v_cmp_lt_f32_e64 s[6:7], 0, v14
	s_nop 1
	v_cndmask_b32_e64 v3, v3, v17, s[6:7]
	v_mul_f32_e32 v14, 0x37800000, v3
	v_cndmask_b32_e32 v3, v3, v14, vcc
	v_cmp_class_f32_e32 vcc, v7, v185
	s_nop 1
	v_cndmask_b32_e32 v3, v3, v7, vcc
	v_div_scale_f32 v7, s[6:7], v3, v3, 1.0
	v_rcp_f32_e32 v14, v7
	s_nop 0
	v_fma_f32 v9, -v7, v14, 1.0
	v_fmac_f32_e32 v14, v9, v14
	v_div_scale_f32 v9, vcc, 1.0, v3, 1.0
	v_mul_f32_e32 v10, v9, v14
	v_fma_f32 v12, -v7, v10, v9
	v_fmac_f32_e32 v10, v12, v14
	v_fma_f32 v7, -v7, v10, v9
	v_div_fmas_f32 v7, v7, v14, v10
	v_div_fixup_f32 v7, v7, v3, 1.0
	v_ashrrev_i32_e32 v3, 31, v2
	v_mul_f32_e32 v6, v6, v7
	v_lshlrev_b64 v[2:3], 10, v[2:3]
	v_mul_f32_e32 v6, v34, v6
	v_mov_b32_e32 v9, v181
	v_lshl_add_u64 v[2:3], v[4:5], 0, v[2:3]
	v_mul_f32_e32 v4, v11, v7
	v_cvt_pk_fp8_f32 v9, v6, 0
	v_mul_f32_e32 v6, v8, v7
	v_mul_f32_e32 v4, v31, v4
	v_mov_b32_e32 v5, v181
	v_mul_f32_e32 v6, v32, v6
	v_mov_b32_e32 v8, v181
	v_cvt_pk_fp8_f32 v5, v4, 0
	v_mul_f32_e32 v4, v15, v7
	v_cvt_pk_fp8_f32 v8, v6, 0
	v_mul_f32_e32 v4, v30, v4
	v_mov_b32_e32 v6, v181
	v_cvt_pk_fp8_f32 v6, v4, 0
	global_store_byte v[2:3], v9, off
	global_store_byte v[2:3], v8, off offset:32
	global_store_byte v[2:3], v5, off offset:64
	global_store_byte v[2:3], v6, off offset:96
	s_cbranch_scc0 .LBB0_1427

.LBB0_1211:
	s_and_b32 s37, s95, 0xffffffc0
	v_lshlrev_b32_e32 v6, 2, v5
	v_lshlrev_b32_e32 v3, 6, v4
	v_and_b32_e32 v6, 48, v6
	s_cmp_lg_u32 0, -1
	v_bitop3_b32 v194, v6, v3, v2 bitop3:0xde
	s_cselect_b32 s38, 0, 0
	v_lshlrev_b32_e32 v2, 3, v5
	v_and_b32_e32 v193, 63, v5
	v_add_u32_e32 v183, s38, v194
	s_addk_i32 s38, 0x4000
	v_and_b32_e32 v2, 32, v2
	s_lshl_b32 s37, s37, 2
	v_add_u32_e32 v188, s38, v194
	v_sub_u32_e32 v195, 16, v2
	v_lshrrev_b32_e32 v2, 5, v193
	s_add_i32 s78, s37, 0
	v_add_u32_e32 v190, v183, v195
	s_mov_b64 s[38:39], -1
	s_and_b64 vcc, exec, s[6:7]
	v_add_u32_e32 v189, v188, v195
	v_cmp_gt_u32_e64 s[6:7], 32, v193
	v_lshlrev_b32_e32 v186, 4, v2
	v_lshl_add_u32 v187, v4, 2, s78
	v_and_b32_e32 v248, 31, v193
	v_mov_b32_e32 v249, 0x38383838
	v_cmp_eq_u32_e64 s[100:101], 0, v248
	v_lshrrev_b32_e32 v250, 4, v193
	s_nop 0
	v_cndmask_b32_e64 v146, 0, v249, s[100:101]
	v_cmp_eq_u32_e64 s[100:101], 17, v248
	v_and_b32_e32 v248, 15, v193
	v_lshlrev_b32_e32 v248, 6, v248
	v_cndmask_b32_e64 v146, v146, v249, s[100:101]
	v_lshl_add_u32 v250, v250, 4, v248
	v_add_u32_e32 v250, s78, v250
	v_mov_b32_e32 v147, v146
	v_mov_b32_e32 v148, v146
	v_mov_b32_e32 v149, v146
	v_mov_b32_e32 v150, v146
	v_mov_b32_e32 v151, v146
	v_mov_b32_e32 v152, v146
	v_mov_b32_e32 v153, v146
	s_cbranch_vccz .LBB0_1264
	ds_read_b128 v[18:21], v183 offset:0
	ds_read_b128 v[22:25], v190 offset:0
	ds_read_b128 v[34:37], v183 offset:0x800
	ds_read_b128 v[38:41], v190 offset:0x800
	s_waitcnt lgkmcnt(0)
	s_waitcnt vmcnt(0)
	v_mfma_f32_32x32x64_f8f6f4 v[18:33], v[18:25], v[154:161], 0
	s_mov_b32 s37, s36
	s_mov_b32 s38, s36
	s_mov_b32 s39, s36
	s_mov_b32 s40, s36
	s_mov_b32 s41, s36
	s_mov_b32 s42, s36
	s_mov_b32 s43, s36
	s_mov_b32 s44, s36
	s_mov_b32 s45, s36
	s_mov_b32 s46, s36
	s_mov_b32 s47, s36
	s_mov_b32 s48, s36
	s_mov_b32 s49, s36
	s_mov_b32 s50, s36
	s_mov_b32 s51, s36
	v_mov_b64_e32 v[2:3], s[36:37]
	v_mov_b64_e32 v[4:5], s[38:39]
	v_mov_b64_e32 v[6:7], s[40:41]
	v_mov_b64_e32 v[8:9], s[42:43]
	v_mov_b64_e32 v[10:11], s[44:45]
	v_mov_b64_e32 v[12:13], s[46:47]
	v_mov_b64_e32 v[14:15], s[48:49]
	v_mov_b64_e32 v[16:17], s[50:51]
	v_max_f32_e32 v42, v19, v19
	v_max_f32_e32 v43, v18, v18
	v_max_f32_e32 v42, v43, v42
	v_max3_f32 v42, v42, v20, v21
	v_max3_f32 v42, v42, v22, v23
	v_max3_f32 v42, v42, v24, v25
	v_max3_f32 v42, v42, v26, v27
	v_max3_f32 v42, v42, v28, v29
	v_max3_f32 v50, v42, v30, v31
	v_mfma_f32_32x32x64_f8f6f4 v[34:49], v[34:41], v[154:161], 0
	v_max3_f32 v50, v50, v32, v33
	s_cmp_lg_u32 0, -1
	s_cselect_b32 s37, 0, 0
	v_mov_b32_e32 v130, v181
	v_mov_b32_e32 v131, v181
	s_add_i32 s38, s37, 0x1000
	s_waitcnt vmcnt(0) lgkmcnt(0)
	s_barrier
	v_add_u32_e32 v207, s38, v194
	v_add_u32_e32 v209, v207, v195
	s_nop 11
	v_max3_f32 v50, v50, v34, v35
	v_max3_f32 v50, v50, v36, v37
	v_max3_f32 v50, v50, v38, v39
	v_max3_f32 v50, v50, v40, v41
	v_max3_f32 v50, v50, v42, v43
	v_max3_f32 v50, v50, v44, v45
	v_max3_f32 v50, v50, v46, v47
	v_max3_f32 v50, v50, v48, v49
	v_mov_b32_e32 v51, v50
	s_nop 1
	v_permlane32_swap_b32_e32 v50, v51
	v_max_f32_e32 v51, v51, v51
	v_max_f32_e32 v50, v50, v50
	v_max_f32_e32 v50, v50, v51
	s_cmp_eq_u32 s98, 0
	s_cselect_b32 s100, 0x3f800000, 0xc0600000
	v_add_f32_e32 v198, s100, v50
	v_sub_f32_e32 v18, v18, v198
	v_sub_f32_e32 v19, v19, v198
	v_sub_f32_e32 v22, v22, v198
	v_sub_f32_e32 v23, v23, v198
	v_exp_f32_e32 v50, v18
	v_exp_f32_e32 v51, v19
	v_exp_f32_e32 v54, v22
	v_exp_f32_e32 v55, v23
	v_xor_b32_e32 v82, 0x80000000, v198
	v_sub_f32_e32 v20, v20, v198
	v_sub_f32_e32 v21, v21, v198
	v_sub_f32_e32 v24, v24, v198
	v_sub_f32_e32 v25, v25, v198
	v_mov_b32_e32 v83, v82
	v_mov_b32_e32 v84, v82
	v_mov_b32_e32 v85, v82
	v_mov_b32_e32 v86, v82
	v_mov_b32_e32 v87, v82
	v_mov_b32_e32 v88, v82
	v_mov_b32_e32 v89, v82
	v_mov_b32_e32 v90, v82
	v_mov_b32_e32 v91, v82
	v_mov_b32_e32 v92, v82
	v_mov_b32_e32 v93, v82
	v_mov_b32_e32 v94, v82
	v_mov_b32_e32 v95, v82
	v_mov_b32_e32 v96, v82
	v_mov_b32_e32 v97, v82
	v_exp_f32_e32 v52, v20
	v_exp_f32_e32 v53, v21
	v_exp_f32_e32 v56, v24
	v_exp_f32_e32 v57, v25
	v_cvt_pk_fp8_f32 v130, v50, v51
	v_cvt_pk_fp8_f32 v131, v54, v55
	ds_read_b128 v[18:21], v207 offset:0
	v_sub_f32_e32 v26, v26, v198
	v_sub_f32_e32 v27, v27, v198
	v_sub_f32_e32 v28, v28, v198
	v_sub_f32_e32 v29, v29, v198
	ds_read_b128 v[22:25], v209 offset:0
	v_sub_f32_e32 v34, v34, v198
	v_sub_f32_e32 v35, v35, v198
	v_sub_f32_e32 v36, v36, v198
	v_sub_f32_e32 v37, v37, v198
	v_sub_f32_e32 v38, v38, v198
	v_sub_f32_e32 v39, v39, v198
	v_sub_f32_e32 v40, v40, v198
	v_sub_f32_e32 v41, v41, v198
	v_sub_f32_e32 v42, v42, v198
	v_sub_f32_e32 v43, v43, v198
	v_sub_f32_e32 v44, v44, v198
	v_sub_f32_e32 v45, v45, v198
	v_sub_f32_e32 v30, v30, v198
	v_sub_f32_e32 v46, v46, v198
	v_sub_f32_e32 v31, v31, v198
	v_sub_f32_e32 v47, v47, v198
	v_sub_f32_e32 v32, v32, v198
	v_sub_f32_e32 v48, v48, v198
	v_sub_f32_e32 v33, v33, v198
	v_sub_f32_e32 v49, v49, v198
	v_exp_f32_e32 v58, v26
	v_exp_f32_e32 v59, v27
	v_exp_f32_e32 v60, v28
	v_exp_f32_e32 v61, v29
	ds_read_b128 v[26:29], v207 offset:0x800
	v_exp_f32_e32 v34, v34
	v_exp_f32_e32 v35, v35
	v_exp_f32_e32 v36, v36
	v_exp_f32_e32 v37, v37
	v_exp_f32_e32 v38, v38
	v_exp_f32_e32 v39, v39
	v_exp_f32_e32 v40, v40
	v_exp_f32_e32 v41, v41
	v_exp_f32_e32 v42, v42
	v_exp_f32_e32 v43, v43
	v_exp_f32_e32 v44, v44
	v_exp_f32_e32 v45, v45
	v_exp_f32_e32 v62, v30
	v_exp_f32_e32 v46, v46
	v_exp_f32_e32 v63, v31
	v_exp_f32_e32 v47, v47
	v_exp_f32_e32 v64, v32
	v_exp_f32_e32 v48, v48
	v_exp_f32_e32 v65, v33
	v_exp_f32_e32 v49, v49
	ds_read_b128 v[30:33], v209 offset:0x800
	v_cvt_pk_fp8_f32 v130, v52, v53 op_sel:[0,0,1]
	v_cvt_pk_fp8_f32 v131, v56, v57 op_sel:[0,0,1]
	s_waitcnt lgkmcnt(2)
	v_mfma_f32_32x32x64_f8f6f4 v[98:113], v[18:25], v[154:161], v[82:97]
	v_mov_b32_e32 v132, v181
	v_mov_b32_e32 v133, v181
	v_cvt_pk_fp8_f32 v132, v58, v59
	v_cvt_pk_fp8_f32 v133, v62, v63
	ds_read_b128 v[170:173], v188 offset:0
	ds_read_b128 v[174:177], v189 offset:0
	v_cvt_pk_fp8_f32 v132, v60, v61 op_sel:[0,0,1]
	v_cvt_pk_fp8_f32 v133, v64, v65 op_sel:[0,0,1]
	s_waitcnt lgkmcnt(2)
	v_mov_b64_e32 v[128:129], v[96:97]
	v_mov_b64_e32 v[126:127], v[94:95]
	v_mov_b64_e32 v[124:125], v[92:93]
	v_mov_b64_e32 v[122:123], v[90:91]
	v_mov_b64_e32 v[120:121], v[88:89]
	v_mov_b64_e32 v[118:119], v[86:87]
	v_mov_b64_e32 v[116:117], v[84:85]
	v_mov_b64_e32 v[114:115], v[82:83]
	v_mov_b32_e32 v134, v181
	v_mov_b32_e32 v135, v181
	v_mfma_f32_32x32x64_f8f6f4 v[114:129], v[26:33], v[154:161], v[114:129]
	v_mov_b32_e32 v136, v181
	v_mov_b32_e32 v137, v181
	v_cvt_pk_fp8_f32 v134, v34, v35
	v_cvt_pk_fp8_f32 v135, v38, v39
	v_cvt_pk_fp8_f32 v136, v42, v43
	v_cvt_pk_fp8_f32 v137, v46, v47
	v_cvt_pk_fp8_f32 v134, v36, v37 op_sel:[0,0,1]
	v_cvt_pk_fp8_f32 v135, v40, v41 op_sel:[0,0,1]
	v_cvt_pk_fp8_f32 v136, v44, v45 op_sel:[0,0,1]
	v_cvt_pk_fp8_f32 v137, v48, v49 op_sel:[0,0,1]
	s_nop 0
	ds_read_b128 v[138:141], v188 offset:0x800
	ds_read_b128 v[142:145], v189 offset:0x800
	s_nop 0
	v_mfma_f32_16x16x128_f8f6f4 v[18:21], v[130:137], v[146:153], 0
	s_add_i32 s38, s37, 0x2000
	v_add_u32_e32 v205, s38, v194
	s_add_i32 s38, s37, 0x6000
	v_add_u32_e32 v203, s38, v194
	s_add_i32 s38, s37, 0x3000
	s_waitcnt vmcnt(0) lgkmcnt(0)
	s_barrier
	v_add_u32_e32 v201, s38, v194
	s_add_i32 s38, s37, 0x8000
	s_add_i32 s37, s37, 0xa000
	v_add_u32_e32 v199, s38, v194
	v_add_u32_e32 v196, s37, v194
	v_mov_b64_e32 v[48:49], v[16:17]
	v_mov_b64_e32 v[64:65], v[16:17]
	v_mov_b64_e32 v[80:81], v[16:17]
	v_add_u32_e32 v206, v205, v195
	v_add_u32_e32 v204, v203, v195
	v_add_u32_e32 v202, v201, v195
	v_add_u32_e32 v200, v199, v195
	v_add_u32_e32 v197, v196, v195
	s_mov_b32 s37, -2
	v_mov_b64_e32 v[46:47], v[14:15]
	v_mov_b64_e32 v[44:45], v[12:13]
	v_mov_b64_e32 v[42:43], v[10:11]
	v_mov_b64_e32 v[40:41], v[8:9]
	v_mov_b64_e32 v[38:39], v[6:7]
	v_mov_b64_e32 v[36:37], v[4:5]
	v_mov_b64_e32 v[34:35], v[2:3]
	v_mov_b64_e32 v[62:63], v[14:15]
	v_mov_b64_e32 v[60:61], v[12:13]
	v_mov_b64_e32 v[58:59], v[10:11]
	v_mov_b64_e32 v[56:57], v[8:9]
	v_mov_b64_e32 v[54:55], v[6:7]
	v_mov_b64_e32 v[52:53], v[4:5]
	v_mov_b64_e32 v[50:51], v[2:3]
	v_mov_b64_e32 v[78:79], v[14:15]
	v_mov_b64_e32 v[76:77], v[12:13]
	v_mov_b64_e32 v[74:75], v[10:11]
	v_mov_b64_e32 v[72:73], v[8:9]
	v_mov_b64_e32 v[70:71], v[6:7]
	v_mov_b64_e32 v[68:69], v[4:5]
	v_mov_b64_e32 v[66:67], v[2:3]
	s_branch .LBB0_1215

.LBB0_1215:
	s_waitcnt lgkmcnt(2)
	v_mfma_f32_32x32x64_f8f6f4 v[2:17], v[130:137], v[170:177], v[2:17]
	ds_read_b128 v[162:165], v188 offset:0x1000
	ds_read_b128 v[166:169], v189 offset:0x1000
	s_mov_b64 s[38:39], 0
	s_cmp_eq_u32 s98, 0
	s_cbranch_scc1 .LBB0_1218
	v_max3_f32 v170, v98, v99, v100
	v_max3_f32 v170, v170, v101, v102
	v_max3_f32 v170, v170, v103, v104
	v_max3_f32 v170, v170, v105, v106
	v_max3_f32 v170, v170, v107, v108
	v_max3_f32 v170, v170, v109, v110
	v_max3_f32 v170, v170, v111, v112
	v_max_f32 v170, v170, v113
	s_nop 0
	v_max3_f32 v170, v170, v114, v115
	v_max3_f32 v170, v170, v116, v117
	v_max3_f32 v170, v170, v118, v119
	v_max3_f32 v170, v170, v120, v121
	v_max3_f32 v170, v170, v122, v123
	v_max3_f32 v170, v170, v124, v125
	v_max3_f32 v170, v170, v126, v127
	v_max3_f32 v170, v170, v128, v129
	v_mov_b32 v171, v170
	s_nop 1
	v_permlane32_swap_b32 v170, v171
	v_max_f32 v170, v170, v171
	s_nop 0
	v_cmp_ge_f32_e32 vcc, s54, v170
	s_cmp_lg_u64 vcc, exec
	s_cselect_b64 s[38:39], -1, 0
	s_cmp_eq_u64 vcc, exec
	s_cbranch_scc1 .LBB0_1217
	s_nop 1
	v_add_f32_e32 v82, 0xc0c00000, v170
	v_max_f32_e32 v82, 0, v82
	v_exp_f32_e64 v170, -v82
	v_add_f32_e32 v198, v198, v82
	v_sub_f32_e32 v98, v98, v82
	v_sub_f32_e32 v114, v114, v82
	v_sub_f32_e32 v99, v99, v82
	v_sub_f32_e32 v115, v115, v82
	v_sub_f32_e32 v100, v100, v82
	v_sub_f32_e32 v116, v116, v82
	v_sub_f32_e32 v101, v101, v82
	v_sub_f32_e32 v117, v117, v82
	v_sub_f32_e32 v102, v102, v82
	v_sub_f32_e32 v118, v118, v82
	v_sub_f32_e32 v103, v103, v82
	v_sub_f32_e32 v119, v119, v82
	v_sub_f32_e32 v104, v104, v82
	v_sub_f32_e32 v120, v120, v82
	v_sub_f32_e32 v105, v105, v82
	v_sub_f32_e32 v121, v121, v82
	v_sub_f32_e32 v106, v106, v82
	v_sub_f32_e32 v122, v122, v82
	v_sub_f32_e32 v107, v107, v82
	v_sub_f32_e32 v123, v123, v82
	v_sub_f32_e32 v108, v108, v82
	v_sub_f32_e32 v124, v124, v82
	v_sub_f32_e32 v109, v109, v82
	v_sub_f32_e32 v125, v125, v82
	v_sub_f32_e32 v110, v110, v82
	v_sub_f32_e32 v126, v126, v82
	v_sub_f32_e32 v111, v111, v82
	v_sub_f32_e32 v127, v127, v82
	v_sub_f32_e32 v112, v112, v82
	v_sub_f32_e32 v128, v128, v82
	v_sub_f32_e32 v113, v113, v82
	v_sub_f32_e32 v129, v129, v82
	v_xor_b32_e32 v82, 0x80000000, v198
	v_mov_b32_e32 v83, v82
	v_mov_b32_e32 v84, v82
	v_mov_b32_e32 v85, v82
	v_mov_b32_e32 v86, v82
	v_mov_b32_e32 v87, v82
	v_mov_b32_e32 v88, v82
	v_mov_b32_e32 v89, v82
	v_mov_b32_e32 v90, v82
	v_mov_b32_e32 v91, v82
	v_mov_b32_e32 v92, v82
	v_mov_b32_e32 v93, v82
	v_mov_b32_e32 v94, v82
	v_mov_b32_e32 v95, v82
	v_mov_b32_e32 v96, v82
	v_mov_b32_e32 v97, v82
	s_branch .LBB0_1218

.LBB0_1222:
	v_cvt_pk_fp8_f32 v130, v98, v99
	v_cvt_pk_fp8_f32 v131, v102, v103
	ds_read_b128 v[138:141], v205 offset:0
	ds_read_b128 v[142:145], v206 offset:0
	ds_read_b128 v[170:173], v205 offset:0x800
	ds_read_b128 v[174:177], v206 offset:0x800
	v_cvt_pk_fp8_f32 v130, v100, v101 op_sel:[0,0,1]
	v_cvt_pk_fp8_f32 v131, v104, v105 op_sel:[0,0,1]
	s_waitcnt lgkmcnt(2)
	v_cvt_pk_fp8_f32 v132, v106, v107
	v_cvt_pk_fp8_f32 v133, v110, v111
	ds_read_b128 v[210:213], v203 offset:0
	ds_read_b128 v[214:217], v204 offset:0
	v_cvt_pk_fp8_f32 v132, v108, v109 op_sel:[0,0,1]
	v_cvt_pk_fp8_f32 v133, v112, v113 op_sel:[0,0,1]
	v_mfma_f32_32x32x64_f8f6f4 v[98:113], v[138:145], v[154:161], v[82:97]
	s_waitcnt lgkmcnt(2)
	v_cvt_pk_fp8_f32 v134, v114, v115
	v_cvt_pk_fp8_f32 v135, v118, v119
	v_cvt_pk_fp8_f32 v136, v122, v123
	v_cvt_pk_fp8_f32 v137, v126, v127
	v_cvt_pk_fp8_f32 v134, v116, v117 op_sel:[0,0,1]
	v_cvt_pk_fp8_f32 v135, v120, v121 op_sel:[0,0,1]
	v_cvt_pk_fp8_f32 v136, v124, v125 op_sel:[0,0,1]
	v_cvt_pk_fp8_f32 v137, v128, v129 op_sel:[0,0,1]
	v_mfma_f32_32x32x64_f8f6f4 v[114:129], v[170:177], v[154:161], v[82:97]
	ds_read_b128 v[162:165], v203 offset:0x800
	ds_read_b128 v[166:169], v204 offset:0x800
	s_nop 0
	v_mfma_f32_16x16x128_f8f6f4 v[18:21], v[130:137], v[146:153], v[18:21]
	s_waitcnt vmcnt(0) lgkmcnt(0)
	s_barrier
	s_waitcnt lgkmcnt(2)
	v_mfma_f32_32x32x64_f8f6f4 v[2:17], v[130:137], v[210:217], v[2:17]
	ds_read_b128 v[138:141], v203 offset:0x1000
	ds_read_b128 v[142:145], v204 offset:0x1000
	s_mov_b64 s[38:39], 0
	s_cmp_eq_u32 s98, 0
	s_cbranch_scc1 .LBB0_1225
	v_max3_f32 v170, v98, v99, v100
	v_max3_f32 v170, v170, v101, v102
	v_max3_f32 v170, v170, v103, v104
	v_max3_f32 v170, v170, v105, v106
	v_max3_f32 v170, v170, v107, v108
	v_max3_f32 v170, v170, v109, v110
	v_max3_f32 v170, v170, v111, v112
	v_max_f32 v170, v170, v113
	s_nop 0
	v_max3_f32 v170, v170, v114, v115
	v_max3_f32 v170, v170, v116, v117
	v_max3_f32 v170, v170, v118, v119
	v_max3_f32 v170, v170, v120, v121
	v_max3_f32 v170, v170, v122, v123
	v_max3_f32 v170, v170, v124, v125
	v_max3_f32 v170, v170, v126, v127
	v_max3_f32 v170, v170, v128, v129
	v_mov_b32 v171, v170
	s_nop 1
	v_permlane32_swap_b32 v170, v171
	v_max_f32 v170, v170, v171
	s_nop 0
	v_cmp_ge_f32_e32 vcc, s54, v170
	s_cmp_lg_u64 vcc, exec
	s_cselect_b64 s[38:39], -1, 0
	s_cmp_eq_u64 vcc, exec
	s_cbranch_scc1 .LBB0_1224
	s_nop 4
	v_add_f32_e32 v82, 0xc0c00000, v170
	v_max_f32_e32 v82, 0, v82
	v_exp_f32_e64 v170, -v82
	v_add_f32_e32 v198, v198, v82
	v_sub_f32_e32 v98, v98, v82
	v_sub_f32_e32 v114, v114, v82
	v_sub_f32_e32 v99, v99, v82
	v_sub_f32_e32 v115, v115, v82
	v_sub_f32_e32 v100, v100, v82
	v_sub_f32_e32 v116, v116, v82
	v_sub_f32_e32 v101, v101, v82
	v_sub_f32_e32 v117, v117, v82
	v_sub_f32_e32 v102, v102, v82
	v_sub_f32_e32 v118, v118, v82
	v_sub_f32_e32 v103, v103, v82
	v_sub_f32_e32 v119, v119, v82
	v_sub_f32_e32 v104, v104, v82
	v_sub_f32_e32 v120, v120, v82
	v_sub_f32_e32 v105, v105, v82
	v_sub_f32_e32 v121, v121, v82
	v_sub_f32_e32 v106, v106, v82
	v_sub_f32_e32 v122, v122, v82
	v_sub_f32_e32 v107, v107, v82
	v_sub_f32_e32 v123, v123, v82
	v_sub_f32_e32 v108, v108, v82
	v_sub_f32_e32 v124, v124, v82
	v_sub_f32_e32 v109, v109, v82
	v_sub_f32_e32 v125, v125, v82
	v_sub_f32_e32 v110, v110, v82
	v_sub_f32_e32 v126, v126, v82
	v_sub_f32_e32 v111, v111, v82
	v_sub_f32_e32 v127, v127, v82
	v_sub_f32_e32 v112, v112, v82
	v_sub_f32_e32 v128, v128, v82
	v_sub_f32_e32 v113, v113, v82
	v_sub_f32_e32 v129, v129, v82
	v_xor_b32_e32 v82, 0x80000000, v198
	v_mov_b32_e32 v83, v82
	v_mov_b32_e32 v84, v82
	v_mov_b32_e32 v85, v82
	v_mov_b32_e32 v86, v82
	v_mov_b32_e32 v87, v82
	v_mov_b32_e32 v88, v82
	v_mov_b32_e32 v89, v82
	v_mov_b32_e32 v90, v82
	v_mov_b32_e32 v91, v82
	v_mov_b32_e32 v92, v82
	v_mov_b32_e32 v93, v82
	v_mov_b32_e32 v94, v82
	v_mov_b32_e32 v95, v82
	v_mov_b32_e32 v96, v82
	v_mov_b32_e32 v97, v82
	s_branch .LBB0_1225

.LBB0_1229:
	v_cvt_pk_fp8_f32 v130, v98, v99
	v_cvt_pk_fp8_f32 v131, v102, v103
	ds_read_b128 v[138:141], v201 offset:0
	ds_read_b128 v[142:145], v202 offset:0
	ds_read_b128 v[170:173], v201 offset:0x800
	ds_read_b128 v[174:177], v202 offset:0x800
	v_cvt_pk_fp8_f32 v130, v100, v101 op_sel:[0,0,1]
	v_cvt_pk_fp8_f32 v131, v104, v105 op_sel:[0,0,1]
	s_waitcnt lgkmcnt(2)
	v_cvt_pk_fp8_f32 v132, v106, v107
	v_cvt_pk_fp8_f32 v133, v110, v111
	ds_read_b128 v[210:213], v199 offset:0
	ds_read_b128 v[214:217], v200 offset:0
	v_cvt_pk_fp8_f32 v132, v108, v109 op_sel:[0,0,1]
	v_cvt_pk_fp8_f32 v133, v112, v113 op_sel:[0,0,1]
	v_mfma_f32_32x32x64_f8f6f4 v[98:113], v[138:145], v[154:161], v[82:97]
	s_waitcnt lgkmcnt(2)
	v_cvt_pk_fp8_f32 v134, v114, v115
	v_cvt_pk_fp8_f32 v135, v118, v119
	v_cvt_pk_fp8_f32 v136, v122, v123
	v_cvt_pk_fp8_f32 v137, v126, v127
	v_cvt_pk_fp8_f32 v134, v116, v117 op_sel:[0,0,1]
	v_cvt_pk_fp8_f32 v135, v120, v121 op_sel:[0,0,1]
	v_cvt_pk_fp8_f32 v136, v124, v125 op_sel:[0,0,1]
	v_cvt_pk_fp8_f32 v137, v128, v129 op_sel:[0,0,1]
	v_mfma_f32_32x32x64_f8f6f4 v[114:129], v[170:177], v[154:161], v[82:97]
	ds_read_b128 v[162:165], v199 offset:0x800
	ds_read_b128 v[166:169], v200 offset:0x800
	s_nop 0
	v_mfma_f32_16x16x128_f8f6f4 v[18:21], v[130:137], v[146:153], v[18:21]
	s_waitcnt vmcnt(0) lgkmcnt(0)
	s_barrier
	s_waitcnt lgkmcnt(2)
	v_mfma_f32_32x32x64_f8f6f4 v[2:17], v[130:137], v[210:217], v[2:17]
	ds_read_b128 v[138:141], v199 offset:0x1000
	ds_read_b128 v[142:145], v200 offset:0x1000
	s_mov_b64 s[38:39], 0
	s_cmp_eq_u32 s98, 0
	s_cbranch_scc1 .LBB0_1232
	v_max3_f32 v170, v98, v99, v100
	v_max3_f32 v170, v170, v101, v102
	v_max3_f32 v170, v170, v103, v104
	v_max3_f32 v170, v170, v105, v106
	v_max3_f32 v170, v170, v107, v108
	v_max3_f32 v170, v170, v109, v110
	v_max3_f32 v170, v170, v111, v112
	v_max_f32 v170, v170, v113
	s_nop 0
	v_max3_f32 v170, v170, v114, v115
	v_max3_f32 v170, v170, v116, v117
	v_max3_f32 v170, v170, v118, v119
	v_max3_f32 v170, v170, v120, v121
	v_max3_f32 v170, v170, v122, v123
	v_max3_f32 v170, v170, v124, v125
	v_max3_f32 v170, v170, v126, v127
	v_max3_f32 v170, v170, v128, v129
	v_mov_b32 v171, v170
	s_nop 1
	v_permlane32_swap_b32 v170, v171
	v_max_f32 v170, v170, v171
	s_nop 0
	v_cmp_ge_f32_e32 vcc, s54, v170
	s_cmp_lg_u64 vcc, exec
	s_cselect_b64 s[38:39], -1, 0
	s_cmp_eq_u64 vcc, exec
	s_cbranch_scc1 .LBB0_1231
	s_nop 4
	v_add_f32_e32 v82, 0xc0c00000, v170
	v_max_f32_e32 v82, 0, v82
	v_exp_f32_e64 v170, -v82
	v_add_f32_e32 v198, v198, v82
	v_sub_f32_e32 v98, v98, v82
	v_sub_f32_e32 v114, v114, v82
	v_sub_f32_e32 v99, v99, v82
	v_sub_f32_e32 v115, v115, v82
	v_sub_f32_e32 v100, v100, v82
	v_sub_f32_e32 v116, v116, v82
	v_sub_f32_e32 v101, v101, v82
	v_sub_f32_e32 v117, v117, v82
	v_sub_f32_e32 v102, v102, v82
	v_sub_f32_e32 v118, v118, v82
	v_sub_f32_e32 v103, v103, v82
	v_sub_f32_e32 v119, v119, v82
	v_sub_f32_e32 v104, v104, v82
	v_sub_f32_e32 v120, v120, v82
	v_sub_f32_e32 v105, v105, v82
	v_sub_f32_e32 v121, v121, v82
	v_sub_f32_e32 v106, v106, v82
	v_sub_f32_e32 v122, v122, v82
	v_sub_f32_e32 v107, v107, v82
	v_sub_f32_e32 v123, v123, v82
	v_sub_f32_e32 v108, v108, v82
	v_sub_f32_e32 v124, v124, v82
	v_sub_f32_e32 v109, v109, v82
	v_sub_f32_e32 v125, v125, v82
	v_sub_f32_e32 v110, v110, v82
	v_sub_f32_e32 v126, v126, v82
	v_sub_f32_e32 v111, v111, v82
	v_sub_f32_e32 v127, v127, v82
	v_sub_f32_e32 v112, v112, v82
	v_sub_f32_e32 v128, v128, v82
	v_sub_f32_e32 v113, v113, v82
	v_sub_f32_e32 v129, v129, v82
	v_xor_b32_e32 v82, 0x80000000, v198
	v_mov_b32_e32 v83, v82
	v_mov_b32_e32 v84, v82
	v_mov_b32_e32 v85, v82
	v_mov_b32_e32 v86, v82
	v_mov_b32_e32 v87, v82
	v_mov_b32_e32 v88, v82
	v_mov_b32_e32 v89, v82
	v_mov_b32_e32 v90, v82
	v_mov_b32_e32 v91, v82
	v_mov_b32_e32 v92, v82
	v_mov_b32_e32 v93, v82
	v_mov_b32_e32 v94, v82
	v_mov_b32_e32 v95, v82
	v_mov_b32_e32 v96, v82
	v_mov_b32_e32 v97, v82
	s_branch .LBB0_1232

.LBB0_1236:
	v_cvt_pk_fp8_f32 v130, v98, v99
	v_cvt_pk_fp8_f32 v131, v102, v103
	ds_read_b128 v[138:141], v183 offset:0
	ds_read_b128 v[142:145], v190 offset:0
	ds_read_b128 v[170:173], v183 offset:0x800
	ds_read_b128 v[174:177], v190 offset:0x800
	v_cvt_pk_fp8_f32 v130, v100, v101 op_sel:[0,0,1]
	v_cvt_pk_fp8_f32 v131, v104, v105 op_sel:[0,0,1]
	s_waitcnt lgkmcnt(2)
	v_cvt_pk_fp8_f32 v132, v106, v107
	v_cvt_pk_fp8_f32 v133, v110, v111
	ds_read_b128 v[210:213], v196 offset:0
	ds_read_b128 v[214:217], v197 offset:0
	v_cvt_pk_fp8_f32 v132, v108, v109 op_sel:[0,0,1]
	v_cvt_pk_fp8_f32 v133, v112, v113 op_sel:[0,0,1]
	v_mfma_f32_32x32x64_f8f6f4 v[98:113], v[138:145], v[154:161], v[82:97]
	s_waitcnt lgkmcnt(2)
	v_cvt_pk_fp8_f32 v134, v114, v115
	v_cvt_pk_fp8_f32 v135, v118, v119
	v_cvt_pk_fp8_f32 v136, v122, v123
	v_cvt_pk_fp8_f32 v137, v126, v127
	v_cvt_pk_fp8_f32 v134, v116, v117 op_sel:[0,0,1]
	v_cvt_pk_fp8_f32 v135, v120, v121 op_sel:[0,0,1]
	v_cvt_pk_fp8_f32 v136, v124, v125 op_sel:[0,0,1]
	v_cvt_pk_fp8_f32 v137, v128, v129 op_sel:[0,0,1]
	v_mfma_f32_32x32x64_f8f6f4 v[114:129], v[170:177], v[154:161], v[82:97]
	ds_read_b128 v[162:165], v196 offset:0x800
	ds_read_b128 v[166:169], v197 offset:0x800
	s_nop 0
	v_mfma_f32_16x16x128_f8f6f4 v[18:21], v[130:137], v[146:153], v[18:21]
	s_waitcnt vmcnt(0) lgkmcnt(0)
	s_barrier
	s_waitcnt lgkmcnt(2)
	v_mfma_f32_32x32x64_f8f6f4 v[2:17], v[130:137], v[210:217], v[2:17]
	ds_read_b128 v[138:141], v196 offset:0x1000
	ds_read_b128 v[142:145], v197 offset:0x1000
	s_mov_b64 s[38:39], 0
	s_cmp_eq_u32 s98, 0
	s_cbranch_scc1 .LBB0_1239
	v_max3_f32 v170, v98, v99, v100
	v_max3_f32 v170, v170, v101, v102
	v_max3_f32 v170, v170, v103, v104
	v_max3_f32 v170, v170, v105, v106
	v_max3_f32 v170, v170, v107, v108
	v_max3_f32 v170, v170, v109, v110
	v_max3_f32 v170, v170, v111, v112
	v_max_f32 v170, v170, v113
	s_nop 0
	v_max3_f32 v170, v170, v114, v115
	v_max3_f32 v170, v170, v116, v117
	v_max3_f32 v170, v170, v118, v119
	v_max3_f32 v170, v170, v120, v121
	v_max3_f32 v170, v170, v122, v123
	v_max3_f32 v170, v170, v124, v125
	v_max3_f32 v170, v170, v126, v127
	v_max3_f32 v170, v170, v128, v129
	v_mov_b32 v171, v170
	s_nop 1
	v_permlane32_swap_b32 v170, v171
	v_max_f32 v170, v170, v171
	s_nop 0
	v_cmp_ge_f32_e32 vcc, s54, v170
	s_cmp_lg_u64 vcc, exec
	s_cselect_b64 s[38:39], -1, 0
	s_cmp_eq_u64 vcc, exec
	s_cbranch_scc1 .LBB0_1238
	s_nop 4
	v_add_f32_e32 v82, 0xc0c00000, v170
	v_max_f32_e32 v82, 0, v82
	v_exp_f32_e64 v170, -v82
	v_add_f32_e32 v198, v198, v82
	v_sub_f32_e32 v98, v98, v82
	v_sub_f32_e32 v114, v114, v82
	v_sub_f32_e32 v99, v99, v82
	v_sub_f32_e32 v115, v115, v82
	v_sub_f32_e32 v100, v100, v82
	v_sub_f32_e32 v116, v116, v82
	v_sub_f32_e32 v101, v101, v82
	v_sub_f32_e32 v117, v117, v82
	v_sub_f32_e32 v102, v102, v82
	v_sub_f32_e32 v118, v118, v82
	v_sub_f32_e32 v103, v103, v82
	v_sub_f32_e32 v119, v119, v82
	v_sub_f32_e32 v104, v104, v82
	v_sub_f32_e32 v120, v120, v82
	v_sub_f32_e32 v105, v105, v82
	v_sub_f32_e32 v121, v121, v82
	v_sub_f32_e32 v106, v106, v82
	v_sub_f32_e32 v122, v122, v82
	v_sub_f32_e32 v107, v107, v82
	v_sub_f32_e32 v123, v123, v82
	v_sub_f32_e32 v108, v108, v82
	v_sub_f32_e32 v124, v124, v82
	v_sub_f32_e32 v109, v109, v82
	v_sub_f32_e32 v125, v125, v82
	v_sub_f32_e32 v110, v110, v82
	v_sub_f32_e32 v126, v126, v82
	v_sub_f32_e32 v111, v111, v82
	v_sub_f32_e32 v127, v127, v82
	v_sub_f32_e32 v112, v112, v82
	v_sub_f32_e32 v128, v128, v82
	v_sub_f32_e32 v113, v113, v82
	v_sub_f32_e32 v129, v129, v82
	v_xor_b32_e32 v82, 0x80000000, v198
	v_mov_b32_e32 v83, v82
	v_mov_b32_e32 v84, v82
	v_mov_b32_e32 v85, v82
	v_mov_b32_e32 v86, v82
	v_mov_b32_e32 v87, v82
	v_mov_b32_e32 v88, v82
	v_mov_b32_e32 v89, v82
	v_mov_b32_e32 v90, v82
	v_mov_b32_e32 v91, v82
	v_mov_b32_e32 v92, v82
	v_mov_b32_e32 v93, v82
	v_mov_b32_e32 v94, v82
	v_mov_b32_e32 v95, v82
	v_mov_b32_e32 v96, v82
	v_mov_b32_e32 v97, v82
	s_branch .LBB0_1239

.LBB0_1256:
	v_cvt_pk_fp8_f32 v130, v98, v99
	v_cvt_pk_fp8_f32 v131, v102, v103
	ds_read_b128 v[138:141], v201 offset:0
	ds_read_b128 v[142:145], v202 offset:0
	ds_read_b128 v[170:173], v201 offset:0x800
	ds_read_b128 v[174:177], v202 offset:0x800
	v_cvt_pk_fp8_f32 v130, v100, v101 op_sel:[0,0,1]
	v_cvt_pk_fp8_f32 v131, v104, v105 op_sel:[0,0,1]
	s_waitcnt lgkmcnt(2)
	v_cvt_pk_fp8_f32 v132, v106, v107
	v_cvt_pk_fp8_f32 v133, v110, v111
	ds_read_b128 v[210:213], v199 offset:0
	ds_read_b128 v[214:217], v200 offset:0
	v_cvt_pk_fp8_f32 v132, v108, v109 op_sel:[0,0,1]
	v_cvt_pk_fp8_f32 v133, v112, v113 op_sel:[0,0,1]
	v_mfma_f32_32x32x64_f8f6f4 v[98:113], v[138:145], v[154:161], v[82:97]
	s_waitcnt lgkmcnt(2)
	v_mfma_f32_32x32x64_f8f6f4 v[82:97], v[170:177], v[154:161], v[82:97]
	v_cvt_pk_fp8_f32 v134, v114, v115
	v_cvt_pk_fp8_f32 v135, v118, v119
	v_cvt_pk_fp8_f32 v136, v122, v123
	v_cvt_pk_fp8_f32 v137, v126, v127
	v_cvt_pk_fp8_f32 v134, v116, v117 op_sel:[0,0,1]
	v_cvt_pk_fp8_f32 v135, v120, v121 op_sel:[0,0,1]
	v_cvt_pk_fp8_f32 v136, v124, v125 op_sel:[0,0,1]
	v_cvt_pk_fp8_f32 v137, v128, v129 op_sel:[0,0,1]
	s_nop 0
	ds_read_b128 v[162:165], v199 offset:0x800
	ds_read_b128 v[166:169], v200 offset:0x800
	s_nop 0
	v_mfma_f32_16x16x128_f8f6f4 v[18:21], v[130:137], v[146:153], v[18:21]
	s_waitcnt vmcnt(0) lgkmcnt(0)
	s_barrier
	s_waitcnt lgkmcnt(2)
	v_mfma_f32_32x32x64_f8f6f4 v[2:17], v[130:137], v[210:217], v[2:17]
	ds_read_b128 v[138:141], v199 offset:0x1000
	ds_read_b128 v[142:145], v200 offset:0x1000
	s_mov_b64 s[38:39], 0
	s_cmp_eq_u32 s98, 0
	s_cbranch_scc1 .LBB0_1259
	v_max3_f32 v114, v98, v99, v100
	v_max3_f32 v114, v114, v101, v102
	v_max3_f32 v114, v114, v103, v104
	v_max3_f32 v114, v114, v105, v106
	v_max3_f32 v114, v114, v107, v108
	v_max3_f32 v114, v114, v109, v110
	v_max3_f32 v114, v114, v111, v112
	v_max_f32 v114, v114, v113
	s_nop 0
	v_max3_f32 v114, v114, v82, v83
	v_max3_f32 v114, v114, v84, v85
	v_max3_f32 v114, v114, v86, v87
	v_max3_f32 v114, v114, v88, v89
	v_max3_f32 v114, v114, v90, v91
	v_max3_f32 v114, v114, v92, v93
	v_max3_f32 v114, v114, v94, v95
	v_max3_f32 v114, v114, v96, v97
	v_mov_b32 v115, v114
	s_nop 1
	v_permlane32_swap_b32 v114, v115
	v_max_f32 v114, v114, v115
	s_nop 0
	v_cmp_ge_f32_e32 vcc, s54, v114
	s_cmp_lg_u64 vcc, exec
	s_cselect_b64 s[38:39], -1, 0
	s_cmp_eq_u64 vcc, exec
	s_cbranch_scc1 .LBB0_1258
	v_add_f32_e32 v114, 0xc0c00000, v114
	v_max_f32_e32 v114, 0, v114
	v_exp_f32_e64 v170, -v114
	v_sub_f32_e32 v98, v98, v114
	v_sub_f32_e32 v82, v82, v114
	v_sub_f32_e32 v99, v99, v114
	v_sub_f32_e32 v83, v83, v114
	v_sub_f32_e32 v100, v100, v114
	v_sub_f32_e32 v84, v84, v114
	v_sub_f32_e32 v101, v101, v114
	v_sub_f32_e32 v85, v85, v114
	v_sub_f32_e32 v102, v102, v114
	v_sub_f32_e32 v86, v86, v114
	v_sub_f32_e32 v103, v103, v114
	v_sub_f32_e32 v87, v87, v114
	v_sub_f32_e32 v104, v104, v114
	v_sub_f32_e32 v88, v88, v114
	v_sub_f32_e32 v105, v105, v114
	v_sub_f32_e32 v89, v89, v114
	v_sub_f32_e32 v106, v106, v114
	v_sub_f32_e32 v90, v90, v114
	v_sub_f32_e32 v107, v107, v114
	v_sub_f32_e32 v91, v91, v114
	v_sub_f32_e32 v108, v108, v114
	v_sub_f32_e32 v92, v92, v114
	v_sub_f32_e32 v109, v109, v114
	v_sub_f32_e32 v93, v93, v114
	v_sub_f32_e32 v110, v110, v114
	v_sub_f32_e32 v94, v94, v114
	v_sub_f32_e32 v111, v111, v114
	v_sub_f32_e32 v95, v95, v114
	v_sub_f32_e32 v112, v112, v114
	v_sub_f32_e32 v96, v96, v114
	v_sub_f32_e32 v113, v113, v114
	v_sub_f32_e32 v97, v97, v114
	v_add_f32_e32 v114, v198, v114
	v_xor_b32_e32 v114, 0x80000000, v114
	v_mov_b32_e32 v115, v114
	v_mov_b32_e32 v116, v114
	v_mov_b32_e32 v117, v114
	v_mov_b32_e32 v118, v114
	v_mov_b32_e32 v119, v114
	v_mov_b32_e32 v120, v114
	v_mov_b32_e32 v121, v114
	v_mov_b32_e32 v122, v114
	v_mov_b32_e32 v123, v114
	v_mov_b32_e32 v124, v114
	v_mov_b32_e32 v125, v114
	v_mov_b32_e32 v126, v114
	v_mov_b32_e32 v127, v114
	v_mov_b32_e32 v128, v114
	v_mov_b32_e32 v129, v114
	s_branch .LBB0_1259

.LBB0_1264:
	s_lshl_b32 s94, s77, 8
	s_add_i32 s77, s94, 0x8000
	s_and_b64 vcc, exec, s[38:39]
	s_cbranch_vccz .LBB0_1317
	ds_read_b128 v[18:21], v183 offset:0
	ds_read_b128 v[22:25], v190 offset:0
	ds_read_b128 v[34:37], v183 offset:0x800
	ds_read_b128 v[38:41], v190 offset:0x800
	s_waitcnt lgkmcnt(0)
	s_waitcnt vmcnt(0)
	s_nop 9
	v_mfma_f32_32x32x64_f8f6f4 v[18:33], v[18:25], v[154:161], 0
	s_mov_b32 s37, s36
	s_mov_b32 s38, s36
	s_mov_b32 s39, s36
	s_mov_b32 s40, s36
	s_mov_b32 s41, s36
	s_mov_b32 s42, s36
	s_mov_b32 s43, s36
	s_mov_b32 s44, s36
	s_mov_b32 s45, s36
	s_mov_b32 s46, s36
	s_mov_b32 s47, s36
	s_mov_b32 s48, s36
	s_mov_b32 s49, s36
	s_mov_b32 s50, s36
	s_mov_b32 s51, s36
	v_mov_b64_e32 v[2:3], s[36:37]
	v_mov_b64_e32 v[4:5], s[38:39]
	v_mov_b64_e32 v[6:7], s[40:41]
	v_mov_b64_e32 v[8:9], s[42:43]
	v_mov_b64_e32 v[10:11], s[44:45]
	v_mov_b64_e32 v[12:13], s[46:47]
	v_mov_b64_e32 v[14:15], s[48:49]
	v_mov_b64_e32 v[16:17], s[50:51]
	v_max_f32_e32 v42, v19, v19
	v_max_f32_e32 v43, v18, v18
	v_max_f32_e32 v42, v43, v42
	v_max3_f32 v42, v42, v20, v21
	v_max3_f32 v42, v42, v22, v23
	v_max3_f32 v42, v42, v24, v25
	v_max3_f32 v42, v42, v26, v27
	v_max3_f32 v42, v42, v28, v29
	v_max3_f32 v50, v42, v30, v31
	v_mfma_f32_32x32x64_f8f6f4 v[34:49], v[34:41], v[154:161], 0
	v_max3_f32 v50, v50, v32, v33
	s_lshl_b32 s45, s81, 10
	s_lshl_b32 s46, s80, 10
	s_cmp_lg_u32 0, -1
	s_cselect_b32 s38, 0, 0
	s_add_i32 s37, s38, 0x2000
	s_add_i32 s39, s38, 0x3000
	s_add_i32 s6, s38, 0x1000
	v_add_u32_e32 v203, s37, v194
	s_add_i32 s37, s38, 0x6000
	v_add_u32_e32 v199, s39, v194
	s_add_i32 s39, s38, 0x8000
	s_add_i32 s38, s38, 0xa000
	v_add_u32_e32 v205, s6, v194
	v_add_u32_e32 v201, s37, v194
	s_nop 4
	v_max3_f32 v50, v50, v34, v35
	v_max3_f32 v50, v50, v36, v37
	v_max3_f32 v50, v50, v38, v39
	v_max3_f32 v50, v50, v40, v41
	v_max3_f32 v50, v50, v42, v43
	v_max3_f32 v50, v50, v44, v45
	v_max3_f32 v50, v50, v46, v47
	v_max3_f32 v50, v50, v48, v49
	v_mov_b32_e32 v51, v50
	s_nop 1
	v_permlane32_swap_b32_e32 v50, v51
	v_max_f32_e32 v51, v51, v51
	v_max_f32_e32 v50, v50, v50
	v_max_f32_e32 v50, v50, v51
	s_cmp_eq_u32 s98, 0
	s_cselect_b32 s100, 0x3f800000, 0xc0600000
	v_add_f32_e32 v198, s100, v50
	v_add_u32_e32 v196, s39, v194
	v_add_u32_e32 v194, s38, v194
	s_lshl_b32 s38, s95, 4
	v_sub_f32_e32 v18, v18, v198
	s_and_b32 s38, s38, 0xfffffc00
	s_ashr_i32 s89, s88, 31
	v_exp_f32_e32 v114, v18
	s_or_b32 s40, s88, 0x100
	s_add_i32 s41, s94, 0x4100
	s_or_b32 s42, s88, 0x140
	s_add_i32 s43, s94, 0x4140
	v_lshl_or_b32 v18, v193, 4, s38
	s_lshl_b64 s[38:39], s[88:89], 10
	s_add_u32 s38, s38, s87
	v_xor_b32_e32 v82, 0x80000000, v198
	v_sub_f32_e32 v34, v34, v198
	v_sub_f32_e32 v19, v19, v198
	v_sub_f32_e32 v35, v35, v198
	v_sub_f32_e32 v20, v20, v198
	v_sub_f32_e32 v36, v36, v198
	v_sub_f32_e32 v21, v21, v198
	v_sub_f32_e32 v37, v37, v198
	v_sub_f32_e32 v22, v22, v198
	v_sub_f32_e32 v38, v38, v198
	v_sub_f32_e32 v23, v23, v198
	v_sub_f32_e32 v39, v39, v198
	v_sub_f32_e32 v24, v24, v198
	v_sub_f32_e32 v40, v40, v198
	v_sub_f32_e32 v25, v25, v198
	v_sub_f32_e32 v41, v41, v198
	v_sub_f32_e32 v26, v26, v198
	v_sub_f32_e32 v42, v42, v198
	v_sub_f32_e32 v27, v27, v198
	v_sub_f32_e32 v43, v43, v198
	v_sub_f32_e32 v28, v28, v198
	v_sub_f32_e32 v44, v44, v198
	v_sub_f32_e32 v29, v29, v198
	v_sub_f32_e32 v45, v45, v198
	v_sub_f32_e32 v30, v30, v198
	v_sub_f32_e32 v46, v46, v198
	v_sub_f32_e32 v31, v31, v198
	v_sub_f32_e32 v47, v47, v198
	v_sub_f32_e32 v32, v32, v198
	v_sub_f32_e32 v48, v48, v198
	v_sub_f32_e32 v33, v33, v198
	v_sub_f32_e32 v49, v49, v198
	s_addc_u32 s39, s39, s76
	v_mov_b32_e32 v83, v82
	v_mov_b32_e32 v84, v82
	v_mov_b32_e32 v85, v82
	v_mov_b32_e32 v86, v82
	v_mov_b32_e32 v87, v82
	v_mov_b32_e32 v88, v82
	v_mov_b32_e32 v89, v82
	v_mov_b32_e32 v90, v82
	v_mov_b32_e32 v91, v82
	v_mov_b32_e32 v92, v82
	v_mov_b32_e32 v93, v82
	v_mov_b32_e32 v94, v82
	v_mov_b32_e32 v95, v82
	v_mov_b32_e32 v96, v82
	v_mov_b32_e32 v97, v82
	v_exp_f32_e32 v98, v34
	v_exp_f32_e32 v115, v19
	v_exp_f32_e32 v99, v35
	v_exp_f32_e32 v116, v20
	v_exp_f32_e32 v100, v36
	v_exp_f32_e32 v117, v21
	v_exp_f32_e32 v101, v37
	v_exp_f32_e32 v118, v22
	v_exp_f32_e32 v102, v38
	v_exp_f32_e32 v119, v23
	v_exp_f32_e32 v103, v39
	v_exp_f32_e32 v120, v24
	v_exp_f32_e32 v104, v40
	v_exp_f32_e32 v121, v25
	v_exp_f32_e32 v105, v41
	v_exp_f32_e32 v122, v26
	v_exp_f32_e32 v106, v42
	v_exp_f32_e32 v123, v27
	v_exp_f32_e32 v107, v43
	v_exp_f32_e32 v124, v28
	v_exp_f32_e32 v108, v44
	v_exp_f32_e32 v125, v29
	v_exp_f32_e32 v109, v45
	v_exp_f32_e32 v126, v30
	v_exp_f32_e32 v110, v46
	v_exp_f32_e32 v127, v31
	v_exp_f32_e32 v111, v47
	v_exp_f32_e32 v128, v32
	v_exp_f32_e32 v112, v48
	v_exp_f32_e32 v129, v33
	v_exp_f32_e32 v113, v49
	v_mov_b32_e32 v19, v181
	s_add_u32 s38, s38, 0x29c30000
	s_waitcnt vmcnt(3) lgkmcnt(0)
	s_barrier
	v_lshl_add_u64 v[172:173], s[92:93], 0, v[18:19]
	s_addc_u32 s39, s39, 0
	v_add3_u32 v18, s79, v191, v192
	v_lshl_add_u64 v[174:175], s[38:39], 0, v[18:19]
	v_mov_b32_e32 v162, 0
	v_mov_b64_e32 v[48:49], v[16:17]
	v_mov_b64_e32 v[64:65], v[16:17]
	v_mov_b64_e32 v[80:81], v[16:17]
	v_mov_b64_e32 v[32:33], v[16:17]
	v_lshl_add_u64 v[170:171], s[28:29], 0, v[180:181]
	v_add_u32_e32 v206, v205, v195
	v_cmp_gt_u32_e64 s[6:7], 32, v193
	v_add_u32_e32 v204, v203, v195
	v_add_u32_e32 v202, v201, v195
	s_movk_i32 s37, 0x100
	v_add_u32_e32 v200, v199, v195
	v_add_u32_e32 v197, v196, v195
	v_add_u32_e32 v195, v194, v195
	s_mov_b32 s44, -3
	s_add_i32 s45, s45, 0
	s_add_i32 s46, s46, 0
	v_mov_b64_e32 v[46:47], v[14:15]
	v_mov_b64_e32 v[44:45], v[12:13]
	v_mov_b64_e32 v[42:43], v[10:11]
	v_mov_b64_e32 v[40:41], v[8:9]
	v_mov_b64_e32 v[38:39], v[6:7]
	v_mov_b64_e32 v[36:37], v[4:5]
	v_mov_b64_e32 v[34:35], v[2:3]
	v_mov_b64_e32 v[62:63], v[14:15]
	v_mov_b64_e32 v[60:61], v[12:13]
	v_mov_b64_e32 v[58:59], v[10:11]
	v_mov_b64_e32 v[56:57], v[8:9]
	v_mov_b64_e32 v[54:55], v[6:7]
	v_mov_b64_e32 v[52:53], v[4:5]
	v_mov_b64_e32 v[50:51], v[2:3]
	v_mov_b64_e32 v[78:79], v[14:15]
	v_mov_b64_e32 v[76:77], v[12:13]
	v_mov_b64_e32 v[74:75], v[10:11]
	v_mov_b64_e32 v[72:73], v[8:9]
	v_mov_b64_e32 v[70:71], v[6:7]
	v_mov_b64_e32 v[68:69], v[4:5]
	v_mov_b64_e32 v[66:67], v[2:3]
	v_mov_b64_e32 v[30:31], v[14:15]
	v_mov_b64_e32 v[28:29], v[12:13]
	v_mov_b64_e32 v[26:27], v[10:11]
	v_mov_b64_e32 v[24:25], v[8:9]
	v_mov_b64_e32 v[22:23], v[6:7]
	v_mov_b64_e32 v[20:21], v[4:5]
	v_mov_b64_e32 v[18:19], v[2:3]
	v_mov_b32_e32 v163, v162
	v_mov_b32_e32 v164, v162
	v_mov_b32_e32 v165, v162
	v_mov_b32_e32 v166, v162
	v_mov_b32_e32 v167, v162
	v_mov_b32_e32 v168, v162
	v_mov_b32_e32 v169, v162
	s_branch .LBB0_1268

.LBB0_1268:
	s_add_i32 s49, s45, 0x3000
	v_lshl_add_u64 v[130:131], s[14:15], 0, v[174:175]
	s_mov_b32 m0, s49
	v_lshl_add_u64 v[176:177], s[14:15], 0, v[172:173]
	s_add_i32 s47, s46, 0x8000
	global_load_lds_dwordx4 v[130:131], off
	v_lshl_add_u64 v[130:131], v[176:177], 0, s[56:57]
	s_mov_b32 m0, s47
	s_add_i32 s48, s46, 0x9000
	global_load_lds_dwordx4 v[130:131], off
	v_lshl_add_u64 v[130:131], v[176:177], 0, s[58:59]
	s_mov_b32 m0, s48
	v_cvt_pk_fp8_f32 v162, v114, v115
	global_load_lds_dwordx4 v[130:131], off
	v_cvt_pk_fp8_f32 v163, v118, v119
	ds_read_b128 v[130:133], v205 offset:0
	ds_read_b128 v[134:137], v206 offset:0
	ds_read_b128 v[210:213], v205 offset:0x800
	ds_read_b128 v[214:217], v206 offset:0x800
	v_cvt_pk_fp8_f32 v162, v116, v117 op_sel:[0,0,1]
	v_cvt_pk_fp8_f32 v163, v120, v121 op_sel:[0,0,1]
	s_waitcnt lgkmcnt(2)
	v_cvt_pk_fp8_f32 v164, v122, v123
	v_cvt_pk_fp8_f32 v165, v126, v127
	ds_read_b128 v[218:221], v188 offset:0
	ds_read_b128 v[222:225], v189 offset:0
	v_cvt_pk_fp8_f32 v164, v124, v125 op_sel:[0,0,1]
	v_cvt_pk_fp8_f32 v165, v128, v129 op_sel:[0,0,1]
	v_mfma_f32_32x32x64_f8f6f4 v[114:129], v[130:137], v[154:161], v[82:97]
	s_waitcnt lgkmcnt(2)
	v_mfma_f32_32x32x64_f8f6f4 v[130:145], v[210:217], v[154:161], v[82:97]
	v_cvt_pk_fp8_f32 v166, v98, v99
	v_cvt_pk_fp8_f32 v167, v102, v103
	v_cvt_pk_fp8_f32 v168, v106, v107
	v_cvt_pk_fp8_f32 v169, v110, v111
	v_cvt_pk_fp8_f32 v166, v100, v101 op_sel:[0,0,1]
	v_cvt_pk_fp8_f32 v167, v104, v105 op_sel:[0,0,1]
	v_cvt_pk_fp8_f32 v168, v108, v109 op_sel:[0,0,1]
	v_cvt_pk_fp8_f32 v169, v112, v113 op_sel:[0,0,1]
	s_nop 0
	ds_read_b128 v[106:109], v188 offset:0x800
	ds_read_b128 v[110:113], v189 offset:0x800
	s_nop 0
	v_mfma_f32_16x16x128_f8f6f4 v[18:21], v[162:169], v[146:153], v[18:21]
	s_waitcnt lgkmcnt(2)
	v_mfma_f32_32x32x64_f8f6f4 v[2:17], v[162:169], v[218:225], v[2:17]
	ds_read_b128 v[98:101], v188 offset:0x1000
	ds_read_b128 v[102:105], v189 offset:0x1000
	s_mov_b64 s[38:39], 0
	s_cmp_eq_u32 s98, 0
	s_cbranch_scc1 .LBB0_1271
	v_max3_f32 v191, v114, v115, v116
	v_max3_f32 v191, v191, v117, v118
	v_max3_f32 v191, v191, v119, v120
	v_max3_f32 v191, v191, v121, v122
	v_max3_f32 v191, v191, v123, v124
	v_max3_f32 v191, v191, v125, v126
	v_max3_f32 v191, v191, v127, v128
	v_max_f32 v191, v191, v129
	s_nop 0
	v_max3_f32 v191, v191, v130, v131
	v_max3_f32 v191, v191, v132, v133
	v_max3_f32 v191, v191, v134, v135
	v_max3_f32 v191, v191, v136, v137
	v_max3_f32 v191, v191, v138, v139
	v_max3_f32 v191, v191, v140, v141
	v_max3_f32 v191, v191, v142, v143
	v_max3_f32 v191, v191, v144, v145
	v_mov_b32 v192, v191
	s_nop 1
	v_permlane32_swap_b32 v191, v192
	v_max_f32 v191, v191, v192
	s_nop 0
	v_cmp_ge_f32_e32 vcc, s54, v191
	s_cmp_lg_u64 vcc, exec
	s_cselect_b64 s[38:39], -1, 0
	s_cmp_eq_u64 vcc, exec
	s_cbranch_scc1 .LBB0_1270
	v_add_f32_e32 v82, 0xc0c00000, v191
	v_max_f32_e32 v82, 0, v82
	v_exp_f32_e64 v191, -v82
	v_add_f32_e32 v198, v198, v82
	v_sub_f32_e32 v114, v114, v82
	v_sub_f32_e32 v130, v130, v82
	v_sub_f32_e32 v115, v115, v82
	v_sub_f32_e32 v131, v131, v82
	v_sub_f32_e32 v116, v116, v82
	v_sub_f32_e32 v132, v132, v82
	v_sub_f32_e32 v117, v117, v82
	v_sub_f32_e32 v133, v133, v82
	v_sub_f32_e32 v118, v118, v82
	v_sub_f32_e32 v134, v134, v82
	v_sub_f32_e32 v119, v119, v82
	v_sub_f32_e32 v135, v135, v82
	v_sub_f32_e32 v120, v120, v82
	v_sub_f32_e32 v136, v136, v82
	v_sub_f32_e32 v121, v121, v82
	v_sub_f32_e32 v137, v137, v82
	v_sub_f32_e32 v122, v122, v82
	v_sub_f32_e32 v138, v138, v82
	v_sub_f32_e32 v123, v123, v82
	v_sub_f32_e32 v139, v139, v82
	v_sub_f32_e32 v124, v124, v82
	v_sub_f32_e32 v140, v140, v82
	v_sub_f32_e32 v125, v125, v82
	v_sub_f32_e32 v141, v141, v82
	v_sub_f32_e32 v126, v126, v82
	v_sub_f32_e32 v142, v142, v82
	v_sub_f32_e32 v127, v127, v82
	v_sub_f32_e32 v143, v143, v82
	v_sub_f32_e32 v128, v128, v82
	v_sub_f32_e32 v144, v144, v82
	v_sub_f32_e32 v129, v129, v82
	v_sub_f32_e32 v145, v145, v82
	v_xor_b32_e32 v82, 0x80000000, v198
	v_mov_b32_e32 v83, v82
	v_mov_b32_e32 v84, v82
	v_mov_b32_e32 v85, v82
	v_mov_b32_e32 v86, v82
	v_mov_b32_e32 v87, v82
	v_mov_b32_e32 v88, v82
	v_mov_b32_e32 v89, v82
	v_mov_b32_e32 v90, v82
	v_mov_b32_e32 v91, v82
	v_mov_b32_e32 v92, v82
	v_mov_b32_e32 v93, v82
	v_mov_b32_e32 v94, v82
	v_mov_b32_e32 v95, v82
	v_mov_b32_e32 v96, v82
	v_mov_b32_e32 v97, v82
	s_branch .LBB0_1271

.LBB0_1275:
	s_add_i32 s38, s88, s37
	s_cmpk_eq_i32 s44, 0xf9
	s_cselect_b32 s38, s77, s38
	s_ashr_i32 s39, s38, 31
	s_lshl_b64 s[38:39], s[38:39], 10
	s_mov_b32 m0, s45
	s_waitcnt vmcnt(3) lgkmcnt(0)
	s_barrier
	v_lshl_add_u64 v[98:99], v[170:171], 0, s[38:39]
	s_add_i32 s51, s46, 0xa000
	global_load_lds_dwordx4 v[98:99], off
	v_lshl_add_u64 v[98:99], v[176:177], 0, s[60:61]
	s_mov_b32 m0, s51
	s_add_i32 s50, s46, 0xb000
	global_load_lds_dwordx4 v[98:99], off
	v_lshl_add_u64 v[98:99], v[176:177], 0, s[62:63]
	s_mov_b32 m0, s50
	v_cvt_pk_fp8_f32 v162, v114, v115
	global_load_lds_dwordx4 v[98:99], off
	v_cvt_pk_fp8_f32 v163, v118, v119
	ds_read_b128 v[210:213], v203 offset:0
	ds_read_b128 v[214:217], v204 offset:0
	ds_read_b128 v[218:221], v203 offset:0x800
	ds_read_b128 v[222:225], v204 offset:0x800
	v_cvt_pk_fp8_f32 v162, v116, v117 op_sel:[0,0,1]
	v_cvt_pk_fp8_f32 v163, v120, v121 op_sel:[0,0,1]
	s_waitcnt lgkmcnt(2)
	v_mfma_f32_32x32x64_f8f6f4 v[98:113], v[210:217], v[154:161], v[82:97]
	v_cvt_pk_fp8_f32 v164, v122, v123
	v_cvt_pk_fp8_f32 v165, v126, v127
	ds_read_b128 v[226:229], v201 offset:0
	ds_read_b128 v[230:233], v202 offset:0
	v_cvt_pk_fp8_f32 v164, v124, v125 op_sel:[0,0,1]
	v_cvt_pk_fp8_f32 v165, v128, v129 op_sel:[0,0,1]
	s_waitcnt lgkmcnt(2)
	v_mfma_f32_32x32x64_f8f6f4 v[114:129], v[218:225], v[154:161], v[82:97]
	v_cvt_pk_fp8_f32 v166, v130, v131
	v_cvt_pk_fp8_f32 v167, v134, v135
	v_cvt_pk_fp8_f32 v168, v138, v139
	v_cvt_pk_fp8_f32 v169, v142, v143
	v_cvt_pk_fp8_f32 v166, v132, v133 op_sel:[0,0,1]
	v_cvt_pk_fp8_f32 v167, v136, v137 op_sel:[0,0,1]
	v_cvt_pk_fp8_f32 v168, v140, v141 op_sel:[0,0,1]
	v_cvt_pk_fp8_f32 v169, v144, v145 op_sel:[0,0,1]
	s_nop 0
	ds_read_b128 v[138:141], v201 offset:0x800
	ds_read_b128 v[142:145], v202 offset:0x800
	s_nop 0
	v_mfma_f32_16x16x128_f8f6f4 v[18:21], v[162:169], v[146:153], v[18:21]
	s_waitcnt lgkmcnt(2)
	v_mfma_f32_32x32x64_f8f6f4 v[2:17], v[162:169], v[226:233], v[2:17]
	ds_read_b128 v[130:133], v201 offset:0x1000
	ds_read_b128 v[134:137], v202 offset:0x1000
	s_mov_b64 s[38:39], 0
	s_cmp_eq_u32 s98, 0
	s_cbranch_scc1 .LBB0_1278
	v_max3_f32 v191, v98, v99, v100
	v_max3_f32 v191, v191, v101, v102
	v_max3_f32 v191, v191, v103, v104
	v_max3_f32 v191, v191, v105, v106
	v_max3_f32 v191, v191, v107, v108
	v_max3_f32 v191, v191, v109, v110
	v_max3_f32 v191, v191, v111, v112
	v_max_f32 v191, v191, v113
	s_nop 0
	v_max3_f32 v191, v191, v114, v115
	v_max3_f32 v191, v191, v116, v117
	v_max3_f32 v191, v191, v118, v119
	v_max3_f32 v191, v191, v120, v121
	v_max3_f32 v191, v191, v122, v123
	v_max3_f32 v191, v191, v124, v125
	v_max3_f32 v191, v191, v126, v127
	v_max3_f32 v191, v191, v128, v129
	v_mov_b32 v192, v191
	s_nop 1
	v_permlane32_swap_b32 v191, v192
	v_max_f32 v191, v191, v192
	s_nop 0
	v_cmp_ge_f32_e32 vcc, s54, v191
	s_cmp_lg_u64 vcc, exec
	s_cselect_b64 s[38:39], -1, 0
	s_cmp_eq_u64 vcc, exec
	s_cbranch_scc1 .LBB0_1277
	v_add_f32_e32 v82, 0xc0c00000, v191
	v_max_f32_e32 v82, 0, v82
	v_exp_f32_e64 v191, -v82
	v_add_f32_e32 v198, v198, v82
	v_sub_f32_e32 v98, v98, v82
	v_sub_f32_e32 v114, v114, v82
	v_sub_f32_e32 v99, v99, v82
	v_sub_f32_e32 v115, v115, v82
	v_sub_f32_e32 v100, v100, v82
	v_sub_f32_e32 v116, v116, v82
	v_sub_f32_e32 v101, v101, v82
	v_sub_f32_e32 v117, v117, v82
	v_sub_f32_e32 v102, v102, v82
	v_sub_f32_e32 v118, v118, v82
	v_sub_f32_e32 v103, v103, v82
	v_sub_f32_e32 v119, v119, v82
	v_sub_f32_e32 v104, v104, v82
	v_sub_f32_e32 v120, v120, v82
	v_sub_f32_e32 v105, v105, v82
	v_sub_f32_e32 v121, v121, v82
	v_sub_f32_e32 v106, v106, v82
	v_sub_f32_e32 v122, v122, v82
	v_sub_f32_e32 v107, v107, v82
	v_sub_f32_e32 v123, v123, v82
	v_sub_f32_e32 v108, v108, v82
	v_sub_f32_e32 v124, v124, v82
	v_sub_f32_e32 v109, v109, v82
	v_sub_f32_e32 v125, v125, v82
	v_sub_f32_e32 v110, v110, v82
	v_sub_f32_e32 v126, v126, v82
	v_sub_f32_e32 v111, v111, v82
	v_sub_f32_e32 v127, v127, v82
	v_sub_f32_e32 v112, v112, v82
	v_sub_f32_e32 v128, v128, v82
	v_sub_f32_e32 v113, v113, v82
	v_sub_f32_e32 v129, v129, v82
	v_xor_b32_e32 v82, 0x80000000, v198
	v_mov_b32_e32 v83, v82
	v_mov_b32_e32 v84, v82
	v_mov_b32_e32 v85, v82
	v_mov_b32_e32 v86, v82
	v_mov_b32_e32 v87, v82
	v_mov_b32_e32 v88, v82
	v_mov_b32_e32 v89, v82
	v_mov_b32_e32 v90, v82
	v_mov_b32_e32 v91, v82
	v_mov_b32_e32 v92, v82
	v_mov_b32_e32 v93, v82
	v_mov_b32_e32 v94, v82
	v_mov_b32_e32 v95, v82
	v_mov_b32_e32 v96, v82
	v_mov_b32_e32 v97, v82
	s_branch .LBB0_1278

.LBB0_1282:
	s_add_i32 s44, s44, 4
	s_cmpk_lt_u32 s44, 0xfc
	s_cselect_b32 s38, s40, s41
	s_add_i32 s38, s38, s37
	s_addk_i32 s38, 0xff40
	s_ashr_i32 s39, s38, 31
	s_lshl_b64 s[38:39], s[38:39], 10
	s_waitcnt vmcnt(3) lgkmcnt(0)
	s_barrier
	v_lshl_add_u64 v[130:131], v[170:171], 0, s[38:39]
	s_add_i32 m0, s45, 0x1000
	v_cvt_pk_fp8_f32 v162, v98, v99
	global_load_lds_dwordx4 v[130:131], off
	v_lshl_add_u64 v[130:131], v[176:177], 0, s[64:65]
	s_add_i32 m0, s46, 0x4000
	v_cvt_pk_fp8_f32 v163, v102, v103
	global_load_lds_dwordx4 v[130:131], off
	v_lshl_add_u64 v[130:131], v[176:177], 0, s[66:67]
	s_add_i32 m0, s46, 0x5000
	v_cvt_pk_fp8_f32 v162, v100, v101 op_sel:[0,0,1]
	global_load_lds_dwordx4 v[130:131], off
	ds_read_b128 v[130:133], v199 offset:0
	ds_read_b128 v[134:137], v200 offset:0
	ds_read_b128 v[210:213], v199 offset:0x800
	ds_read_b128 v[214:217], v200 offset:0x800
	v_cvt_pk_fp8_f32 v163, v104, v105 op_sel:[0,0,1]
	s_waitcnt lgkmcnt(2)
	v_cvt_pk_fp8_f32 v164, v106, v107
	v_cvt_pk_fp8_f32 v165, v110, v111
	ds_read_b128 v[218:221], v196 offset:0
	ds_read_b128 v[222:225], v197 offset:0
	v_cvt_pk_fp8_f32 v164, v108, v109 op_sel:[0,0,1]
	v_cvt_pk_fp8_f32 v165, v112, v113 op_sel:[0,0,1]
	v_mfma_f32_32x32x64_f8f6f4 v[98:113], v[130:137], v[154:161], v[82:97]
	s_waitcnt lgkmcnt(2)
	v_mfma_f32_32x32x64_f8f6f4 v[130:145], v[210:217], v[154:161], v[82:97]
	v_cvt_pk_fp8_f32 v166, v114, v115
	v_cvt_pk_fp8_f32 v167, v118, v119
	v_cvt_pk_fp8_f32 v168, v122, v123
	v_cvt_pk_fp8_f32 v169, v126, v127
	v_cvt_pk_fp8_f32 v166, v116, v117 op_sel:[0,0,1]
	v_cvt_pk_fp8_f32 v167, v120, v121 op_sel:[0,0,1]
	v_cvt_pk_fp8_f32 v168, v124, v125 op_sel:[0,0,1]
	v_cvt_pk_fp8_f32 v169, v128, v129 op_sel:[0,0,1]
	s_nop 0
	ds_read_b128 v[122:125], v196 offset:0x800
	ds_read_b128 v[126:129], v197 offset:0x800
	s_nop 0
	v_mfma_f32_16x16x128_f8f6f4 v[18:21], v[162:169], v[146:153], v[18:21]
	s_waitcnt lgkmcnt(2)
	v_mfma_f32_32x32x64_f8f6f4 v[2:17], v[162:169], v[218:225], v[2:17]
	ds_read_b128 v[114:117], v196 offset:0x1000
	ds_read_b128 v[118:121], v197 offset:0x1000
	s_mov_b64 s[38:39], 0
	s_cmp_eq_u32 s98, 0
	s_cbranch_scc1 .LBB0_1285
	v_max3_f32 v191, v98, v99, v100
	v_max3_f32 v191, v191, v101, v102
	v_max3_f32 v191, v191, v103, v104
	v_max3_f32 v191, v191, v105, v106
	v_max3_f32 v191, v191, v107, v108
	v_max3_f32 v191, v191, v109, v110
	v_max3_f32 v191, v191, v111, v112
	v_max_f32 v191, v191, v113
	s_nop 0
	v_max3_f32 v191, v191, v130, v131
	v_max3_f32 v191, v191, v132, v133
	v_max3_f32 v191, v191, v134, v135
	v_max3_f32 v191, v191, v136, v137
	v_max3_f32 v191, v191, v138, v139
	v_max3_f32 v191, v191, v140, v141
	v_max3_f32 v191, v191, v142, v143
	v_max3_f32 v191, v191, v144, v145
	v_mov_b32 v192, v191
	s_nop 1
	v_permlane32_swap_b32 v191, v192
	v_max_f32 v191, v191, v192
	s_nop 0
	v_cmp_ge_f32_e32 vcc, s54, v191
	s_cmp_lg_u64 vcc, exec
	s_cselect_b64 s[38:39], -1, 0
	s_cmp_eq_u64 vcc, exec
	s_cbranch_scc1 .LBB0_1284
	v_add_f32_e32 v82, 0xc0c00000, v191
	v_max_f32_e32 v82, 0, v82
	v_exp_f32_e64 v191, -v82
	v_add_f32_e32 v198, v198, v82
	v_sub_f32_e32 v98, v98, v82
	v_sub_f32_e32 v130, v130, v82
	v_sub_f32_e32 v99, v99, v82
	v_sub_f32_e32 v131, v131, v82
	v_sub_f32_e32 v100, v100, v82
	v_sub_f32_e32 v132, v132, v82
	v_sub_f32_e32 v101, v101, v82
	v_sub_f32_e32 v133, v133, v82
	v_sub_f32_e32 v102, v102, v82
	v_sub_f32_e32 v134, v134, v82
	v_sub_f32_e32 v103, v103, v82
	v_sub_f32_e32 v135, v135, v82
	v_sub_f32_e32 v104, v104, v82
	v_sub_f32_e32 v136, v136, v82
	v_sub_f32_e32 v105, v105, v82
	v_sub_f32_e32 v137, v137, v82
	v_sub_f32_e32 v106, v106, v82
	v_sub_f32_e32 v138, v138, v82
	v_sub_f32_e32 v107, v107, v82
	v_sub_f32_e32 v139, v139, v82
	v_sub_f32_e32 v108, v108, v82
	v_sub_f32_e32 v140, v140, v82
	v_sub_f32_e32 v109, v109, v82
	v_sub_f32_e32 v141, v141, v82
	v_sub_f32_e32 v110, v110, v82
	v_sub_f32_e32 v142, v142, v82
	v_sub_f32_e32 v111, v111, v82
	v_sub_f32_e32 v143, v143, v82
	v_sub_f32_e32 v112, v112, v82
	v_sub_f32_e32 v144, v144, v82
	v_sub_f32_e32 v113, v113, v82
	v_sub_f32_e32 v145, v145, v82
	v_xor_b32_e32 v82, 0x80000000, v198
	v_mov_b32_e32 v83, v82
	v_mov_b32_e32 v84, v82
	v_mov_b32_e32 v85, v82
	v_mov_b32_e32 v86, v82
	v_mov_b32_e32 v87, v82
	v_mov_b32_e32 v88, v82
	v_mov_b32_e32 v89, v82
	v_mov_b32_e32 v90, v82
	v_mov_b32_e32 v91, v82
	v_mov_b32_e32 v92, v82
	v_mov_b32_e32 v93, v82
	v_mov_b32_e32 v94, v82
	v_mov_b32_e32 v95, v82
	v_mov_b32_e32 v96, v82
	v_mov_b32_e32 v97, v82
	s_branch .LBB0_1285

.LBB0_1289:
	s_cmpk_lt_u32 s44, 0xfb
	s_cselect_b32 s38, s42, s43
	s_add_i32 s38, s38, s37
	s_addk_i32 s38, 0xff40
	s_ashr_i32 s39, s38, 31
	s_lshl_b64 s[38:39], s[38:39], 10
	s_waitcnt vmcnt(3) lgkmcnt(0)
	s_barrier
	v_lshl_add_u64 v[114:115], v[170:171], 0, s[38:39]
	s_add_i32 m0, s45, 0x2000
	v_cvt_pk_fp8_f32 v162, v98, v99
	global_load_lds_dwordx4 v[114:115], off
	v_lshl_add_u64 v[114:115], v[176:177], 0, s[68:69]
	s_add_i32 m0, s46, 0x6000
	v_cvt_pk_fp8_f32 v163, v102, v103
	global_load_lds_dwordx4 v[114:115], off
	v_lshl_add_u64 v[114:115], v[176:177], 0, s[70:71]
	s_add_i32 m0, s46, 0x7000
	v_cvt_pk_fp8_f32 v162, v100, v101 op_sel:[0,0,1]
	global_load_lds_dwordx4 v[114:115], off
	ds_read_b128 v[210:213], v183 offset:0
	ds_read_b128 v[214:217], v190 offset:0
	ds_read_b128 v[218:221], v183 offset:0x800
	ds_read_b128 v[222:225], v190 offset:0x800
	v_cvt_pk_fp8_f32 v163, v104, v105 op_sel:[0,0,1]
	s_waitcnt lgkmcnt(2)
	v_mfma_f32_32x32x64_f8f6f4 v[114:129], v[210:217], v[154:161], v[82:97]
	v_cvt_pk_fp8_f32 v164, v106, v107
	v_cvt_pk_fp8_f32 v165, v110, v111
	ds_read_b128 v[226:229], v194 offset:0
	ds_read_b128 v[230:233], v195 offset:0
	v_cvt_pk_fp8_f32 v164, v108, v109 op_sel:[0,0,1]
	v_cvt_pk_fp8_f32 v165, v112, v113 op_sel:[0,0,1]
	s_waitcnt lgkmcnt(2)
	v_mfma_f32_32x32x64_f8f6f4 v[98:113], v[218:225], v[154:161], v[82:97]
	v_cvt_pk_fp8_f32 v166, v130, v131
	v_cvt_pk_fp8_f32 v167, v134, v135
	v_cvt_pk_fp8_f32 v168, v138, v139
	v_cvt_pk_fp8_f32 v169, v142, v143
	v_cvt_pk_fp8_f32 v166, v132, v133 op_sel:[0,0,1]
	v_cvt_pk_fp8_f32 v167, v136, v137 op_sel:[0,0,1]
	v_cvt_pk_fp8_f32 v168, v140, v141 op_sel:[0,0,1]
	v_cvt_pk_fp8_f32 v169, v144, v145 op_sel:[0,0,1]
	s_nop 0
	ds_read_b128 v[138:141], v194 offset:0x800
	ds_read_b128 v[142:145], v195 offset:0x800
	s_nop 0
	v_mfma_f32_16x16x128_f8f6f4 v[18:21], v[162:169], v[146:153], v[18:21]
	s_waitcnt lgkmcnt(2)
	v_mfma_f32_32x32x64_f8f6f4 v[2:17], v[162:169], v[226:233], v[2:17]
	ds_read_b128 v[130:133], v194 offset:0x1000
	ds_read_b128 v[134:137], v195 offset:0x1000
	s_mov_b64 s[38:39], 0
	s_cmp_eq_u32 s98, 0
	s_cbranch_scc1 .LBB0_1292
	v_max3_f32 v176, v114, v115, v116
	v_max3_f32 v176, v176, v117, v118
	v_max3_f32 v176, v176, v119, v120
	v_max3_f32 v176, v176, v121, v122
	v_max3_f32 v176, v176, v123, v124
	v_max3_f32 v176, v176, v125, v126
	v_max3_f32 v176, v176, v127, v128
	v_max_f32 v176, v176, v129
	s_nop 0
	v_max3_f32 v176, v176, v98, v99
	v_max3_f32 v176, v176, v100, v101
	v_max3_f32 v176, v176, v102, v103
	v_max3_f32 v176, v176, v104, v105
	v_max3_f32 v176, v176, v106, v107
	v_max3_f32 v176, v176, v108, v109
	v_max3_f32 v176, v176, v110, v111
	v_max3_f32 v176, v176, v112, v113
	v_mov_b32 v177, v176
	s_nop 1
	v_permlane32_swap_b32 v176, v177
	v_max_f32 v176, v176, v177
	s_nop 0
	v_cmp_ge_f32_e32 vcc, s54, v176
	s_cmp_lg_u64 vcc, exec
	s_cselect_b64 s[38:39], -1, 0
	s_cmp_eq_u64 vcc, exec
	s_cbranch_scc1 .LBB0_1291
	v_add_f32_e32 v82, 0xc0c00000, v176
	v_max_f32_e32 v82, 0, v82
	v_exp_f32_e64 v176, -v82
	v_add_f32_e32 v198, v198, v82
	v_sub_f32_e32 v114, v114, v82
	v_sub_f32_e32 v98, v98, v82
	v_sub_f32_e32 v115, v115, v82
	v_sub_f32_e32 v99, v99, v82
	v_sub_f32_e32 v116, v116, v82
	v_sub_f32_e32 v100, v100, v82
	v_sub_f32_e32 v117, v117, v82
	v_sub_f32_e32 v101, v101, v82
	v_sub_f32_e32 v118, v118, v82
	v_sub_f32_e32 v102, v102, v82
	v_sub_f32_e32 v119, v119, v82
	v_sub_f32_e32 v103, v103, v82
	v_sub_f32_e32 v120, v120, v82
	v_sub_f32_e32 v104, v104, v82
	v_sub_f32_e32 v121, v121, v82
	v_sub_f32_e32 v105, v105, v82
	v_sub_f32_e32 v122, v122, v82
	v_sub_f32_e32 v106, v106, v82
	v_sub_f32_e32 v123, v123, v82
	v_sub_f32_e32 v107, v107, v82
	v_sub_f32_e32 v124, v124, v82
	v_sub_f32_e32 v108, v108, v82
	v_sub_f32_e32 v125, v125, v82
	v_sub_f32_e32 v109, v109, v82
	v_sub_f32_e32 v126, v126, v82
	v_sub_f32_e32 v110, v110, v82
	v_sub_f32_e32 v127, v127, v82
	v_sub_f32_e32 v111, v111, v82
	v_sub_f32_e32 v128, v128, v82
	v_sub_f32_e32 v112, v112, v82
	v_sub_f32_e32 v129, v129, v82
	v_sub_f32_e32 v113, v113, v82
	v_xor_b32_e32 v82, 0x80000000, v198
	v_mov_b32_e32 v83, v82
	v_mov_b32_e32 v84, v82
	v_mov_b32_e32 v85, v82
	v_mov_b32_e32 v86, v82
	v_mov_b32_e32 v87, v82
	v_mov_b32_e32 v88, v82
	v_mov_b32_e32 v89, v82
	v_mov_b32_e32 v90, v82
	v_mov_b32_e32 v91, v82
	v_mov_b32_e32 v92, v82
	v_mov_b32_e32 v93, v82
	v_mov_b32_e32 v94, v82
	v_mov_b32_e32 v95, v82
	v_mov_b32_e32 v96, v82
	v_mov_b32_e32 v97, v82
	s_branch .LBB0_1292

.LBB0_1295:
	s_ashr_i32 s95, s94, 31
	s_lshl_b64 s[38:39], s[94:95], 10
	s_add_u32 s28, s28, s38
	s_addc_u32 s29, s29, s39
	v_mov_b32_e32 v183, v181
	v_lshl_add_u64 v[130:131], s[28:29], 0, v[180:181]
	s_mov_b64 s[28:29], 0x2030000
	s_mov_b32 m0, s49
	v_lshl_add_u64 v[130:131], v[130:131], 0, s[28:29]
	v_lshl_add_u64 v[170:171], s[90:91], 0, v[182:183]
	s_mov_b64 s[28:29], 0x204000
	global_load_lds_dwordx4 v[130:131], off
	v_lshl_add_u64 v[130:131], v[170:171], 0, s[28:29]
	s_mov_b32 m0, s47
	s_mov_b64 s[28:29], 0x205000
	global_load_lds_dwordx4 v[130:131], off
	v_lshl_add_u64 v[130:131], v[170:171], 0, s[28:29]
	s_mov_b32 m0, s48
	v_cvt_pk_fp8_f32 v162, v114, v115
	global_load_lds_dwordx4 v[130:131], off
	v_cvt_pk_fp8_f32 v163, v118, v119
	ds_read_b128 v[130:133], v205 offset:0
	ds_read_b128 v[134:137], v206 offset:0
	ds_read_b128 v[210:213], v205 offset:0x800
	ds_read_b128 v[214:217], v206 offset:0x800
	v_cvt_pk_fp8_f32 v162, v116, v117 op_sel:[0,0,1]
	v_cvt_pk_fp8_f32 v163, v120, v121 op_sel:[0,0,1]
	s_waitcnt lgkmcnt(2)
	v_cvt_pk_fp8_f32 v164, v122, v123
	v_cvt_pk_fp8_f32 v165, v126, v127
	ds_read_b128 v[218:221], v188 offset:0
	ds_read_b128 v[222:225], v189 offset:0
	v_cvt_pk_fp8_f32 v164, v124, v125 op_sel:[0,0,1]
	v_cvt_pk_fp8_f32 v165, v128, v129 op_sel:[0,0,1]
	v_mfma_f32_32x32x64_f8f6f4 v[114:129], v[130:137], v[154:161], v[82:97]
	s_waitcnt lgkmcnt(2)
	v_mfma_f32_32x32x64_f8f6f4 v[130:145], v[210:217], v[154:161], v[82:97]
	v_cvt_pk_fp8_f32 v166, v98, v99
	v_cvt_pk_fp8_f32 v167, v102, v103
	v_cvt_pk_fp8_f32 v168, v106, v107
	v_cvt_pk_fp8_f32 v169, v110, v111
	v_cvt_pk_fp8_f32 v166, v100, v101 op_sel:[0,0,1]
	v_cvt_pk_fp8_f32 v167, v104, v105 op_sel:[0,0,1]
	v_cvt_pk_fp8_f32 v168, v108, v109 op_sel:[0,0,1]
	v_cvt_pk_fp8_f32 v169, v112, v113 op_sel:[0,0,1]
	s_nop 0
	ds_read_b128 v[106:109], v188 offset:0x800
	ds_read_b128 v[110:113], v189 offset:0x800
	s_nop 0
	v_mfma_f32_16x16x128_f8f6f4 v[18:21], v[162:169], v[146:153], v[18:21]
	s_waitcnt lgkmcnt(2)
	v_mfma_f32_32x32x64_f8f6f4 v[2:17], v[162:169], v[218:225], v[2:17]
	ds_read_b128 v[98:101], v188 offset:0x1000
	ds_read_b128 v[102:105], v189 offset:0x1000
	s_mov_b64 s[28:29], 0
	s_cmp_eq_u32 s98, 0
	s_cbranch_scc1 .LBB0_1298
	v_max3_f32 v172, v114, v115, v116
	v_max3_f32 v172, v172, v117, v118
	v_max3_f32 v172, v172, v119, v120
	v_max3_f32 v172, v172, v121, v122
	v_max3_f32 v172, v172, v123, v124
	v_max3_f32 v172, v172, v125, v126
	v_max3_f32 v172, v172, v127, v128
	v_max_f32 v172, v172, v129
	s_nop 0
	v_max3_f32 v172, v172, v130, v131
	v_max3_f32 v172, v172, v132, v133
	v_max3_f32 v172, v172, v134, v135
	v_max3_f32 v172, v172, v136, v137
	v_max3_f32 v172, v172, v138, v139
	v_max3_f32 v172, v172, v140, v141
	v_max3_f32 v172, v172, v142, v143
	v_max3_f32 v172, v172, v144, v145
	v_mov_b32 v173, v172
	s_nop 1
	v_permlane32_swap_b32 v172, v173
	v_max_f32 v172, v172, v173
	s_nop 0
	v_cmp_ge_f32_e32 vcc, s54, v172
	s_cmp_lg_u64 vcc, exec
	s_cselect_b64 s[28:29], -1, 0
	s_cmp_eq_u64 vcc, exec
	s_cbranch_scc1 .LBB0_1297
	v_add_f32_e32 v82, 0xc0c00000, v172
	v_max_f32_e32 v82, 0, v82
	v_exp_f32_e64 v172, -v82
	v_add_f32_e32 v198, v198, v82
	v_sub_f32_e32 v114, v114, v82
	v_sub_f32_e32 v130, v130, v82
	v_sub_f32_e32 v115, v115, v82
	v_sub_f32_e32 v131, v131, v82
	v_sub_f32_e32 v116, v116, v82
	v_sub_f32_e32 v132, v132, v82
	v_sub_f32_e32 v117, v117, v82
	v_sub_f32_e32 v133, v133, v82
	v_sub_f32_e32 v118, v118, v82
	v_sub_f32_e32 v134, v134, v82
	v_sub_f32_e32 v119, v119, v82
	v_sub_f32_e32 v135, v135, v82
	v_sub_f32_e32 v120, v120, v82
	v_sub_f32_e32 v136, v136, v82
	v_sub_f32_e32 v121, v121, v82
	v_sub_f32_e32 v137, v137, v82
	v_sub_f32_e32 v122, v122, v82
	v_sub_f32_e32 v138, v138, v82
	v_sub_f32_e32 v123, v123, v82
	v_sub_f32_e32 v139, v139, v82
	v_sub_f32_e32 v124, v124, v82
	v_sub_f32_e32 v140, v140, v82
	v_sub_f32_e32 v125, v125, v82
	v_sub_f32_e32 v141, v141, v82
	v_sub_f32_e32 v126, v126, v82
	v_sub_f32_e32 v142, v142, v82
	v_sub_f32_e32 v127, v127, v82
	v_sub_f32_e32 v143, v143, v82
	v_sub_f32_e32 v128, v128, v82
	v_sub_f32_e32 v144, v144, v82
	v_sub_f32_e32 v129, v129, v82
	v_sub_f32_e32 v145, v145, v82
	v_xor_b32_e32 v82, 0x80000000, v198
	v_mov_b32_e32 v83, v82
	v_mov_b32_e32 v84, v82
	v_mov_b32_e32 v85, v82
	v_mov_b32_e32 v86, v82
	v_mov_b32_e32 v87, v82
	v_mov_b32_e32 v88, v82
	v_mov_b32_e32 v89, v82
	v_mov_b32_e32 v90, v82
	v_mov_b32_e32 v91, v82
	v_mov_b32_e32 v92, v82
	v_mov_b32_e32 v93, v82
	v_mov_b32_e32 v94, v82
	v_mov_b32_e32 v95, v82
	v_mov_b32_e32 v96, v82
	v_mov_b32_e32 v97, v82
	s_branch .LBB0_1298

.LBB0_1302:
	s_mov_b32 m0, s51
	s_waitcnt vmcnt(3) lgkmcnt(0)
	s_barrier
	v_lshl_add_u64 v[98:99], v[170:171], 0, s[82:83]
	global_load_lds_dwordx4 v[98:99], off
	v_lshl_add_u64 v[98:99], v[170:171], 0, s[84:85]
	s_mov_b32 m0, s50
	v_cvt_pk_fp8_f32 v162, v114, v115
	global_load_lds_dwordx4 v[98:99], off
	v_cvt_pk_fp8_f32 v163, v118, v119
	ds_read_b128 v[170:173], v203 offset:0
	ds_read_b128 v[174:177], v204 offset:0
	ds_read_b128 v[210:213], v203 offset:0x800
	ds_read_b128 v[214:217], v204 offset:0x800
	v_cvt_pk_fp8_f32 v162, v116, v117 op_sel:[0,0,1]
	v_cvt_pk_fp8_f32 v163, v120, v121 op_sel:[0,0,1]
	s_waitcnt lgkmcnt(2)
	v_mfma_f32_32x32x64_f8f6f4 v[98:113], v[170:177], v[154:161], v[82:97]
	v_cvt_pk_fp8_f32 v164, v122, v123
	v_cvt_pk_fp8_f32 v165, v126, v127
	ds_read_b128 v[218:221], v201 offset:0
	ds_read_b128 v[222:225], v202 offset:0
	v_cvt_pk_fp8_f32 v164, v124, v125 op_sel:[0,0,1]
	v_cvt_pk_fp8_f32 v165, v128, v129 op_sel:[0,0,1]
	s_waitcnt lgkmcnt(2)
	v_mfma_f32_32x32x64_f8f6f4 v[114:129], v[210:217], v[154:161], v[82:97]
	v_cvt_pk_fp8_f32 v166, v130, v131
	v_cvt_pk_fp8_f32 v167, v134, v135
	v_cvt_pk_fp8_f32 v168, v138, v139
	v_cvt_pk_fp8_f32 v169, v142, v143
	v_cvt_pk_fp8_f32 v166, v132, v133 op_sel:[0,0,1]
	v_cvt_pk_fp8_f32 v167, v136, v137 op_sel:[0,0,1]
	v_cvt_pk_fp8_f32 v168, v140, v141 op_sel:[0,0,1]
	v_cvt_pk_fp8_f32 v169, v144, v145 op_sel:[0,0,1]
	s_nop 0
	ds_read_b128 v[138:141], v201 offset:0x800
	ds_read_b128 v[142:145], v202 offset:0x800
	s_nop 0
	v_mfma_f32_16x16x128_f8f6f4 v[18:21], v[162:169], v[146:153], v[18:21]
	s_waitcnt lgkmcnt(2)
	v_mfma_f32_32x32x64_f8f6f4 v[2:17], v[162:169], v[218:225], v[2:17]
	ds_read_b128 v[130:133], v201 offset:0x1000
	ds_read_b128 v[134:137], v202 offset:0x1000
	s_mov_b64 s[28:29], 0
	s_cmp_eq_u32 s98, 0
	s_cbranch_scc1 .LBB0_1305
	v_max3_f32 v170, v98, v99, v100
	v_max3_f32 v170, v170, v101, v102
	v_max3_f32 v170, v170, v103, v104
	v_max3_f32 v170, v170, v105, v106
	v_max3_f32 v170, v170, v107, v108
	v_max3_f32 v170, v170, v109, v110
	v_max3_f32 v170, v170, v111, v112
	v_max_f32 v170, v170, v113
	s_nop 0
	v_max3_f32 v170, v170, v114, v115
	v_max3_f32 v170, v170, v116, v117
	v_max3_f32 v170, v170, v118, v119
	v_max3_f32 v170, v170, v120, v121
	v_max3_f32 v170, v170, v122, v123
	v_max3_f32 v170, v170, v124, v125
	v_max3_f32 v170, v170, v126, v127
	v_max3_f32 v170, v170, v128, v129
	v_mov_b32 v171, v170
	s_nop 1
	v_permlane32_swap_b32 v170, v171
	v_max_f32 v170, v170, v171
	s_nop 0
	v_cmp_ge_f32_e32 vcc, s54, v170
	s_cmp_lg_u64 vcc, exec
	s_cselect_b64 s[28:29], -1, 0
	s_cmp_eq_u64 vcc, exec
	s_cbranch_scc1 .LBB0_1304
	v_add_f32_e32 v82, 0xc0c00000, v170
	v_max_f32_e32 v82, 0, v82
	v_exp_f32_e64 v170, -v82
	v_add_f32_e32 v198, v198, v82
	v_sub_f32_e32 v98, v98, v82
	v_sub_f32_e32 v114, v114, v82
	v_sub_f32_e32 v99, v99, v82
	v_sub_f32_e32 v115, v115, v82
	v_sub_f32_e32 v100, v100, v82
	v_sub_f32_e32 v116, v116, v82
	v_sub_f32_e32 v101, v101, v82
	v_sub_f32_e32 v117, v117, v82
	v_sub_f32_e32 v102, v102, v82
	v_sub_f32_e32 v118, v118, v82
	v_sub_f32_e32 v103, v103, v82
	v_sub_f32_e32 v119, v119, v82
	v_sub_f32_e32 v104, v104, v82
	v_sub_f32_e32 v120, v120, v82
	v_sub_f32_e32 v105, v105, v82
	v_sub_f32_e32 v121, v121, v82
	v_sub_f32_e32 v106, v106, v82
	v_sub_f32_e32 v122, v122, v82
	v_sub_f32_e32 v107, v107, v82
	v_sub_f32_e32 v123, v123, v82
	v_sub_f32_e32 v108, v108, v82
	v_sub_f32_e32 v124, v124, v82
	v_sub_f32_e32 v109, v109, v82
	v_sub_f32_e32 v125, v125, v82
	v_sub_f32_e32 v110, v110, v82
	v_sub_f32_e32 v126, v126, v82
	v_sub_f32_e32 v111, v111, v82
	v_sub_f32_e32 v127, v127, v82
	v_sub_f32_e32 v112, v112, v82
	v_sub_f32_e32 v128, v128, v82
	v_sub_f32_e32 v113, v113, v82
	v_sub_f32_e32 v129, v129, v82
	v_xor_b32_e32 v82, 0x80000000, v198
	v_mov_b32_e32 v83, v82
	v_mov_b32_e32 v84, v82
	v_mov_b32_e32 v85, v82
	v_mov_b32_e32 v86, v82
	v_mov_b32_e32 v87, v82
	v_mov_b32_e32 v88, v82
	v_mov_b32_e32 v89, v82
	v_mov_b32_e32 v90, v82
	v_mov_b32_e32 v91, v82
	v_mov_b32_e32 v92, v82
	v_mov_b32_e32 v93, v82
	v_mov_b32_e32 v94, v82
	v_mov_b32_e32 v95, v82
	v_mov_b32_e32 v96, v82
	v_mov_b32_e32 v97, v82
	s_branch .LBB0_1305

.LBB0_1309:
	s_waitcnt vmcnt(0) lgkmcnt(0)
	s_barrier
	v_cvt_pk_fp8_f32 v162, v98, v99
	v_cvt_pk_fp8_f32 v163, v102, v103
	ds_read_b128 v[130:133], v199 offset:0
	ds_read_b128 v[134:137], v200 offset:0
	ds_read_b128 v[170:173], v199 offset:0x800
	ds_read_b128 v[174:177], v200 offset:0x800
	v_cvt_pk_fp8_f32 v162, v100, v101 op_sel:[0,0,1]
	v_cvt_pk_fp8_f32 v163, v104, v105 op_sel:[0,0,1]
	s_waitcnt lgkmcnt(2)
	v_cvt_pk_fp8_f32 v164, v106, v107
	v_cvt_pk_fp8_f32 v165, v110, v111
	ds_read_b128 v[200:203], v196 offset:0
	ds_read_b128 v[204:207], v197 offset:0
	v_cvt_pk_fp8_f32 v164, v108, v109 op_sel:[0,0,1]
	v_cvt_pk_fp8_f32 v165, v112, v113 op_sel:[0,0,1]
	v_mfma_f32_32x32x64_f8f6f4 v[98:113], v[130:137], v[154:161], v[82:97]
	s_waitcnt lgkmcnt(2)
	v_mfma_f32_32x32x64_f8f6f4 v[82:97], v[170:177], v[154:161], v[82:97]
	v_cvt_pk_fp8_f32 v166, v114, v115
	v_cvt_pk_fp8_f32 v167, v118, v119
	v_cvt_pk_fp8_f32 v168, v122, v123
	v_cvt_pk_fp8_f32 v169, v126, v127
	v_cvt_pk_fp8_f32 v166, v116, v117 op_sel:[0,0,1]
	v_cvt_pk_fp8_f32 v167, v120, v121 op_sel:[0,0,1]
	v_cvt_pk_fp8_f32 v168, v124, v125 op_sel:[0,0,1]
	v_cvt_pk_fp8_f32 v169, v128, v129 op_sel:[0,0,1]
	s_nop 0
	ds_read_b128 v[138:141], v196 offset:0x800
	ds_read_b128 v[142:145], v197 offset:0x800
	s_nop 0
	v_mfma_f32_16x16x128_f8f6f4 v[18:21], v[162:169], v[146:153], v[18:21]
	s_waitcnt lgkmcnt(2)
	v_mfma_f32_32x32x64_f8f6f4 v[2:17], v[162:169], v[200:207], v[2:17]
	ds_read_b128 v[130:133], v196 offset:0x1000
	ds_read_b128 v[134:137], v197 offset:0x1000
	s_mov_b64 s[28:29], 0
	s_cmp_eq_u32 s98, 0
	s_cbranch_scc1 .LBB0_1312
	v_max3_f32 v114, v98, v99, v100
	v_max3_f32 v114, v114, v101, v102
	v_max3_f32 v114, v114, v103, v104
	v_max3_f32 v114, v114, v105, v106
	v_max3_f32 v114, v114, v107, v108
	v_max3_f32 v114, v114, v109, v110
	v_max3_f32 v114, v114, v111, v112
	v_max_f32 v114, v114, v113
	s_nop 0
	v_max3_f32 v114, v114, v82, v83
	v_max3_f32 v114, v114, v84, v85
	v_max3_f32 v114, v114, v86, v87
	v_max3_f32 v114, v114, v88, v89
	v_max3_f32 v114, v114, v90, v91
	v_max3_f32 v114, v114, v92, v93
	v_max3_f32 v114, v114, v94, v95
	v_max3_f32 v114, v114, v96, v97
	v_mov_b32 v115, v114
	s_nop 1
	v_permlane32_swap_b32 v114, v115
	v_max_f32 v114, v114, v115
	s_nop 0
	v_cmp_ge_f32_e32 vcc, s54, v114
	s_cmp_lg_u64 vcc, exec
	s_cselect_b64 s[28:29], -1, 0
	s_cmp_eq_u64 vcc, exec
	s_cbranch_scc1 .LBB0_1311
	v_add_f32_e32 v114, 0xc0c00000, v114
	v_max_f32_e32 v114, 0, v114
	v_exp_f32_e64 v154, -v114
	v_sub_f32_e32 v98, v98, v114
	v_sub_f32_e32 v82, v82, v114
	v_sub_f32_e32 v99, v99, v114
	v_sub_f32_e32 v83, v83, v114
	v_sub_f32_e32 v100, v100, v114
	v_sub_f32_e32 v84, v84, v114
	v_sub_f32_e32 v101, v101, v114
	v_sub_f32_e32 v85, v85, v114
	v_sub_f32_e32 v102, v102, v114
	v_sub_f32_e32 v86, v86, v114
	v_sub_f32_e32 v103, v103, v114
	v_sub_f32_e32 v87, v87, v114
	v_sub_f32_e32 v104, v104, v114
	v_sub_f32_e32 v88, v88, v114
	v_sub_f32_e32 v105, v105, v114
	v_sub_f32_e32 v89, v89, v114
	v_sub_f32_e32 v106, v106, v114
	v_sub_f32_e32 v90, v90, v114
	v_sub_f32_e32 v107, v107, v114
	v_sub_f32_e32 v91, v91, v114
	v_sub_f32_e32 v108, v108, v114
	v_sub_f32_e32 v92, v92, v114
	v_sub_f32_e32 v109, v109, v114
	v_sub_f32_e32 v93, v93, v114
	v_sub_f32_e32 v110, v110, v114
	v_sub_f32_e32 v94, v94, v114
	v_sub_f32_e32 v111, v111, v114
	v_sub_f32_e32 v95, v95, v114
	v_sub_f32_e32 v112, v112, v114
	v_sub_f32_e32 v96, v96, v114
	v_sub_f32_e32 v113, v113, v114
	v_sub_f32_e32 v97, v97, v114
	v_add_f32_e32 v114, v198, v114
	v_xor_b32_e32 v114, 0x80000000, v114
	v_mov_b32_e32 v115, v114
	v_mov_b32_e32 v116, v114
	v_mov_b32_e32 v117, v114
	v_mov_b32_e32 v118, v114
	v_mov_b32_e32 v119, v114
	v_mov_b32_e32 v120, v114
	v_mov_b32_e32 v121, v114
	v_mov_b32_e32 v122, v114
	v_mov_b32_e32 v123, v114
	v_mov_b32_e32 v124, v114
	v_mov_b32_e32 v125, v114
	v_mov_b32_e32 v126, v114
	v_mov_b32_e32 v127, v114
	v_mov_b32_e32 v128, v114
	v_mov_b32_e32 v129, v114
	s_branch .LBB0_1312

.LBB0_1317:
	s_nop 15
	v_add_f32_e32 v248, v18, v19
	v_add_f32_e32 v249, v20, v21
	v_add_f32_e32 v248, v248, v249
	v_cmp_u_f32_e64 s[100:101], v248, v248
	s_nop 1
	s_cmp_lg_u64 s[100:101], 0
	s_cselect_b32 s100, 1, 0
	s_or_b32 s99, s99, s100
	s_mov_b64 s[100:101], exec
	s_mov_b32 exec_lo, 0x30003
	s_mov_b32 exec_hi, 0x30003
	ds_write_b128 v250, v[18:21] offset:49152
	s_mov_b64 exec, s[100:101]
	v_add_u32_e32 v249, s78, v186
	s_waitcnt lgkmcnt(0)
	ds_read_b128 v[30:33], v249 offset:49248
	ds_read_b128 v[26:29], v249 offset:49216
	ds_read_b128 v[22:25], v249 offset:49184
	ds_read_b128 v[18:21], v249 offset:49152
	s_waitcnt lgkmcnt(0)
	v_rcp_f32_e32 v18, v18
	v_rcp_f32_e32 v19, v19
	v_rcp_f32_e32 v20, v20
	v_rcp_f32_e32 v21, v21
	v_rcp_f32_e32 v22, v22
	v_rcp_f32_e32 v23, v23
	v_mul_f32_e32 v2, v2, v18
	v_mul_f32_e32 v34, v34, v18
	v_mul_f32_e32 v50, v50, v18
	v_mul_f32_e32 v18, v66, v18
	v_rcp_f32_e32 v24, v24
	v_rcp_f32_e32 v25, v25
	v_mov_b32_e32 v66, v179
	v_mul_f32_e32 v3, v3, v19
	v_rcp_f32_e32 v26, v26
	v_rcp_f32_e32 v27, v27
	s_waitcnt vmcnt(0) lgkmcnt(0)
	s_barrier
	v_cvt_pk_bf16_f32 v2, v2, v3
	v_mul_f32_e32 v4, v4, v20
	v_mul_f32_e32 v5, v5, v21
	v_rcp_f32_e32 v28, v28
	v_rcp_f32_e32 v29, v29
	ds_write_b32 v66, v2
	v_cvt_pk_bf16_f32 v2, v4, v5
	v_mul_f32_e32 v6, v6, v22
	v_mul_f32_e32 v7, v7, v23
	v_rcp_f32_e32 v30, v30
	v_rcp_f32_e32 v31, v31
	ds_write_b32 v66, v2 offset:2048
	v_cvt_pk_bf16_f32 v2, v6, v7
	v_mul_f32_e32 v8, v8, v24
	v_mul_f32_e32 v9, v9, v25
	v_rcp_f32_e32 v32, v32
	v_rcp_f32_e32 v33, v33
	ds_write_b32 v66, v2 offset:4096
	v_cvt_pk_bf16_f32 v2, v8, v9
	v_mul_f32_e32 v10, v10, v26
	v_mul_f32_e32 v11, v11, v27
	ds_write_b32 v66, v2 offset:6144
	v_cvt_pk_bf16_f32 v2, v10, v11
	v_mul_f32_e32 v12, v12, v28
	v_mul_f32_e32 v13, v13, v29
	ds_write_b32 v66, v2 offset:8192
	v_cvt_pk_bf16_f32 v2, v12, v13
	v_mul_f32_e32 v14, v14, v30
	v_mul_f32_e32 v15, v15, v31
	ds_write_b32 v66, v2 offset:10240
	v_cvt_pk_bf16_f32 v2, v14, v15
	v_mul_f32_e32 v16, v16, v32
	v_mul_f32_e32 v17, v17, v33
	ds_write_b32 v66, v2 offset:12288
	v_cvt_pk_bf16_f32 v2, v16, v17
	v_mul_f32_e32 v35, v35, v19
	ds_write_b32 v66, v2 offset:14336
	v_cvt_pk_bf16_f32 v2, v34, v35
	v_mul_f32_e32 v36, v36, v20
	v_mul_f32_e32 v37, v37, v21
	ds_write_b32 v66, v2 offset:16384
	v_cvt_pk_bf16_f32 v2, v36, v37
	v_mul_f32_e32 v38, v38, v22
	v_mul_f32_e32 v39, v39, v23
	ds_write_b32 v66, v2 offset:18432
	v_cvt_pk_bf16_f32 v2, v38, v39
	v_mul_f32_e32 v40, v40, v24
	v_mul_f32_e32 v41, v41, v25
	ds_write_b32 v66, v2 offset:20480
	v_cvt_pk_bf16_f32 v2, v40, v41
	v_mul_f32_e32 v42, v42, v26
	v_mul_f32_e32 v43, v43, v27
	ds_write_b32 v66, v2 offset:22528
	v_cvt_pk_bf16_f32 v2, v42, v43
	v_mul_f32_e32 v44, v44, v28
	v_mul_f32_e32 v45, v45, v29
	ds_write_b32 v66, v2 offset:24576
	v_cvt_pk_bf16_f32 v2, v44, v45
	v_mul_f32_e32 v46, v46, v30
	v_mul_f32_e32 v47, v47, v31
	ds_write_b32 v66, v2 offset:26624
	v_cvt_pk_bf16_f32 v2, v46, v47
	v_mul_f32_e32 v48, v48, v32
	v_mul_f32_e32 v49, v49, v33
	ds_write_b32 v66, v2 offset:28672
	v_cvt_pk_bf16_f32 v2, v48, v49
	v_mul_f32_e32 v51, v51, v19
	ds_write_b32 v66, v2 offset:30720
	v_cvt_pk_bf16_f32 v2, v50, v51
	v_mul_f32_e32 v52, v52, v20
	v_mul_f32_e32 v53, v53, v21
	ds_write_b32 v66, v2 offset:32768
	v_cvt_pk_bf16_f32 v2, v52, v53
	v_mul_f32_e32 v54, v54, v22
	v_mul_f32_e32 v55, v55, v23
	ds_write_b32 v66, v2 offset:34816
	v_cvt_pk_bf16_f32 v2, v54, v55
	v_mul_f32_e32 v56, v56, v24
	v_mul_f32_e32 v57, v57, v25
	ds_write_b32 v66, v2 offset:36864
	v_cvt_pk_bf16_f32 v2, v56, v57
	v_mul_f32_e32 v58, v58, v26
	v_mul_f32_e32 v59, v59, v27
	ds_write_b32 v66, v2 offset:38912
	v_cvt_pk_bf16_f32 v2, v58, v59
	v_mul_f32_e32 v60, v60, v28
	v_mul_f32_e32 v61, v61, v29
	ds_write_b32 v66, v2 offset:40960
	v_cvt_pk_bf16_f32 v2, v60, v61
	v_mul_f32_e32 v62, v62, v30
	v_mul_f32_e32 v63, v63, v31
	ds_write_b32 v66, v2 offset:43008
	v_cvt_pk_bf16_f32 v2, v62, v63
	v_mul_f32_e32 v64, v64, v32
	v_mul_f32_e32 v65, v65, v33
	ds_write_b32 v66, v2 offset:45056
	v_cvt_pk_bf16_f32 v2, v64, v65
	v_mul_f32_e32 v19, v67, v19
	ds_write_b32 v66, v2 offset:47104
	v_cvt_pk_bf16_f32 v2, v18, v19
	v_mul_f32_e32 v20, v68, v20
	v_mul_f32_e32 v21, v69, v21
	ds_write_b32 v66, v2 offset:49152
	v_cvt_pk_bf16_f32 v2, v20, v21
	v_mul_f32_e32 v22, v70, v22
	v_mul_f32_e32 v23, v71, v23
	ds_write_b32 v66, v2 offset:51200
	v_cvt_pk_bf16_f32 v2, v22, v23
	v_mul_f32_e32 v24, v72, v24
	v_mul_f32_e32 v25, v73, v25
	ds_write_b32 v66, v2 offset:53248
	v_cvt_pk_bf16_f32 v2, v24, v25
	v_mul_f32_e32 v26, v74, v26
	v_mul_f32_e32 v27, v75, v27
	ds_write_b32 v66, v2 offset:55296
	v_cvt_pk_bf16_f32 v2, v26, v27
	v_mul_f32_e32 v28, v76, v28
	v_mul_f32_e32 v29, v77, v29
	ds_write_b32 v66, v2 offset:57344
	v_cvt_pk_bf16_f32 v2, v28, v29
	v_mul_f32_e32 v30, v78, v30
	v_mul_f32_e32 v31, v79, v31
	ds_write_b32 v66, v2 offset:59392
	v_cvt_pk_bf16_f32 v2, v30, v31
	v_mov_b32_e32 v5, v0
	v_mul_f32_e32 v32, v80, v32
	v_mul_f32_e32 v33, v81, v33
	ds_write_b32 v66, v2 offset:61440
	v_cvt_pk_bf16_f32 v2, v32, v33
	ds_write_b32 v66, v2 offset:63488
	v_mov_b32_e32 v3, v181
	v_and_b32_e32 v4, 31, v5
	v_lshlrev_b32_e32 v2, 10, v4
	v_lshl_add_u64 v[6:7], s[96:97], 0, v[2:3]
	v_and_b32_e32 v2, 32, v5
	v_lshl_add_u64 v[6:7], v[6:7], 0, v[2:3]
	global_load_dwordx4 v[158:161], v[6:7], off offset:80
	global_load_dwordx4 v[154:157], v[6:7], off offset:64
	s_or_b32 s28, s87, 64
	v_readfirstlane_b32 s80, v5
	s_ashr_i32 s29, s28, 31
	s_ashr_i32 s81, s80, 6
	v_lshlrev_b32_e32 v3, 8, v5
	s_cmp_gt_i32 s81, 3
	v_and_b32_e32 v191, 0x3c00, v3
	v_lshlrev_b32_e32 v3, 4, v5
	s_cselect_b64 s[6:7], -1, 0
	s_and_b32 s95, s81, 3
	v_bitop3_b32 v192, v3, 48, v5 bitop3:0x48
	v_mov_b32_e32 v3, s80
	s_lshl_b32 s79, s95, 14
	v_bfi_b32 v3, s21, v3, v5
	v_or3_b32 v180, s79, v191, v192
	v_lshlrev_b32_e32 v182, 4, v3
	s_and_b64 vcc, exec, s[6:7]
	s_cbranch_vccnz .LBB0_1319
	s_ashr_i32 s89, s88, 31
	s_lshl_b64 s[38:39], s[88:89], 10
	s_add_u32 s38, s16, s38
	s_addc_u32 s39, s17, s39
	s_lshl_b32 s37, s95, 10
	s_cmp_lg_u32 0, -1
	v_lshl_add_u64 v[6:7], s[38:39], 0, v[180:181]
	s_cselect_b32 s38, 0, 0
	s_add_i32 s37, s38, s37
	v_lshl_add_u64 v[6:7], v[6:7], 0, s[28:29]
	s_mov_b32 m0, s37
	v_mov_b32_e32 v183, v181
	s_lshl_b32 s39, s81, 10
	global_load_lds_dwordx4 v[6:7], off
	v_lshl_add_u64 v[6:7], s[90:91], 0, v[182:183]
	s_add_i32 s40, s38, s39
	s_mov_b64 s[38:39], 0x1000
	v_lshl_add_u64 v[8:9], v[6:7], 0, s[38:39]
	s_or_b32 s38, s88, 64
	s_add_i32 m0, s40, 0x4000
	s_ashr_i32 s39, s38, 31
	global_load_lds_dwordx4 v182, s[90:91]
	s_add_i32 m0, s40, 0x5000
	s_lshl_b64 s[38:39], s[38:39], 10
	s_add_u32 s38, s16, s38
	s_addc_u32 s39, s17, s39
	global_load_lds_dwordx4 v[8:9], off
	v_lshl_add_u64 v[8:9], s[38:39], 0, v[180:181]
	s_or_b32 s38, s88, 0x80
	s_ashr_i32 s39, s38, 31
	s_add_i32 m0, s37, 0x1000
	s_lshl_b64 s[38:39], s[38:39], 10
	s_add_u32 s38, s16, s38
	v_lshl_add_u64 v[8:9], v[8:9], 0, s[28:29]
	s_addc_u32 s39, s17, s39
	global_load_lds_dwordx4 v[8:9], off
	v_lshl_add_u64 v[8:9], s[38:39], 0, v[180:181]
	v_lshl_add_u64 v[8:9], v[8:9], 0, s[28:29]
	s_add_i32 m0, s37, 0x2000
	s_mov_b64 s[38:39], 0x2000
	global_load_lds_dwordx4 v[8:9], off
	v_lshl_add_u64 v[8:9], v[6:7], 0, s[38:39]
	s_add_i32 m0, s40, 0x6000
	s_mov_b64 s[38:39], 0x3000
	global_load_lds_dwordx4 v[8:9], off
	v_lshl_add_u64 v[6:7], v[6:7], 0, s[38:39]
	s_add_i32 m0, s40, 0x7000
	s_nop 0
	global_load_lds_dwordx4 v[6:7], off

.LBB0_1323:
	s_and_b32 s37, s80, 0xffffffc0
	v_lshlrev_b32_e32 v6, 2, v5
	v_lshlrev_b32_e32 v3, 6, v4
	v_and_b32_e32 v6, 48, v6
	s_cmp_lg_u32 0, -1
	v_bitop3_b32 v194, v6, v3, v2 bitop3:0xde
	s_cselect_b32 s38, 0, 0
	v_lshlrev_b32_e32 v2, 3, v5
	v_and_b32_e32 v193, 63, v5
	v_add_u32_e32 v183, s38, v194
	s_addk_i32 s38, 0x4000
	v_and_b32_e32 v2, 32, v2
	s_lshl_b32 s37, s37, 2
	v_add_u32_e32 v188, s38, v194
	v_sub_u32_e32 v195, 16, v2
	v_lshrrev_b32_e32 v2, 5, v193
	s_add_i32 s78, s37, 0
	v_add_u32_e32 v190, v183, v195
	s_mov_b64 s[38:39], -1
	s_and_b64 vcc, exec, s[6:7]
	v_add_u32_e32 v189, v188, v195
	v_cmp_gt_u32_e64 s[6:7], 32, v193
	v_lshlrev_b32_e32 v186, 4, v2
	v_lshl_add_u32 v187, v4, 2, s78
	v_and_b32_e32 v248, 31, v193
	v_mov_b32_e32 v249, 0x38383838
	v_cmp_eq_u32_e64 s[100:101], 0, v248
	v_lshrrev_b32_e32 v250, 4, v193
	s_nop 0
	v_cndmask_b32_e64 v146, 0, v249, s[100:101]
	v_cmp_eq_u32_e64 s[100:101], 17, v248
	v_and_b32_e32 v248, 15, v193
	v_lshlrev_b32_e32 v248, 6, v248
	v_cndmask_b32_e64 v146, v146, v249, s[100:101]
	v_lshl_add_u32 v250, v250, 4, v248
	v_add_u32_e32 v250, s78, v250
	v_mov_b32_e32 v147, v146
	v_mov_b32_e32 v148, v146
	v_mov_b32_e32 v149, v146
	v_mov_b32_e32 v150, v146
	v_mov_b32_e32 v151, v146
	v_mov_b32_e32 v152, v146
	v_mov_b32_e32 v153, v146
	s_cbranch_vccz .LBB0_1376
	ds_read_b128 v[18:21], v183 offset:0
	ds_read_b128 v[22:25], v190 offset:0
	ds_read_b128 v[34:37], v183 offset:0x800
	ds_read_b128 v[38:41], v190 offset:0x800
	s_waitcnt lgkmcnt(0)
	s_waitcnt vmcnt(0)
	v_mfma_f32_32x32x64_f8f6f4 v[18:33], v[18:25], v[154:161], 0
	s_mov_b32 s37, s36
	s_mov_b32 s38, s36
	s_mov_b32 s39, s36
	s_mov_b32 s40, s36
	s_mov_b32 s41, s36
	s_mov_b32 s42, s36
	s_mov_b32 s43, s36
	s_mov_b32 s44, s36
	s_mov_b32 s45, s36
	s_mov_b32 s46, s36
	s_mov_b32 s47, s36
	s_mov_b32 s48, s36
	s_mov_b32 s49, s36
	s_mov_b32 s50, s36
	s_mov_b32 s51, s36
	v_mov_b64_e32 v[2:3], s[36:37]
	v_mov_b64_e32 v[4:5], s[38:39]
	v_mov_b64_e32 v[6:7], s[40:41]
	v_mov_b64_e32 v[8:9], s[42:43]
	v_mov_b64_e32 v[10:11], s[44:45]
	v_mov_b64_e32 v[12:13], s[46:47]
	v_mov_b64_e32 v[14:15], s[48:49]
	v_mov_b64_e32 v[16:17], s[50:51]
	v_max_f32_e32 v42, v19, v19
	v_max_f32_e32 v43, v18, v18
	v_max_f32_e32 v42, v43, v42
	v_max3_f32 v42, v42, v20, v21
	v_max3_f32 v42, v42, v22, v23
	v_max3_f32 v42, v42, v24, v25
	v_max3_f32 v42, v42, v26, v27
	v_max3_f32 v42, v42, v28, v29
	v_max3_f32 v50, v42, v30, v31
	v_mfma_f32_32x32x64_f8f6f4 v[34:49], v[34:41], v[154:161], 0
	v_max3_f32 v50, v50, v32, v33
	s_cmp_lg_u32 0, -1
	s_cselect_b32 s37, 0, 0
	v_mov_b32_e32 v130, v181
	v_mov_b32_e32 v131, v181
	s_add_i32 s38, s37, 0x1000
	s_waitcnt vmcnt(0) lgkmcnt(0)
	s_barrier
	v_add_u32_e32 v207, s38, v194
	v_add_u32_e32 v209, v207, v195
	s_nop 11
	v_max3_f32 v50, v50, v34, v35
	v_max3_f32 v50, v50, v36, v37
	v_max3_f32 v50, v50, v38, v39
	v_max3_f32 v50, v50, v40, v41
	v_max3_f32 v50, v50, v42, v43
	v_max3_f32 v50, v50, v44, v45
	v_max3_f32 v50, v50, v46, v47
	v_max3_f32 v50, v50, v48, v49
	v_mov_b32_e32 v51, v50
	s_nop 1
	v_permlane32_swap_b32_e32 v50, v51
	v_max_f32_e32 v51, v51, v51
	v_max_f32_e32 v50, v50, v50
	v_max_f32_e32 v50, v50, v51
	s_cmp_eq_u32 s98, 0
	s_cselect_b32 s100, 0x3f800000, 0xc0600000
	v_add_f32_e32 v198, s100, v50
	v_sub_f32_e32 v18, v18, v198
	v_sub_f32_e32 v19, v19, v198
	v_sub_f32_e32 v22, v22, v198
	v_sub_f32_e32 v23, v23, v198
	v_exp_f32_e32 v50, v18
	v_exp_f32_e32 v51, v19
	v_exp_f32_e32 v54, v22
	v_exp_f32_e32 v55, v23
	v_xor_b32_e32 v82, 0x80000000, v198
	v_sub_f32_e32 v20, v20, v198
	v_sub_f32_e32 v21, v21, v198
	v_sub_f32_e32 v24, v24, v198
	v_sub_f32_e32 v25, v25, v198
	v_mov_b32_e32 v83, v82
	v_mov_b32_e32 v84, v82
	v_mov_b32_e32 v85, v82
	v_mov_b32_e32 v86, v82
	v_mov_b32_e32 v87, v82
	v_mov_b32_e32 v88, v82
	v_mov_b32_e32 v89, v82
	v_mov_b32_e32 v90, v82
	v_mov_b32_e32 v91, v82
	v_mov_b32_e32 v92, v82
	v_mov_b32_e32 v93, v82
	v_mov_b32_e32 v94, v82
	v_mov_b32_e32 v95, v82
	v_mov_b32_e32 v96, v82
	v_mov_b32_e32 v97, v82
	v_exp_f32_e32 v52, v20
	v_exp_f32_e32 v53, v21
	v_exp_f32_e32 v56, v24
	v_exp_f32_e32 v57, v25
	v_cvt_pk_fp8_f32 v130, v50, v51
	v_cvt_pk_fp8_f32 v131, v54, v55
	ds_read_b128 v[18:21], v207 offset:0
	v_sub_f32_e32 v26, v26, v198
	v_sub_f32_e32 v27, v27, v198
	v_sub_f32_e32 v28, v28, v198
	v_sub_f32_e32 v29, v29, v198
	ds_read_b128 v[22:25], v209 offset:0
	v_sub_f32_e32 v34, v34, v198
	v_sub_f32_e32 v35, v35, v198
	v_sub_f32_e32 v36, v36, v198
	v_sub_f32_e32 v37, v37, v198
	v_sub_f32_e32 v38, v38, v198
	v_sub_f32_e32 v39, v39, v198
	v_sub_f32_e32 v40, v40, v198
	v_sub_f32_e32 v41, v41, v198
	v_sub_f32_e32 v42, v42, v198
	v_sub_f32_e32 v43, v43, v198
	v_sub_f32_e32 v44, v44, v198
	v_sub_f32_e32 v45, v45, v198
	v_sub_f32_e32 v30, v30, v198
	v_sub_f32_e32 v46, v46, v198
	v_sub_f32_e32 v31, v31, v198
	v_sub_f32_e32 v47, v47, v198
	v_sub_f32_e32 v32, v32, v198
	v_sub_f32_e32 v48, v48, v198
	v_sub_f32_e32 v33, v33, v198
	v_sub_f32_e32 v49, v49, v198
	v_exp_f32_e32 v58, v26
	v_exp_f32_e32 v59, v27
	v_exp_f32_e32 v60, v28
	v_exp_f32_e32 v61, v29
	ds_read_b128 v[26:29], v207 offset:0x800
	v_exp_f32_e32 v34, v34
	v_exp_f32_e32 v35, v35
	v_exp_f32_e32 v36, v36
	v_exp_f32_e32 v37, v37
	v_exp_f32_e32 v38, v38
	v_exp_f32_e32 v39, v39
	v_exp_f32_e32 v40, v40
	v_exp_f32_e32 v41, v41
	v_exp_f32_e32 v42, v42
	v_exp_f32_e32 v43, v43
	v_exp_f32_e32 v44, v44
	v_exp_f32_e32 v45, v45
	v_exp_f32_e32 v62, v30
	v_exp_f32_e32 v46, v46
	v_exp_f32_e32 v63, v31
	v_exp_f32_e32 v47, v47
	v_exp_f32_e32 v64, v32
	v_exp_f32_e32 v48, v48
	v_exp_f32_e32 v65, v33
	v_exp_f32_e32 v49, v49
	ds_read_b128 v[30:33], v209 offset:0x800
	v_cvt_pk_fp8_f32 v130, v52, v53 op_sel:[0,0,1]
	v_cvt_pk_fp8_f32 v131, v56, v57 op_sel:[0,0,1]
	s_waitcnt lgkmcnt(2)
	v_mfma_f32_32x32x64_f8f6f4 v[98:113], v[18:25], v[154:161], v[82:97]
	v_mov_b32_e32 v132, v181
	v_mov_b32_e32 v133, v181
	v_cvt_pk_fp8_f32 v132, v58, v59
	v_cvt_pk_fp8_f32 v133, v62, v63
	ds_read_b128 v[170:173], v188 offset:0
	ds_read_b128 v[174:177], v189 offset:0
	v_cvt_pk_fp8_f32 v132, v60, v61 op_sel:[0,0,1]
	v_cvt_pk_fp8_f32 v133, v64, v65 op_sel:[0,0,1]
	s_waitcnt lgkmcnt(2)
	v_mov_b64_e32 v[128:129], v[96:97]
	v_mov_b64_e32 v[126:127], v[94:95]
	v_mov_b64_e32 v[124:125], v[92:93]
	v_mov_b64_e32 v[122:123], v[90:91]
	v_mov_b64_e32 v[120:121], v[88:89]
	v_mov_b64_e32 v[118:119], v[86:87]
	v_mov_b64_e32 v[116:117], v[84:85]
	v_mov_b64_e32 v[114:115], v[82:83]
	v_mov_b32_e32 v134, v181
	v_mov_b32_e32 v135, v181
	v_mfma_f32_32x32x64_f8f6f4 v[114:129], v[26:33], v[154:161], v[114:129]
	v_mov_b32_e32 v136, v181
	v_mov_b32_e32 v137, v181
	v_cvt_pk_fp8_f32 v134, v34, v35
	v_cvt_pk_fp8_f32 v135, v38, v39
	v_cvt_pk_fp8_f32 v136, v42, v43
	v_cvt_pk_fp8_f32 v137, v46, v47
	v_cvt_pk_fp8_f32 v134, v36, v37 op_sel:[0,0,1]
	v_cvt_pk_fp8_f32 v135, v40, v41 op_sel:[0,0,1]
	v_cvt_pk_fp8_f32 v136, v44, v45 op_sel:[0,0,1]
	v_cvt_pk_fp8_f32 v137, v48, v49 op_sel:[0,0,1]
	s_nop 0
	ds_read_b128 v[138:141], v188 offset:0x800
	ds_read_b128 v[142:145], v189 offset:0x800
	s_nop 0
	v_mfma_f32_16x16x128_f8f6f4 v[18:21], v[130:137], v[146:153], 0
	s_add_i32 s38, s37, 0x2000
	v_add_u32_e32 v205, s38, v194
	s_add_i32 s38, s37, 0x6000
	v_add_u32_e32 v203, s38, v194
	s_add_i32 s38, s37, 0x3000
	s_waitcnt vmcnt(0) lgkmcnt(0)
	s_barrier
	v_add_u32_e32 v201, s38, v194
	s_add_i32 s38, s37, 0x8000
	s_add_i32 s37, s37, 0xa000
	v_add_u32_e32 v199, s38, v194
	v_add_u32_e32 v196, s37, v194
	v_mov_b64_e32 v[48:49], v[16:17]
	v_mov_b64_e32 v[64:65], v[16:17]
	v_mov_b64_e32 v[80:81], v[16:17]
	v_add_u32_e32 v206, v205, v195
	v_add_u32_e32 v204, v203, v195
	v_add_u32_e32 v202, v201, v195
	v_add_u32_e32 v200, v199, v195
	v_add_u32_e32 v197, v196, v195
	s_mov_b32 s37, -2
	v_mov_b64_e32 v[46:47], v[14:15]
	v_mov_b64_e32 v[44:45], v[12:13]
	v_mov_b64_e32 v[42:43], v[10:11]
	v_mov_b64_e32 v[40:41], v[8:9]
	v_mov_b64_e32 v[38:39], v[6:7]
	v_mov_b64_e32 v[36:37], v[4:5]
	v_mov_b64_e32 v[34:35], v[2:3]
	v_mov_b64_e32 v[62:63], v[14:15]
	v_mov_b64_e32 v[60:61], v[12:13]
	v_mov_b64_e32 v[58:59], v[10:11]
	v_mov_b64_e32 v[56:57], v[8:9]
	v_mov_b64_e32 v[54:55], v[6:7]
	v_mov_b64_e32 v[52:53], v[4:5]
	v_mov_b64_e32 v[50:51], v[2:3]
	v_mov_b64_e32 v[78:79], v[14:15]
	v_mov_b64_e32 v[76:77], v[12:13]
	v_mov_b64_e32 v[74:75], v[10:11]
	v_mov_b64_e32 v[72:73], v[8:9]
	v_mov_b64_e32 v[70:71], v[6:7]
	v_mov_b64_e32 v[68:69], v[4:5]
	v_mov_b64_e32 v[66:67], v[2:3]
	s_branch .LBB0_1327

.LBB0_1376:
	s_and_b64 vcc, exec, s[38:39]
	s_cbranch_vccz .LBB0_1202
	ds_read_b128 v[18:21], v183 offset:0
	ds_read_b128 v[22:25], v190 offset:0
	ds_read_b128 v[34:37], v183 offset:0x800
	ds_read_b128 v[38:41], v190 offset:0x800
	s_waitcnt lgkmcnt(0)
	s_waitcnt vmcnt(0)
	s_nop 11
	v_mfma_f32_32x32x64_f8f6f4 v[18:33], v[18:25], v[154:161], 0
	s_mov_b32 s37, s36
	s_mov_b32 s38, s36
	s_mov_b32 s39, s36
	s_mov_b32 s40, s36
	s_mov_b32 s41, s36
	s_mov_b32 s42, s36
	s_mov_b32 s43, s36
	s_mov_b32 s44, s36
	s_mov_b32 s45, s36
	s_mov_b32 s46, s36
	s_mov_b32 s47, s36
	s_mov_b32 s48, s36
	s_mov_b32 s49, s36
	s_mov_b32 s50, s36
	s_mov_b32 s51, s36
	v_mov_b64_e32 v[2:3], s[36:37]
	v_mov_b64_e32 v[4:5], s[38:39]
	v_mov_b64_e32 v[6:7], s[40:41]
	v_mov_b64_e32 v[8:9], s[42:43]
	v_mov_b64_e32 v[10:11], s[44:45]
	v_mov_b64_e32 v[12:13], s[46:47]
	v_mov_b64_e32 v[14:15], s[48:49]
	v_mov_b64_e32 v[16:17], s[50:51]
	v_max_f32_e32 v42, v19, v19
	v_max_f32_e32 v43, v18, v18
	v_max_f32_e32 v42, v43, v42
	v_max3_f32 v42, v42, v20, v21
	v_max3_f32 v42, v42, v22, v23
	v_max3_f32 v42, v42, v24, v25
	v_max3_f32 v42, v42, v26, v27
	v_max3_f32 v42, v42, v28, v29
	v_max3_f32 v50, v42, v30, v31
	v_mfma_f32_32x32x64_f8f6f4 v[34:49], v[34:41], v[154:161], 0
	v_max3_f32 v50, v50, v32, v33
	s_lshl_b32 s45, s95, 10
	s_lshl_b32 s46, s81, 10
	s_cmp_lg_u32 0, -1
	s_cselect_b32 s38, 0, 0
	s_add_i32 s37, s38, 0x2000
	s_add_i32 s39, s38, 0x3000
	s_add_i32 s6, s38, 0x1000
	v_add_u32_e32 v203, s37, v194
	s_add_i32 s37, s38, 0x6000
	v_add_u32_e32 v199, s39, v194
	s_add_i32 s39, s38, 0x8000
	s_add_i32 s38, s38, 0xa000
	v_add_u32_e32 v205, s6, v194
	v_add_u32_e32 v201, s37, v194
	s_nop 4
	v_max3_f32 v50, v50, v34, v35
	v_max3_f32 v50, v50, v36, v37
	v_max3_f32 v50, v50, v38, v39
	v_max3_f32 v50, v50, v40, v41
	v_max3_f32 v50, v50, v42, v43
	v_max3_f32 v50, v50, v44, v45
	v_max3_f32 v50, v50, v46, v47
	v_max3_f32 v50, v50, v48, v49
	v_mov_b32_e32 v51, v50
	s_nop 1
	v_permlane32_swap_b32_e32 v50, v51
	v_max_f32_e32 v51, v51, v51
	v_max_f32_e32 v50, v50, v50
	v_max_f32_e32 v50, v50, v51
	s_cmp_eq_u32 s98, 0
	s_cselect_b32 s100, 0x3f800000, 0xc0600000
	v_add_f32_e32 v198, s100, v50
	v_sub_f32_e32 v18, v18, v198
	v_sub_f32_e32 v19, v19, v198
	v_add_u32_e32 v196, s39, v194
	v_add_u32_e32 v194, s38, v194
	s_lshl_b32 s38, s80, 4
	v_exp_f32_e32 v114, v18
	v_exp_f32_e32 v115, v19
	v_lshl_add_u64 v[18:19], s[16:17], 0, v[180:181]
	s_and_b32 s38, s38, 0xfffffc00
	s_ashr_i32 s89, s88, 31
	s_or_b32 s40, s88, 0x100
	s_add_i32 s41, s94, 0x4100
	s_or_b32 s42, s88, 0x140
	s_add_i32 s43, s94, 0x4140
	v_lshl_add_u64 v[170:171], v[18:19], 0, s[28:29]
	v_lshl_or_b32 v18, v193, 4, s38
	s_lshl_b64 s[38:39], s[88:89], 10
	s_add_u32 s38, s38, s87
	v_xor_b32_e32 v82, 0x80000000, v198
	v_sub_f32_e32 v34, v34, v198
	v_sub_f32_e32 v35, v35, v198
	v_sub_f32_e32 v20, v20, v198
	v_sub_f32_e32 v36, v36, v198
	v_sub_f32_e32 v21, v21, v198
	v_sub_f32_e32 v37, v37, v198
	v_sub_f32_e32 v22, v22, v198
	v_sub_f32_e32 v38, v38, v198
	v_sub_f32_e32 v23, v23, v198
	v_sub_f32_e32 v39, v39, v198
	v_sub_f32_e32 v24, v24, v198
	v_sub_f32_e32 v40, v40, v198
	v_sub_f32_e32 v25, v25, v198
	v_sub_f32_e32 v41, v41, v198
	v_sub_f32_e32 v26, v26, v198
	v_sub_f32_e32 v42, v42, v198
	v_sub_f32_e32 v27, v27, v198
	v_sub_f32_e32 v43, v43, v198
	v_sub_f32_e32 v28, v28, v198
	v_sub_f32_e32 v44, v44, v198
	v_sub_f32_e32 v29, v29, v198
	v_sub_f32_e32 v45, v45, v198
	v_sub_f32_e32 v30, v30, v198
	v_sub_f32_e32 v46, v46, v198
	v_sub_f32_e32 v31, v31, v198
	v_sub_f32_e32 v47, v47, v198
	v_sub_f32_e32 v32, v32, v198
	v_sub_f32_e32 v48, v48, v198
	v_sub_f32_e32 v33, v33, v198
	v_sub_f32_e32 v49, v49, v198
	s_addc_u32 s39, s39, s76
	v_mov_b32_e32 v83, v82
	v_mov_b32_e32 v84, v82
	v_mov_b32_e32 v85, v82
	v_mov_b32_e32 v86, v82
	v_mov_b32_e32 v87, v82
	v_mov_b32_e32 v88, v82
	v_mov_b32_e32 v89, v82
	v_mov_b32_e32 v90, v82
	v_mov_b32_e32 v91, v82
	v_mov_b32_e32 v92, v82
	v_mov_b32_e32 v93, v82
	v_mov_b32_e32 v94, v82
	v_mov_b32_e32 v95, v82
	v_mov_b32_e32 v96, v82
	v_mov_b32_e32 v97, v82
	v_exp_f32_e32 v98, v34
	v_exp_f32_e32 v99, v35
	v_exp_f32_e32 v116, v20
	v_exp_f32_e32 v100, v36
	v_exp_f32_e32 v117, v21
	v_exp_f32_e32 v101, v37
	v_exp_f32_e32 v118, v22
	v_exp_f32_e32 v102, v38
	v_exp_f32_e32 v119, v23
	v_exp_f32_e32 v103, v39
	v_exp_f32_e32 v120, v24
	v_exp_f32_e32 v104, v40
	v_exp_f32_e32 v121, v25
	v_exp_f32_e32 v105, v41
	v_exp_f32_e32 v122, v26
	v_exp_f32_e32 v106, v42
	v_exp_f32_e32 v123, v27
	v_exp_f32_e32 v107, v43
	v_exp_f32_e32 v124, v28
	v_exp_f32_e32 v108, v44
	v_exp_f32_e32 v125, v29
	v_exp_f32_e32 v109, v45
	v_exp_f32_e32 v126, v30
	v_exp_f32_e32 v110, v46
	v_exp_f32_e32 v127, v31
	v_exp_f32_e32 v111, v47
	v_exp_f32_e32 v128, v32
	v_exp_f32_e32 v112, v48
	v_exp_f32_e32 v129, v33
	v_exp_f32_e32 v113, v49
	v_mov_b32_e32 v19, v181
	s_add_u32 s38, s38, 0x29c30040
	s_waitcnt vmcnt(3) lgkmcnt(0)
	s_barrier
	v_lshl_add_u64 v[172:173], s[92:93], 0, v[18:19]
	s_addc_u32 s39, s39, 0
	v_add3_u32 v18, s79, v191, v192
	v_lshl_add_u64 v[174:175], s[38:39], 0, v[18:19]
	v_mov_b32_e32 v162, 0
	v_mov_b64_e32 v[48:49], v[16:17]
	v_mov_b64_e32 v[64:65], v[16:17]
	v_mov_b64_e32 v[80:81], v[16:17]
	v_mov_b64_e32 v[32:33], v[16:17]
	v_add_u32_e32 v206, v205, v195
	v_cmp_gt_u32_e64 s[6:7], 32, v193
	v_add_u32_e32 v204, v203, v195
	v_add_u32_e32 v202, v201, v195
	s_movk_i32 s37, 0x100
	v_add_u32_e32 v200, v199, v195
	v_add_u32_e32 v197, v196, v195
	v_add_u32_e32 v195, v194, v195
	s_mov_b32 s44, -3
	s_add_i32 s45, s45, 0
	s_add_i32 s46, s46, 0
	v_mov_b64_e32 v[46:47], v[14:15]
	v_mov_b64_e32 v[44:45], v[12:13]
	v_mov_b64_e32 v[42:43], v[10:11]
	v_mov_b64_e32 v[40:41], v[8:9]
	v_mov_b64_e32 v[38:39], v[6:7]
	v_mov_b64_e32 v[36:37], v[4:5]
	v_mov_b64_e32 v[34:35], v[2:3]
	v_mov_b64_e32 v[62:63], v[14:15]
	v_mov_b64_e32 v[60:61], v[12:13]
	v_mov_b64_e32 v[58:59], v[10:11]
	v_mov_b64_e32 v[56:57], v[8:9]
	v_mov_b64_e32 v[54:55], v[6:7]
	v_mov_b64_e32 v[52:53], v[4:5]
	v_mov_b64_e32 v[50:51], v[2:3]
	v_mov_b64_e32 v[78:79], v[14:15]
	v_mov_b64_e32 v[76:77], v[12:13]
	v_mov_b64_e32 v[74:75], v[10:11]
	v_mov_b64_e32 v[72:73], v[8:9]
	v_mov_b64_e32 v[70:71], v[6:7]
	v_mov_b64_e32 v[68:69], v[4:5]
	v_mov_b64_e32 v[66:67], v[2:3]
	v_mov_b64_e32 v[30:31], v[14:15]
	v_mov_b64_e32 v[28:29], v[12:13]
	v_mov_b64_e32 v[26:27], v[10:11]
	v_mov_b64_e32 v[24:25], v[8:9]
	v_mov_b64_e32 v[22:23], v[6:7]
	v_mov_b64_e32 v[20:21], v[4:5]
	v_mov_b64_e32 v[18:19], v[2:3]
	v_mov_b32_e32 v163, v162
	v_mov_b32_e32 v164, v162
	v_mov_b32_e32 v165, v162
	v_mov_b32_e32 v166, v162
	v_mov_b32_e32 v167, v162
	v_mov_b32_e32 v168, v162
	v_mov_b32_e32 v169, v162
	s_branch .LBB0_1380

.LBB0_1407:
	s_ashr_i32 s95, s94, 31
	s_lshl_b64 s[38:39], s[94:95], 10
	s_add_u32 s38, s16, s38
	s_addc_u32 s39, s17, s39
	v_lshl_add_u64 v[130:131], s[38:39], 0, v[180:181]
	v_mov_b32_e32 v183, v181
	v_lshl_add_u64 v[130:131], v[130:131], 0, s[28:29]
	s_mov_b64 s[28:29], 0x2030000
	s_mov_b32 m0, s49
	v_lshl_add_u64 v[130:131], v[130:131], 0, s[28:29]
	v_lshl_add_u64 v[170:171], s[90:91], 0, v[182:183]
	s_mov_b64 s[28:29], 0x204000
	global_load_lds_dwordx4 v[130:131], off
	v_lshl_add_u64 v[130:131], v[170:171], 0, s[28:29]
	s_mov_b32 m0, s47
	s_mov_b64 s[28:29], 0x205000
	global_load_lds_dwordx4 v[130:131], off
	v_lshl_add_u64 v[130:131], v[170:171], 0, s[28:29]
	s_mov_b32 m0, s48
	v_cvt_pk_fp8_f32 v162, v114, v115
	global_load_lds_dwordx4 v[130:131], off
	v_cvt_pk_fp8_f32 v163, v118, v119
	ds_read_b128 v[130:133], v205 offset:0
	ds_read_b128 v[134:137], v206 offset:0
	ds_read_b128 v[210:213], v205 offset:0x800
	ds_read_b128 v[214:217], v206 offset:0x800
	v_cvt_pk_fp8_f32 v162, v116, v117 op_sel:[0,0,1]
	v_cvt_pk_fp8_f32 v163, v120, v121 op_sel:[0,0,1]
	s_waitcnt lgkmcnt(2)
	v_cvt_pk_fp8_f32 v164, v122, v123
	v_cvt_pk_fp8_f32 v165, v126, v127
	ds_read_b128 v[218:221], v188 offset:0
	ds_read_b128 v[222:225], v189 offset:0
	v_cvt_pk_fp8_f32 v164, v124, v125 op_sel:[0,0,1]
	v_cvt_pk_fp8_f32 v165, v128, v129 op_sel:[0,0,1]
	v_mfma_f32_32x32x64_f8f6f4 v[114:129], v[130:137], v[154:161], v[82:97]
	s_waitcnt lgkmcnt(2)
	v_mfma_f32_32x32x64_f8f6f4 v[130:145], v[210:217], v[154:161], v[82:97]
	v_cvt_pk_fp8_f32 v166, v98, v99
	v_cvt_pk_fp8_f32 v167, v102, v103
	v_cvt_pk_fp8_f32 v168, v106, v107
	v_cvt_pk_fp8_f32 v169, v110, v111
	v_cvt_pk_fp8_f32 v166, v100, v101 op_sel:[0,0,1]
	v_cvt_pk_fp8_f32 v167, v104, v105 op_sel:[0,0,1]
	v_cvt_pk_fp8_f32 v168, v108, v109 op_sel:[0,0,1]
	v_cvt_pk_fp8_f32 v169, v112, v113 op_sel:[0,0,1]
	s_nop 0
	ds_read_b128 v[106:109], v188 offset:0x800
	ds_read_b128 v[110:113], v189 offset:0x800
	s_nop 0
	v_mfma_f32_16x16x128_f8f6f4 v[18:21], v[162:169], v[146:153], v[18:21]
	s_waitcnt lgkmcnt(2)
	v_mfma_f32_32x32x64_f8f6f4 v[2:17], v[162:169], v[218:225], v[2:17]
	ds_read_b128 v[98:101], v188 offset:0x1000
	ds_read_b128 v[102:105], v189 offset:0x1000
	s_mov_b64 s[28:29], 0
	s_cmp_eq_u32 s98, 0
	s_cbranch_scc1 .LBB0_1410
	v_max3_f32 v172, v114, v115, v116
	v_max3_f32 v172, v172, v117, v118
	v_max3_f32 v172, v172, v119, v120
	v_max3_f32 v172, v172, v121, v122
	v_max3_f32 v172, v172, v123, v124
	v_max3_f32 v172, v172, v125, v126
	v_max3_f32 v172, v172, v127, v128
	v_max_f32 v172, v172, v129
	s_nop 0
	v_max3_f32 v172, v172, v130, v131
	v_max3_f32 v172, v172, v132, v133
	v_max3_f32 v172, v172, v134, v135
	v_max3_f32 v172, v172, v136, v137
	v_max3_f32 v172, v172, v138, v139
	v_max3_f32 v172, v172, v140, v141
	v_max3_f32 v172, v172, v142, v143
	v_max3_f32 v172, v172, v144, v145
	v_mov_b32 v173, v172
	s_nop 1
	v_permlane32_swap_b32 v172, v173
	v_max_f32 v172, v172, v173
	s_nop 0
	v_cmp_ge_f32_e32 vcc, s54, v172
	s_cmp_lg_u64 vcc, exec
	s_cselect_b64 s[28:29], -1, 0
	s_cmp_eq_u64 vcc, exec
	s_cbranch_scc1 .LBB0_1409
	v_add_f32_e32 v82, 0xc0c00000, v172
	v_max_f32_e32 v82, 0, v82
	v_exp_f32_e64 v172, -v82
	v_add_f32_e32 v198, v198, v82
	v_sub_f32_e32 v114, v114, v82
	v_sub_f32_e32 v130, v130, v82
	v_sub_f32_e32 v115, v115, v82
	v_sub_f32_e32 v131, v131, v82
	v_sub_f32_e32 v116, v116, v82
	v_sub_f32_e32 v132, v132, v82
	v_sub_f32_e32 v117, v117, v82
	v_sub_f32_e32 v133, v133, v82
	v_sub_f32_e32 v118, v118, v82
	v_sub_f32_e32 v134, v134, v82
	v_sub_f32_e32 v119, v119, v82
	v_sub_f32_e32 v135, v135, v82
	v_sub_f32_e32 v120, v120, v82
	v_sub_f32_e32 v136, v136, v82
	v_sub_f32_e32 v121, v121, v82
	v_sub_f32_e32 v137, v137, v82
	v_sub_f32_e32 v122, v122, v82
	v_sub_f32_e32 v138, v138, v82
	v_sub_f32_e32 v123, v123, v82
	v_sub_f32_e32 v139, v139, v82
	v_sub_f32_e32 v124, v124, v82
	v_sub_f32_e32 v140, v140, v82
	v_sub_f32_e32 v125, v125, v82
	v_sub_f32_e32 v141, v141, v82
	v_sub_f32_e32 v126, v126, v82
	v_sub_f32_e32 v142, v142, v82
	v_sub_f32_e32 v127, v127, v82
	v_sub_f32_e32 v143, v143, v82
	v_sub_f32_e32 v128, v128, v82
	v_sub_f32_e32 v144, v144, v82
	v_sub_f32_e32 v129, v129, v82
	v_sub_f32_e32 v145, v145, v82
	v_xor_b32_e32 v82, 0x80000000, v198
	v_mov_b32_e32 v83, v82
	v_mov_b32_e32 v84, v82
	v_mov_b32_e32 v85, v82
	v_mov_b32_e32 v86, v82
	v_mov_b32_e32 v87, v82
	v_mov_b32_e32 v88, v82
	v_mov_b32_e32 v89, v82
	v_mov_b32_e32 v90, v82
	v_mov_b32_e32 v91, v82
	v_mov_b32_e32 v92, v82
	v_mov_b32_e32 v93, v82
	v_mov_b32_e32 v94, v82
	v_mov_b32_e32 v95, v82
	v_mov_b32_e32 v96, v82
	v_mov_b32_e32 v97, v82
	s_branch .LBB0_1410
